# indexer scoring loops: f32 relu+fmac head-sum, ping-pong accumulators; emission constants computed at selection head instead of hoisted
# baseline (speedup 1.0000x reference)
.LBB0_1251:
	s_andn2_b64 vcc, exec, s[24:25]
	s_cbranch_vccnz .LBB0_1151
	s_cmpk_gt_i32 s13, 0xff
	s_mov_b64 s[2:3], -1
	s_cbranch_scc0 .LBB0_1852
	s_cmp_gt_i32 s14, 4
	s_cselect_b64 s[28:29], -1, 0
	s_cmp_gt_i32 s14, 8
	s_cselect_b64 s[26:27], -1, 0
	s_cmp_gt_i32 s14, 12
	s_cselect_b64 s[2:3], -1, 0
	s_waitcnt vmcnt(0)
	v_or_b32_e32 v120, 1, v119
	v_or_b32_e32 v121, 2, v119
	v_or_b32_e32 v122, 3, v119
	v_or_b32_e32 v123, 4, v119
	v_or_b32_e32 v124, 5, v119
	v_or_b32_e32 v125, 6, v119
	v_or_b32_e32 v126, 7, v119
	v_or_b32_e32 v152, 0x801, v119
	v_or_b32_e32 v153, 0x802, v119
	v_or_b32_e32 v154, 0x803, v119
	v_or_b32_e32 v155, 0x804, v119
	v_or_b32_e32 v156, 0x805, v119
	v_or_b32_e32 v157, 0x806, v119
	v_or_b32_e32 v158, 0x807, v119
	v_or_b32_e32 v159, 0xa00, v119
	v_or_b32_e32 v160, 0xa01, v119
	v_or_b32_e32 v161, 0xa02, v119
	v_or_b32_e32 v162, 0xa03, v119
	v_or_b32_e32 v163, 0xa04, v119
	v_or_b32_e32 v164, 0xa05, v119
	v_or_b32_e32 v165, 0xa06, v119
	v_or_b32_e32 v166, 0xa07, v119
	v_or_b32_e32 v167, 0xc00, v119
	v_or_b32_e32 v168, 0xc01, v119
	v_or_b32_e32 v169, 0xc02, v119
	v_or_b32_e32 v170, 0xc03, v119
	v_or_b32_e32 v171, 0xc04, v119
	v_or_b32_e32 v172, 0xc05, v119
	v_or_b32_e32 v173, 0xc06, v119
	v_or_b32_e32 v174, 0xc07, v119
	v_or_b32_e32 v175, 0xe00, v119
	v_or_b32_e32 v176, 0xe01, v119
	v_or_b32_e32 v177, 0xe02, v119
	v_or_b32_e32 v178, 0xe03, v119
	v_or_b32_e32 v179, 0xe04, v119
	v_or_b32_e32 v180, 0xe05, v119
	v_or_b32_e32 v181, 0xe06, v119
	v_or_b32_e32 v182, 0xe07, v119
	v_or_b32_e32 v183, 0x1000, v119
	v_or_b32_e32 v184, 0x1001, v119
	v_or_b32_e32 v185, 0x1002, v119
	v_or_b32_e32 v186, 0x1003, v119
	v_or_b32_e32 v187, 0x1004, v119
	v_or_b32_e32 v188, 0x1005, v119
	v_or_b32_e32 v189, 0x1006, v119
	v_or_b32_e32 v190, 0x1007, v119
	v_or_b32_e32 v191, 0x1200, v119
	v_or_b32_e32 v192, 0x1201, v119
	v_or_b32_e32 v193, 0x1202, v119
	v_or_b32_e32 v194, 0x1203, v119
	v_or_b32_e32 v195, 0x1204, v119
	v_or_b32_e32 v196, 0x1205, v119
	v_or_b32_e32 v197, 0x1206, v119
	v_or_b32_e32 v198, 0x1207, v119
	v_or_b32_e32 v199, 0x1400, v119
	v_or_b32_e32 v200, 0x1401, v119
	v_or_b32_e32 v201, 0x1402, v119
	v_or_b32_e32 v202, 0x1403, v119
	v_or_b32_e32 v203, 0x1404, v119
	v_or_b32_e32 v204, 0x1405, v119
	v_or_b32_e32 v205, 0x1406, v119
	v_or_b32_e32 v206, 0x1407, v119
	v_or_b32_e32 v207, 0x1600, v119
	v_or_b32_e32 v208, 0x1601, v119
	v_or_b32_e32 v209, 0x1602, v119
	v_or_b32_e32 v210, 0x1603, v119
	v_or_b32_e32 v211, 0x1604, v119
	v_or_b32_e32 v212, 0x1605, v119
	v_or_b32_e32 v213, 0x1606, v119
	v_or_b32_e32 v214, 0x1607, v119
	v_or_b32_e32 v215, 0x1800, v119
	v_or_b32_e32 v216, 0x1801, v119
	v_or_b32_e32 v217, 0x1802, v119
	v_or_b32_e32 v218, 0x1803, v119
	v_or_b32_e32 v219, 0x1804, v119
	v_or_b32_e32 v220, 0x1805, v119
	v_or_b32_e32 v221, 0x1806, v119
	v_or_b32_e32 v222, 0x1807, v119
	v_or_b32_e32 v223, 0x1a00, v119
	v_or_b32_e32 v224, 0x1a01, v119
	v_or_b32_e32 v225, 0x1a02, v119
	v_or_b32_e32 v226, 0x1a03, v119
	v_or_b32_e32 v227, 0x1a04, v119
	v_or_b32_e32 v228, 0x1a05, v119
	v_or_b32_e32 v229, 0x1a06, v119
	v_or_b32_e32 v230, 0x1a07, v119
	v_or_b32_e32 v231, 0x1c00, v119
	v_or_b32_e32 v232, 0x1c01, v119
	v_or_b32_e32 v233, 0x1c02, v119
	v_or_b32_e32 v234, 0x1c03, v119
	v_or_b32_e32 v235, 0x1c04, v119
	v_or_b32_e32 v236, 0x1c05, v119
	v_or_b32_e32 v237, 0x1c06, v119
	v_or_b32_e32 v238, 0x1c07, v119
	v_or_b32_e32 v239, 0x1e00, v119
	v_or_b32_e32 v240, 0x1e01, v119
	v_or_b32_e32 v241, 0x1e02, v119
	v_or_b32_e32 v242, 0x1e03, v119
	v_or_b32_e32 v243, 0x1e04, v119
	v_or_b32_e32 v244, 0x1e05, v119
	v_or_b32_e32 v245, 0x1e06, v119
	v_or_b32_e32 v246, 0x1e07, v119
	v_mov_b32_e32 v67, 15
	v_mov_b32_e32 v66, 0
	s_branch .LBB0_1255

.LBB0_1262:
	s_or_b64 exec, exec, s[34:35]
	s_bcnt1_i32_b64 s4, s[30:31]
	v_cmp_gt_u32_sdwa s[30:31], v50, v66 src0_sel:WORD_1 src1_sel:DWORD
	s_and_saveexec_b64 s[34:35], s[30:31]
	s_cbranch_execz .LBB0_1264
	v_and_b32_e32 v68, s30, v100
	s_lshl_b32 s15, s4, 1
	v_and_b32_e32 v67, s31, v1
	v_bcnt_u32_b32 v68, v68, 0
	s_add_i32 s15, s52, s15
	v_bcnt_u32_b32 v67, v67, v68
	v_lshl_add_u32 v67, v67, 1, s15
	ds_write_b16 v67, v120 offset:32768
.LBB0_1264:
	s_or_b64 exec, exec, s[34:35]
	s_bcnt1_i32_b64 s15, s[30:31]
	s_add_i32 s4, s15, s4
	v_cmp_gt_u32_sdwa s[30:31], v51, v66 src0_sel:WORD_0 src1_sel:DWORD
	s_and_saveexec_b64 s[34:35], s[30:31]
	s_cbranch_execz .LBB0_1266
	v_and_b32_e32 v68, s30, v100
	s_lshl_b32 s15, s4, 1
	v_and_b32_e32 v67, s31, v1
	v_bcnt_u32_b32 v68, v68, 0
	s_add_i32 s15, s52, s15
	v_bcnt_u32_b32 v67, v67, v68
	v_lshl_add_u32 v67, v67, 1, s15
	ds_write_b16 v67, v121 offset:32768
.LBB0_1266:
	s_or_b64 exec, exec, s[34:35]
	s_bcnt1_i32_b64 s15, s[30:31]
	s_add_i32 s4, s4, s15
	v_cmp_gt_u32_sdwa s[30:31], v51, v66 src0_sel:WORD_1 src1_sel:DWORD
	s_and_saveexec_b64 s[34:35], s[30:31]
	s_cbranch_execz .LBB0_1268
	v_and_b32_e32 v68, s30, v100
	s_lshl_b32 s15, s4, 1
	v_and_b32_e32 v67, s31, v1
	v_bcnt_u32_b32 v68, v68, 0
	s_add_i32 s15, s52, s15
	v_bcnt_u32_b32 v67, v67, v68
	v_lshl_add_u32 v67, v67, 1, s15
	ds_write_b16 v67, v122 offset:32768
.LBB0_1268:
	s_or_b64 exec, exec, s[34:35]
	s_bcnt1_i32_b64 s15, s[30:31]
	s_add_i32 s4, s4, s15
	v_cmp_gt_u32_sdwa s[30:31], v52, v66 src0_sel:WORD_0 src1_sel:DWORD
	s_and_saveexec_b64 s[34:35], s[30:31]
	s_cbranch_execz .LBB0_1270
	v_and_b32_e32 v68, s30, v100
	s_lshl_b32 s15, s4, 1
	v_and_b32_e32 v67, s31, v1
	v_bcnt_u32_b32 v68, v68, 0
	s_add_i32 s15, s52, s15
	v_bcnt_u32_b32 v67, v67, v68
	v_lshl_add_u32 v67, v67, 1, s15
	ds_write_b16 v67, v123 offset:32768
.LBB0_1270:
	s_or_b64 exec, exec, s[34:35]
	s_bcnt1_i32_b64 s15, s[30:31]
	s_add_i32 s4, s4, s15
	v_cmp_gt_u32_sdwa s[30:31], v52, v66 src0_sel:WORD_1 src1_sel:DWORD
	s_and_saveexec_b64 s[34:35], s[30:31]
	s_cbranch_execz .LBB0_1272
	v_and_b32_e32 v68, s30, v100
	s_lshl_b32 s15, s4, 1
	v_and_b32_e32 v67, s31, v1
	v_bcnt_u32_b32 v68, v68, 0
	s_add_i32 s15, s52, s15
	v_bcnt_u32_b32 v67, v67, v68
	v_lshl_add_u32 v67, v67, 1, s15
	ds_write_b16 v67, v124 offset:32768
.LBB0_1272:
	s_or_b64 exec, exec, s[34:35]
	s_bcnt1_i32_b64 s15, s[30:31]
	s_add_i32 s4, s4, s15
	v_cmp_gt_u32_sdwa s[30:31], v53, v66 src0_sel:WORD_0 src1_sel:DWORD
	s_and_saveexec_b64 s[34:35], s[30:31]
	s_cbranch_execz .LBB0_1274
	v_and_b32_e32 v68, s30, v100
	s_lshl_b32 s15, s4, 1
	v_and_b32_e32 v67, s31, v1
	v_bcnt_u32_b32 v68, v68, 0
	s_add_i32 s15, s52, s15
	v_bcnt_u32_b32 v67, v67, v68
	v_lshl_add_u32 v67, v67, 1, s15
	ds_write_b16 v67, v125 offset:32768
.LBB0_1274:
	s_or_b64 exec, exec, s[34:35]
	s_bcnt1_i32_b64 s15, s[30:31]
	s_add_i32 s4, s4, s15
	v_cmp_gt_u32_sdwa s[30:31], v53, v66 src0_sel:WORD_1 src1_sel:DWORD
	s_and_saveexec_b64 s[34:35], s[30:31]
	s_cbranch_execz .LBB0_1276
	v_and_b32_e32 v68, s30, v100
	s_lshl_b32 s15, s4, 1
	v_and_b32_e32 v67, s31, v1
	v_bcnt_u32_b32 v68, v68, 0
	s_add_i32 s15, s52, s15
	v_bcnt_u32_b32 v67, v67, v68
	v_lshl_add_u32 v67, v67, 1, s15
	ds_write_b16 v67, v126 offset:32768

.LBB0_1345:
	s_or_b64 exec, exec, s[30:31]
	s_bcnt1_i32_b64 s8, s[8:9]
	s_add_i32 s4, s4, s8
	v_cmp_gt_u32_sdwa s[8:9], v58, v66 src0_sel:WORD_1 src1_sel:DWORD
	s_and_saveexec_b64 s[30:31], s[8:9]
	s_cbranch_execz .LBB0_1347
	v_and_b32_e32 v68, s8, v100
	s_lshl_b32 s15, s4, 1
	v_and_b32_e32 v67, s9, v1
	v_bcnt_u32_b32 v68, v68, 0
	s_add_i32 s15, s52, s15
	v_bcnt_u32_b32 v67, v67, v68
	v_lshl_add_u32 v67, v67, 1, s15
	ds_write_b16 v67, v152 offset:32768
.LBB0_1347:
	s_or_b64 exec, exec, s[30:31]
	s_bcnt1_i32_b64 s8, s[8:9]
	s_add_i32 s4, s4, s8
	v_cmp_gt_u32_sdwa s[8:9], v59, v66 src0_sel:WORD_0 src1_sel:DWORD
	s_and_saveexec_b64 s[30:31], s[8:9]
	s_cbranch_execz .LBB0_1349
	v_and_b32_e32 v68, s8, v100
	s_lshl_b32 s15, s4, 1
	v_and_b32_e32 v67, s9, v1
	v_bcnt_u32_b32 v68, v68, 0
	s_add_i32 s15, s52, s15
	v_bcnt_u32_b32 v67, v67, v68
	v_lshl_add_u32 v67, v67, 1, s15
	ds_write_b16 v67, v153 offset:32768
.LBB0_1349:
	s_or_b64 exec, exec, s[30:31]
	s_bcnt1_i32_b64 s8, s[8:9]
	s_add_i32 s4, s4, s8
	v_cmp_gt_u32_sdwa s[8:9], v59, v66 src0_sel:WORD_1 src1_sel:DWORD
	s_and_saveexec_b64 s[30:31], s[8:9]
	s_cbranch_execz .LBB0_1351
	v_and_b32_e32 v68, s8, v100
	s_lshl_b32 s15, s4, 1
	v_and_b32_e32 v67, s9, v1
	v_bcnt_u32_b32 v68, v68, 0
	s_add_i32 s15, s52, s15
	v_bcnt_u32_b32 v67, v67, v68
	v_lshl_add_u32 v67, v67, 1, s15
	ds_write_b16 v67, v154 offset:32768
.LBB0_1351:
	s_or_b64 exec, exec, s[30:31]
	s_bcnt1_i32_b64 s8, s[8:9]
	s_add_i32 s4, s4, s8
	v_cmp_gt_u32_sdwa s[8:9], v60, v66 src0_sel:WORD_0 src1_sel:DWORD
	s_and_saveexec_b64 s[30:31], s[8:9]
	s_cbranch_execz .LBB0_1353
	v_and_b32_e32 v68, s8, v100
	s_lshl_b32 s15, s4, 1
	v_and_b32_e32 v67, s9, v1
	v_bcnt_u32_b32 v68, v68, 0
	s_add_i32 s15, s52, s15
	v_bcnt_u32_b32 v67, v67, v68
	v_lshl_add_u32 v67, v67, 1, s15
	ds_write_b16 v67, v155 offset:32768
.LBB0_1353:
	s_or_b64 exec, exec, s[30:31]
	s_bcnt1_i32_b64 s8, s[8:9]
	s_add_i32 s4, s4, s8
	v_cmp_gt_u32_sdwa s[8:9], v60, v66 src0_sel:WORD_1 src1_sel:DWORD
	s_and_saveexec_b64 s[30:31], s[8:9]
	s_cbranch_execz .LBB0_1355
	v_and_b32_e32 v68, s8, v100
	s_lshl_b32 s15, s4, 1
	v_and_b32_e32 v67, s9, v1
	v_bcnt_u32_b32 v68, v68, 0
	s_add_i32 s15, s52, s15
	v_bcnt_u32_b32 v67, v67, v68
	v_lshl_add_u32 v67, v67, 1, s15
	ds_write_b16 v67, v156 offset:32768
.LBB0_1355:
	s_or_b64 exec, exec, s[30:31]
	s_bcnt1_i32_b64 s8, s[8:9]
	s_add_i32 s4, s4, s8
	v_cmp_gt_u32_sdwa s[8:9], v61, v66 src0_sel:WORD_0 src1_sel:DWORD
	s_and_saveexec_b64 s[30:31], s[8:9]
	s_cbranch_execz .LBB0_1357
	v_and_b32_e32 v68, s8, v100
	s_lshl_b32 s15, s4, 1
	v_and_b32_e32 v67, s9, v1
	v_bcnt_u32_b32 v68, v68, 0
	s_add_i32 s15, s52, s15
	v_bcnt_u32_b32 v67, v67, v68
	v_lshl_add_u32 v67, v67, 1, s15
	ds_write_b16 v67, v157 offset:32768
.LBB0_1357:
	s_or_b64 exec, exec, s[30:31]
	s_bcnt1_i32_b64 s8, s[8:9]
	s_add_i32 s4, s4, s8
	v_cmp_gt_u32_sdwa s[8:9], v61, v66 src0_sel:WORD_1 src1_sel:DWORD
	s_and_saveexec_b64 s[30:31], s[8:9]
	s_cbranch_execz .LBB0_1359
	v_and_b32_e32 v68, s8, v100
	s_lshl_b32 s15, s4, 1
	v_and_b32_e32 v67, s9, v1
	v_bcnt_u32_b32 v68, v68, 0
	s_add_i32 s15, s52, s15
	v_bcnt_u32_b32 v67, v67, v68
	v_lshl_add_u32 v67, v67, 1, s15
	ds_write_b16 v67, v158 offset:32768

.LBB0_1360:
	v_cmp_gt_u32_sdwa s[8:9], v46, v66 src0_sel:WORD_0 src1_sel:DWORD
	s_and_saveexec_b64 s[30:31], s[8:9]
	s_cbranch_execz .LBB0_1362
	v_and_b32_e32 v68, s8, v100
	s_lshl_b32 s15, s4, 1
	v_and_b32_e32 v67, s9, v1
	v_bcnt_u32_b32 v68, v68, 0
	s_add_i32 s15, s52, s15
	v_bcnt_u32_b32 v67, v67, v68
	v_lshl_add_u32 v67, v67, 1, s15
	ds_write_b16 v67, v159 offset:32768
.LBB0_1362:
	s_or_b64 exec, exec, s[30:31]
	s_bcnt1_i32_b64 s8, s[8:9]
	s_add_i32 s4, s4, s8
	v_cmp_gt_u32_sdwa s[8:9], v46, v66 src0_sel:WORD_1 src1_sel:DWORD
	s_and_saveexec_b64 s[30:31], s[8:9]
	s_cbranch_execz .LBB0_1364
	v_and_b32_e32 v68, s8, v100
	s_lshl_b32 s15, s4, 1
	v_and_b32_e32 v67, s9, v1
	v_bcnt_u32_b32 v68, v68, 0
	s_add_i32 s15, s52, s15
	v_bcnt_u32_b32 v67, v67, v68
	v_lshl_add_u32 v67, v67, 1, s15
	ds_write_b16 v67, v160 offset:32768
.LBB0_1364:
	s_or_b64 exec, exec, s[30:31]
	s_bcnt1_i32_b64 s8, s[8:9]
	s_add_i32 s4, s4, s8
	v_cmp_gt_u32_sdwa s[8:9], v47, v66 src0_sel:WORD_0 src1_sel:DWORD
	s_and_saveexec_b64 s[30:31], s[8:9]
	s_cbranch_execz .LBB0_1366
	v_and_b32_e32 v68, s8, v100
	s_lshl_b32 s15, s4, 1
	v_and_b32_e32 v67, s9, v1
	v_bcnt_u32_b32 v68, v68, 0
	s_add_i32 s15, s52, s15
	v_bcnt_u32_b32 v67, v67, v68
	v_lshl_add_u32 v67, v67, 1, s15
	ds_write_b16 v67, v161 offset:32768
.LBB0_1366:
	s_or_b64 exec, exec, s[30:31]
	s_bcnt1_i32_b64 s8, s[8:9]
	s_add_i32 s4, s4, s8
	v_cmp_gt_u32_sdwa s[8:9], v47, v66 src0_sel:WORD_1 src1_sel:DWORD
	s_and_saveexec_b64 s[30:31], s[8:9]
	s_cbranch_execz .LBB0_1368
	v_and_b32_e32 v68, s8, v100
	s_lshl_b32 s15, s4, 1
	v_and_b32_e32 v67, s9, v1
	v_bcnt_u32_b32 v68, v68, 0
	s_add_i32 s15, s52, s15
	v_bcnt_u32_b32 v67, v67, v68
	v_lshl_add_u32 v67, v67, 1, s15
	ds_write_b16 v67, v162 offset:32768
.LBB0_1368:
	s_or_b64 exec, exec, s[30:31]
	s_bcnt1_i32_b64 s8, s[8:9]
	s_add_i32 s4, s4, s8
	v_cmp_gt_u32_sdwa s[8:9], v48, v66 src0_sel:WORD_0 src1_sel:DWORD
	s_and_saveexec_b64 s[30:31], s[8:9]
	s_cbranch_execz .LBB0_1370
	v_and_b32_e32 v68, s8, v100
	s_lshl_b32 s15, s4, 1
	v_and_b32_e32 v67, s9, v1
	v_bcnt_u32_b32 v68, v68, 0
	s_add_i32 s15, s52, s15
	v_bcnt_u32_b32 v67, v67, v68
	v_lshl_add_u32 v67, v67, 1, s15
	ds_write_b16 v67, v163 offset:32768
.LBB0_1370:
	s_or_b64 exec, exec, s[30:31]
	s_bcnt1_i32_b64 s8, s[8:9]
	s_add_i32 s4, s4, s8
	v_cmp_gt_u32_sdwa s[8:9], v48, v66 src0_sel:WORD_1 src1_sel:DWORD
	s_and_saveexec_b64 s[30:31], s[8:9]
	s_cbranch_execz .LBB0_1372
	v_and_b32_e32 v68, s8, v100
	s_lshl_b32 s15, s4, 1
	v_and_b32_e32 v67, s9, v1
	v_bcnt_u32_b32 v68, v68, 0
	s_add_i32 s15, s52, s15
	v_bcnt_u32_b32 v67, v67, v68
	v_lshl_add_u32 v67, v67, 1, s15
	ds_write_b16 v67, v164 offset:32768
.LBB0_1372:
	s_or_b64 exec, exec, s[30:31]
	s_bcnt1_i32_b64 s8, s[8:9]
	s_add_i32 s4, s4, s8
	v_cmp_gt_u32_sdwa s[8:9], v49, v66 src0_sel:WORD_0 src1_sel:DWORD
	s_and_saveexec_b64 s[30:31], s[8:9]
	s_cbranch_execz .LBB0_1374
	v_and_b32_e32 v68, s8, v100
	s_lshl_b32 s15, s4, 1
	v_and_b32_e32 v67, s9, v1
	v_bcnt_u32_b32 v68, v68, 0
	s_add_i32 s15, s52, s15
	v_bcnt_u32_b32 v67, v67, v68
	v_lshl_add_u32 v67, v67, 1, s15
	ds_write_b16 v67, v165 offset:32768
.LBB0_1374:
	s_or_b64 exec, exec, s[30:31]
	s_bcnt1_i32_b64 s8, s[8:9]
	s_add_i32 s4, s4, s8
	v_cmp_gt_u32_sdwa s[8:9], v49, v66 src0_sel:WORD_1 src1_sel:DWORD
	s_and_saveexec_b64 s[30:31], s[8:9]
	s_cbranch_execz .LBB0_1376
	v_and_b32_e32 v68, s8, v100
	s_lshl_b32 s15, s4, 1
	v_and_b32_e32 v67, s9, v1
	v_bcnt_u32_b32 v68, v68, 0
	s_add_i32 s15, s52, s15
	v_bcnt_u32_b32 v67, v67, v68
	v_lshl_add_u32 v67, v67, 1, s15
	ds_write_b16 v67, v166 offset:32768

.LBB0_1377:
	v_cmp_gt_u32_sdwa s[8:9], v34, v66 src0_sel:WORD_0 src1_sel:DWORD
	s_and_saveexec_b64 s[30:31], s[8:9]
	s_cbranch_execz .LBB0_1379
	v_and_b32_e32 v68, s8, v100
	s_lshl_b32 s15, s4, 1
	v_and_b32_e32 v67, s9, v1
	v_bcnt_u32_b32 v68, v68, 0
	s_add_i32 s15, s52, s15
	v_bcnt_u32_b32 v67, v67, v68
	v_lshl_add_u32 v67, v67, 1, s15
	ds_write_b16 v67, v167 offset:32768
.LBB0_1379:
	s_or_b64 exec, exec, s[30:31]
	s_bcnt1_i32_b64 s8, s[8:9]
	s_add_i32 s4, s4, s8
	v_cmp_gt_u32_sdwa s[8:9], v34, v66 src0_sel:WORD_1 src1_sel:DWORD
	s_and_saveexec_b64 s[30:31], s[8:9]
	s_cbranch_execz .LBB0_1381
	v_and_b32_e32 v68, s8, v100
	s_lshl_b32 s15, s4, 1
	v_and_b32_e32 v67, s9, v1
	v_bcnt_u32_b32 v68, v68, 0
	s_add_i32 s15, s52, s15
	v_bcnt_u32_b32 v67, v67, v68
	v_lshl_add_u32 v67, v67, 1, s15
	ds_write_b16 v67, v168 offset:32768
.LBB0_1381:
	s_or_b64 exec, exec, s[30:31]
	s_bcnt1_i32_b64 s8, s[8:9]
	s_add_i32 s4, s4, s8
	v_cmp_gt_u32_sdwa s[8:9], v35, v66 src0_sel:WORD_0 src1_sel:DWORD
	s_and_saveexec_b64 s[30:31], s[8:9]
	s_cbranch_execz .LBB0_1383
	v_and_b32_e32 v68, s8, v100
	s_lshl_b32 s15, s4, 1
	v_and_b32_e32 v67, s9, v1
	v_bcnt_u32_b32 v68, v68, 0
	s_add_i32 s15, s52, s15
	v_bcnt_u32_b32 v67, v67, v68
	v_lshl_add_u32 v67, v67, 1, s15
	ds_write_b16 v67, v169 offset:32768
.LBB0_1383:
	s_or_b64 exec, exec, s[30:31]
	s_bcnt1_i32_b64 s8, s[8:9]
	s_add_i32 s4, s4, s8
	v_cmp_gt_u32_sdwa s[8:9], v35, v66 src0_sel:WORD_1 src1_sel:DWORD
	s_and_saveexec_b64 s[30:31], s[8:9]
	s_cbranch_execz .LBB0_1385
	v_and_b32_e32 v68, s8, v100
	s_lshl_b32 s15, s4, 1
	v_and_b32_e32 v67, s9, v1
	v_bcnt_u32_b32 v68, v68, 0
	s_add_i32 s15, s52, s15
	v_bcnt_u32_b32 v67, v67, v68
	v_lshl_add_u32 v67, v67, 1, s15
	ds_write_b16 v67, v170 offset:32768
.LBB0_1385:
	s_or_b64 exec, exec, s[30:31]
	s_bcnt1_i32_b64 s8, s[8:9]
	s_add_i32 s4, s4, s8
	v_cmp_gt_u32_sdwa s[8:9], v36, v66 src0_sel:WORD_0 src1_sel:DWORD
	s_and_saveexec_b64 s[30:31], s[8:9]
	s_cbranch_execz .LBB0_1387
	v_and_b32_e32 v68, s8, v100
	s_lshl_b32 s15, s4, 1
	v_and_b32_e32 v67, s9, v1
	v_bcnt_u32_b32 v68, v68, 0
	s_add_i32 s15, s52, s15
	v_bcnt_u32_b32 v67, v67, v68
	v_lshl_add_u32 v67, v67, 1, s15
	ds_write_b16 v67, v171 offset:32768
.LBB0_1387:
	s_or_b64 exec, exec, s[30:31]
	s_bcnt1_i32_b64 s8, s[8:9]
	s_add_i32 s4, s4, s8
	v_cmp_gt_u32_sdwa s[8:9], v36, v66 src0_sel:WORD_1 src1_sel:DWORD
	s_and_saveexec_b64 s[30:31], s[8:9]
	s_cbranch_execz .LBB0_1389
	v_and_b32_e32 v68, s8, v100
	s_lshl_b32 s15, s4, 1
	v_and_b32_e32 v67, s9, v1
	v_bcnt_u32_b32 v68, v68, 0
	s_add_i32 s15, s52, s15
	v_bcnt_u32_b32 v67, v67, v68
	v_lshl_add_u32 v67, v67, 1, s15
	ds_write_b16 v67, v172 offset:32768
.LBB0_1389:
	s_or_b64 exec, exec, s[30:31]
	s_bcnt1_i32_b64 s8, s[8:9]
	s_add_i32 s4, s4, s8
	v_cmp_gt_u32_sdwa s[8:9], v37, v66 src0_sel:WORD_0 src1_sel:DWORD
	s_and_saveexec_b64 s[30:31], s[8:9]
	s_cbranch_execz .LBB0_1391
	v_and_b32_e32 v68, s8, v100
	s_lshl_b32 s15, s4, 1
	v_and_b32_e32 v67, s9, v1
	v_bcnt_u32_b32 v68, v68, 0
	s_add_i32 s15, s52, s15
	v_bcnt_u32_b32 v67, v67, v68
	v_lshl_add_u32 v67, v67, 1, s15
	ds_write_b16 v67, v173 offset:32768
.LBB0_1391:
	s_or_b64 exec, exec, s[30:31]
	s_bcnt1_i32_b64 s8, s[8:9]
	s_add_i32 s4, s4, s8
	v_cmp_gt_u32_sdwa s[8:9], v37, v66 src0_sel:WORD_1 src1_sel:DWORD
	s_and_saveexec_b64 s[30:31], s[8:9]
	s_cbranch_execz .LBB0_1393
	v_and_b32_e32 v68, s8, v100
	s_lshl_b32 s15, s4, 1
	v_and_b32_e32 v67, s9, v1
	v_bcnt_u32_b32 v68, v68, 0
	s_add_i32 s15, s52, s15
	v_bcnt_u32_b32 v67, v67, v68
	v_lshl_add_u32 v67, v67, 1, s15
	ds_write_b16 v67, v174 offset:32768

.LBB0_1394:
	v_cmp_gt_u32_sdwa s[8:9], v22, v66 src0_sel:WORD_0 src1_sel:DWORD
	s_and_saveexec_b64 s[30:31], s[8:9]
	s_cbranch_execz .LBB0_1396
	v_and_b32_e32 v68, s8, v100
	s_lshl_b32 s15, s4, 1
	v_and_b32_e32 v67, s9, v1
	v_bcnt_u32_b32 v68, v68, 0
	s_add_i32 s15, s52, s15
	v_bcnt_u32_b32 v67, v67, v68
	v_lshl_add_u32 v67, v67, 1, s15
	ds_write_b16 v67, v175 offset:32768
.LBB0_1396:
	s_or_b64 exec, exec, s[30:31]
	s_bcnt1_i32_b64 s8, s[8:9]
	s_add_i32 s4, s4, s8
	v_cmp_gt_u32_sdwa s[8:9], v22, v66 src0_sel:WORD_1 src1_sel:DWORD
	s_and_saveexec_b64 s[30:31], s[8:9]
	s_cbranch_execz .LBB0_1398
	v_and_b32_e32 v68, s8, v100
	s_lshl_b32 s15, s4, 1
	v_and_b32_e32 v67, s9, v1
	v_bcnt_u32_b32 v68, v68, 0
	s_add_i32 s15, s52, s15
	v_bcnt_u32_b32 v67, v67, v68
	v_lshl_add_u32 v67, v67, 1, s15
	ds_write_b16 v67, v176 offset:32768
.LBB0_1398:
	s_or_b64 exec, exec, s[30:31]
	s_bcnt1_i32_b64 s8, s[8:9]
	s_add_i32 s4, s4, s8
	v_cmp_gt_u32_sdwa s[8:9], v23, v66 src0_sel:WORD_0 src1_sel:DWORD
	s_and_saveexec_b64 s[30:31], s[8:9]
	s_cbranch_execz .LBB0_1400
	v_and_b32_e32 v68, s8, v100
	s_lshl_b32 s15, s4, 1
	v_and_b32_e32 v67, s9, v1
	v_bcnt_u32_b32 v68, v68, 0
	s_add_i32 s15, s52, s15
	v_bcnt_u32_b32 v67, v67, v68
	v_lshl_add_u32 v67, v67, 1, s15
	ds_write_b16 v67, v177 offset:32768
.LBB0_1400:
	s_or_b64 exec, exec, s[30:31]
	s_bcnt1_i32_b64 s8, s[8:9]
	s_add_i32 s4, s4, s8
	v_cmp_gt_u32_sdwa s[8:9], v23, v66 src0_sel:WORD_1 src1_sel:DWORD
	s_and_saveexec_b64 s[30:31], s[8:9]
	s_cbranch_execz .LBB0_1402
	v_and_b32_e32 v68, s8, v100
	s_lshl_b32 s15, s4, 1
	v_and_b32_e32 v67, s9, v1
	v_bcnt_u32_b32 v68, v68, 0
	s_add_i32 s15, s52, s15
	v_bcnt_u32_b32 v67, v67, v68
	v_lshl_add_u32 v67, v67, 1, s15
	ds_write_b16 v67, v178 offset:32768
.LBB0_1402:
	s_or_b64 exec, exec, s[30:31]
	s_bcnt1_i32_b64 s8, s[8:9]
	s_add_i32 s4, s4, s8
	v_cmp_gt_u32_sdwa s[8:9], v24, v66 src0_sel:WORD_0 src1_sel:DWORD
	s_and_saveexec_b64 s[30:31], s[8:9]
	s_cbranch_execz .LBB0_1404
	v_and_b32_e32 v68, s8, v100
	s_lshl_b32 s15, s4, 1
	v_and_b32_e32 v67, s9, v1
	v_bcnt_u32_b32 v68, v68, 0
	s_add_i32 s15, s52, s15
	v_bcnt_u32_b32 v67, v67, v68
	v_lshl_add_u32 v67, v67, 1, s15
	ds_write_b16 v67, v179 offset:32768
.LBB0_1404:
	s_or_b64 exec, exec, s[30:31]
	s_bcnt1_i32_b64 s8, s[8:9]
	s_add_i32 s4, s4, s8
	v_cmp_gt_u32_sdwa s[8:9], v24, v66 src0_sel:WORD_1 src1_sel:DWORD
	s_and_saveexec_b64 s[30:31], s[8:9]
	s_cbranch_execz .LBB0_1406
	v_and_b32_e32 v68, s8, v100
	s_lshl_b32 s15, s4, 1
	v_and_b32_e32 v67, s9, v1
	v_bcnt_u32_b32 v68, v68, 0
	s_add_i32 s15, s52, s15
	v_bcnt_u32_b32 v67, v67, v68
	v_lshl_add_u32 v67, v67, 1, s15
	ds_write_b16 v67, v180 offset:32768
.LBB0_1406:
	s_or_b64 exec, exec, s[30:31]
	s_bcnt1_i32_b64 s8, s[8:9]
	s_add_i32 s4, s4, s8
	v_cmp_gt_u32_sdwa s[8:9], v25, v66 src0_sel:WORD_0 src1_sel:DWORD
	s_and_saveexec_b64 s[30:31], s[8:9]
	s_cbranch_execz .LBB0_1408
	v_and_b32_e32 v68, s8, v100
	s_lshl_b32 s15, s4, 1
	v_and_b32_e32 v67, s9, v1
	v_bcnt_u32_b32 v68, v68, 0
	s_add_i32 s15, s52, s15
	v_bcnt_u32_b32 v67, v67, v68
	v_lshl_add_u32 v67, v67, 1, s15
	ds_write_b16 v67, v181 offset:32768
.LBB0_1408:
	s_or_b64 exec, exec, s[30:31]
	s_bcnt1_i32_b64 s8, s[8:9]
	s_add_i32 s4, s4, s8
	v_cmp_gt_u32_sdwa s[8:9], v25, v66 src0_sel:WORD_1 src1_sel:DWORD
	s_and_saveexec_b64 s[30:31], s[8:9]
	s_cbranch_execz .LBB0_1410
	v_and_b32_e32 v68, s8, v100
	s_lshl_b32 s15, s4, 1
	v_and_b32_e32 v67, s9, v1
	v_bcnt_u32_b32 v68, v68, 0
	s_add_i32 s15, s52, s15
	v_bcnt_u32_b32 v67, v67, v68
	v_lshl_add_u32 v67, v67, 1, s15
	ds_write_b16 v67, v182 offset:32768

.LBB0_1411:
	v_cmp_gt_u32_sdwa s[8:9], v62, v66 src0_sel:WORD_0 src1_sel:DWORD
	s_and_saveexec_b64 s[30:31], s[8:9]
	s_cbranch_execz .LBB0_1413
	v_and_b32_e32 v68, s8, v100
	s_lshl_b32 s15, s4, 1
	v_and_b32_e32 v67, s9, v1
	v_bcnt_u32_b32 v68, v68, 0
	s_add_i32 s15, s52, s15
	v_bcnt_u32_b32 v67, v67, v68
	v_lshl_add_u32 v67, v67, 1, s15
	ds_write_b16 v67, v183 offset:32768
.LBB0_1413:
	s_or_b64 exec, exec, s[30:31]
	s_bcnt1_i32_b64 s8, s[8:9]
	s_add_i32 s4, s4, s8
	v_cmp_gt_u32_sdwa s[8:9], v62, v66 src0_sel:WORD_1 src1_sel:DWORD
	s_and_saveexec_b64 s[30:31], s[8:9]
	s_cbranch_execz .LBB0_1415
	v_and_b32_e32 v68, s8, v100
	s_lshl_b32 s15, s4, 1
	v_and_b32_e32 v67, s9, v1
	v_bcnt_u32_b32 v68, v68, 0
	s_add_i32 s15, s52, s15
	v_bcnt_u32_b32 v67, v67, v68
	v_lshl_add_u32 v67, v67, 1, s15
	ds_write_b16 v67, v184 offset:32768
.LBB0_1415:
	s_or_b64 exec, exec, s[30:31]
	s_bcnt1_i32_b64 s8, s[8:9]
	s_add_i32 s4, s4, s8
	v_cmp_gt_u32_sdwa s[8:9], v63, v66 src0_sel:WORD_0 src1_sel:DWORD
	s_and_saveexec_b64 s[30:31], s[8:9]
	s_cbranch_execz .LBB0_1417
	v_and_b32_e32 v68, s8, v100
	s_lshl_b32 s15, s4, 1
	v_and_b32_e32 v67, s9, v1
	v_bcnt_u32_b32 v68, v68, 0
	s_add_i32 s15, s52, s15
	v_bcnt_u32_b32 v67, v67, v68
	v_lshl_add_u32 v67, v67, 1, s15
	ds_write_b16 v67, v185 offset:32768
.LBB0_1417:
	s_or_b64 exec, exec, s[30:31]
	s_bcnt1_i32_b64 s8, s[8:9]
	s_add_i32 s4, s4, s8
	v_cmp_gt_u32_sdwa s[8:9], v63, v66 src0_sel:WORD_1 src1_sel:DWORD
	s_and_saveexec_b64 s[30:31], s[8:9]
	s_cbranch_execz .LBB0_1419
	v_and_b32_e32 v68, s8, v100
	s_lshl_b32 s15, s4, 1
	v_and_b32_e32 v67, s9, v1
	v_bcnt_u32_b32 v68, v68, 0
	s_add_i32 s15, s52, s15
	v_bcnt_u32_b32 v67, v67, v68
	v_lshl_add_u32 v67, v67, 1, s15
	ds_write_b16 v67, v186 offset:32768
.LBB0_1419:
	s_or_b64 exec, exec, s[30:31]
	s_bcnt1_i32_b64 s8, s[8:9]
	s_add_i32 s4, s4, s8
	v_cmp_gt_u32_sdwa s[8:9], v64, v66 src0_sel:WORD_0 src1_sel:DWORD
	s_and_saveexec_b64 s[30:31], s[8:9]
	s_cbranch_execz .LBB0_1421
	v_and_b32_e32 v68, s8, v100
	s_lshl_b32 s15, s4, 1
	v_and_b32_e32 v67, s9, v1
	v_bcnt_u32_b32 v68, v68, 0
	s_add_i32 s15, s52, s15
	v_bcnt_u32_b32 v67, v67, v68
	v_lshl_add_u32 v67, v67, 1, s15
	ds_write_b16 v67, v187 offset:32768
.LBB0_1421:
	s_or_b64 exec, exec, s[30:31]
	s_bcnt1_i32_b64 s8, s[8:9]
	s_add_i32 s4, s4, s8
	v_cmp_gt_u32_sdwa s[8:9], v64, v66 src0_sel:WORD_1 src1_sel:DWORD
	s_and_saveexec_b64 s[30:31], s[8:9]
	s_cbranch_execz .LBB0_1423
	v_and_b32_e32 v68, s8, v100
	s_lshl_b32 s15, s4, 1
	v_and_b32_e32 v67, s9, v1
	v_bcnt_u32_b32 v68, v68, 0
	s_add_i32 s15, s52, s15
	v_bcnt_u32_b32 v67, v67, v68
	v_lshl_add_u32 v67, v67, 1, s15
	ds_write_b16 v67, v188 offset:32768
.LBB0_1423:
	s_or_b64 exec, exec, s[30:31]
	s_bcnt1_i32_b64 s8, s[8:9]
	s_add_i32 s4, s4, s8
	v_cmp_gt_u32_sdwa s[8:9], v65, v66 src0_sel:WORD_0 src1_sel:DWORD
	s_and_saveexec_b64 s[30:31], s[8:9]
	s_cbranch_execz .LBB0_1425
	v_and_b32_e32 v68, s8, v100
	s_lshl_b32 s15, s4, 1
	v_and_b32_e32 v67, s9, v1
	v_bcnt_u32_b32 v68, v68, 0
	s_add_i32 s15, s52, s15
	v_bcnt_u32_b32 v67, v67, v68
	v_lshl_add_u32 v67, v67, 1, s15
	ds_write_b16 v67, v189 offset:32768
.LBB0_1425:
	s_or_b64 exec, exec, s[30:31]
	s_bcnt1_i32_b64 s8, s[8:9]
	s_add_i32 s4, s4, s8
	v_cmp_gt_u32_sdwa s[8:9], v65, v66 src0_sel:WORD_1 src1_sel:DWORD
	s_and_saveexec_b64 s[30:31], s[8:9]
	s_cbranch_execz .LBB0_1427
	v_and_b32_e32 v68, s8, v100
	s_lshl_b32 s15, s4, 1
	v_and_b32_e32 v67, s9, v1
	v_bcnt_u32_b32 v68, v68, 0
	s_add_i32 s15, s52, s15
	v_bcnt_u32_b32 v67, v67, v68
	v_lshl_add_u32 v67, v67, 1, s15
	ds_write_b16 v67, v190 offset:32768

.LBB0_1428:
	v_cmp_gt_u32_sdwa s[8:9], v54, v66 src0_sel:WORD_0 src1_sel:DWORD
	s_and_saveexec_b64 s[30:31], s[8:9]
	s_cbranch_execz .LBB0_1430
	v_and_b32_e32 v68, s8, v100
	s_lshl_b32 s15, s4, 1
	v_and_b32_e32 v67, s9, v1
	v_bcnt_u32_b32 v68, v68, 0
	s_add_i32 s15, s52, s15
	v_bcnt_u32_b32 v67, v67, v68
	v_lshl_add_u32 v67, v67, 1, s15
	ds_write_b16 v67, v191 offset:32768
.LBB0_1430:
	s_or_b64 exec, exec, s[30:31]
	s_bcnt1_i32_b64 s8, s[8:9]
	s_add_i32 s4, s4, s8
	v_cmp_gt_u32_sdwa s[8:9], v54, v66 src0_sel:WORD_1 src1_sel:DWORD
	s_and_saveexec_b64 s[30:31], s[8:9]
	s_cbranch_execz .LBB0_1432
	v_and_b32_e32 v68, s8, v100
	s_lshl_b32 s15, s4, 1
	v_and_b32_e32 v67, s9, v1
	v_bcnt_u32_b32 v68, v68, 0
	s_add_i32 s15, s52, s15
	v_bcnt_u32_b32 v67, v67, v68
	v_lshl_add_u32 v67, v67, 1, s15
	ds_write_b16 v67, v192 offset:32768
.LBB0_1432:
	s_or_b64 exec, exec, s[30:31]
	s_bcnt1_i32_b64 s8, s[8:9]
	s_add_i32 s4, s4, s8
	v_cmp_gt_u32_sdwa s[8:9], v55, v66 src0_sel:WORD_0 src1_sel:DWORD
	s_and_saveexec_b64 s[30:31], s[8:9]
	s_cbranch_execz .LBB0_1434
	v_and_b32_e32 v68, s8, v100
	s_lshl_b32 s15, s4, 1
	v_and_b32_e32 v67, s9, v1
	v_bcnt_u32_b32 v68, v68, 0
	s_add_i32 s15, s52, s15
	v_bcnt_u32_b32 v67, v67, v68
	v_lshl_add_u32 v67, v67, 1, s15
	ds_write_b16 v67, v193 offset:32768
.LBB0_1434:
	s_or_b64 exec, exec, s[30:31]
	s_bcnt1_i32_b64 s8, s[8:9]
	s_add_i32 s4, s4, s8
	v_cmp_gt_u32_sdwa s[8:9], v55, v66 src0_sel:WORD_1 src1_sel:DWORD
	s_and_saveexec_b64 s[30:31], s[8:9]
	s_cbranch_execz .LBB0_1436
	v_and_b32_e32 v68, s8, v100
	s_lshl_b32 s15, s4, 1
	v_and_b32_e32 v67, s9, v1
	v_bcnt_u32_b32 v68, v68, 0
	s_add_i32 s15, s52, s15
	v_bcnt_u32_b32 v67, v67, v68
	v_lshl_add_u32 v67, v67, 1, s15
	ds_write_b16 v67, v194 offset:32768
.LBB0_1436:
	s_or_b64 exec, exec, s[30:31]
	s_bcnt1_i32_b64 s8, s[8:9]
	s_add_i32 s4, s4, s8
	v_cmp_gt_u32_sdwa s[8:9], v56, v66 src0_sel:WORD_0 src1_sel:DWORD
	s_and_saveexec_b64 s[30:31], s[8:9]
	s_cbranch_execz .LBB0_1438
	v_and_b32_e32 v68, s8, v100
	s_lshl_b32 s15, s4, 1
	v_and_b32_e32 v67, s9, v1
	v_bcnt_u32_b32 v68, v68, 0
	s_add_i32 s15, s52, s15
	v_bcnt_u32_b32 v67, v67, v68
	v_lshl_add_u32 v67, v67, 1, s15
	ds_write_b16 v67, v195 offset:32768
.LBB0_1438:
	s_or_b64 exec, exec, s[30:31]
	s_bcnt1_i32_b64 s8, s[8:9]
	s_add_i32 s4, s4, s8
	v_cmp_gt_u32_sdwa s[8:9], v56, v66 src0_sel:WORD_1 src1_sel:DWORD
	s_and_saveexec_b64 s[30:31], s[8:9]
	s_cbranch_execz .LBB0_1440
	v_and_b32_e32 v68, s8, v100
	s_lshl_b32 s15, s4, 1
	v_and_b32_e32 v67, s9, v1
	v_bcnt_u32_b32 v68, v68, 0
	s_add_i32 s15, s52, s15
	v_bcnt_u32_b32 v67, v67, v68
	v_lshl_add_u32 v67, v67, 1, s15
	ds_write_b16 v67, v196 offset:32768
.LBB0_1440:
	s_or_b64 exec, exec, s[30:31]
	s_bcnt1_i32_b64 s8, s[8:9]
	s_add_i32 s4, s4, s8
	v_cmp_gt_u32_sdwa s[8:9], v57, v66 src0_sel:WORD_0 src1_sel:DWORD
	s_and_saveexec_b64 s[30:31], s[8:9]
	s_cbranch_execz .LBB0_1442
	v_and_b32_e32 v68, s8, v100
	s_lshl_b32 s15, s4, 1
	v_and_b32_e32 v67, s9, v1
	v_bcnt_u32_b32 v68, v68, 0
	s_add_i32 s15, s52, s15
	v_bcnt_u32_b32 v67, v67, v68
	v_lshl_add_u32 v67, v67, 1, s15
	ds_write_b16 v67, v197 offset:32768
.LBB0_1442:
	s_or_b64 exec, exec, s[30:31]
	s_bcnt1_i32_b64 s8, s[8:9]
	s_add_i32 s4, s4, s8
	v_cmp_gt_u32_sdwa s[8:9], v57, v66 src0_sel:WORD_1 src1_sel:DWORD
	s_and_saveexec_b64 s[30:31], s[8:9]
	s_cbranch_execz .LBB0_1444
	v_and_b32_e32 v68, s8, v100
	s_lshl_b32 s15, s4, 1
	v_and_b32_e32 v67, s9, v1
	v_bcnt_u32_b32 v68, v68, 0
	s_add_i32 s15, s52, s15
	v_bcnt_u32_b32 v67, v67, v68
	v_lshl_add_u32 v67, v67, 1, s15
	ds_write_b16 v67, v198 offset:32768

.LBB0_1445:
	v_cmp_gt_u32_sdwa s[8:9], v42, v66 src0_sel:WORD_0 src1_sel:DWORD
	s_and_saveexec_b64 s[30:31], s[8:9]
	s_cbranch_execz .LBB0_1447
	v_and_b32_e32 v68, s8, v100
	s_lshl_b32 s15, s4, 1
	v_and_b32_e32 v67, s9, v1
	v_bcnt_u32_b32 v68, v68, 0
	s_add_i32 s15, s52, s15
	v_bcnt_u32_b32 v67, v67, v68
	v_lshl_add_u32 v67, v67, 1, s15
	ds_write_b16 v67, v199 offset:32768
.LBB0_1447:
	s_or_b64 exec, exec, s[30:31]
	s_bcnt1_i32_b64 s8, s[8:9]
	s_add_i32 s4, s4, s8
	v_cmp_gt_u32_sdwa s[8:9], v42, v66 src0_sel:WORD_1 src1_sel:DWORD
	s_and_saveexec_b64 s[30:31], s[8:9]
	s_cbranch_execz .LBB0_1449
	v_and_b32_e32 v68, s8, v100
	s_lshl_b32 s15, s4, 1
	v_and_b32_e32 v67, s9, v1
	v_bcnt_u32_b32 v68, v68, 0
	s_add_i32 s15, s52, s15
	v_bcnt_u32_b32 v67, v67, v68
	v_lshl_add_u32 v67, v67, 1, s15
	ds_write_b16 v67, v200 offset:32768
.LBB0_1449:
	s_or_b64 exec, exec, s[30:31]
	s_bcnt1_i32_b64 s8, s[8:9]
	s_add_i32 s4, s4, s8
	v_cmp_gt_u32_sdwa s[8:9], v43, v66 src0_sel:WORD_0 src1_sel:DWORD
	s_and_saveexec_b64 s[30:31], s[8:9]
	s_cbranch_execz .LBB0_1451
	v_and_b32_e32 v68, s8, v100
	s_lshl_b32 s15, s4, 1
	v_and_b32_e32 v67, s9, v1
	v_bcnt_u32_b32 v68, v68, 0
	s_add_i32 s15, s52, s15
	v_bcnt_u32_b32 v67, v67, v68
	v_lshl_add_u32 v67, v67, 1, s15
	ds_write_b16 v67, v201 offset:32768
.LBB0_1451:
	s_or_b64 exec, exec, s[30:31]
	s_bcnt1_i32_b64 s8, s[8:9]
	s_add_i32 s4, s4, s8
	v_cmp_gt_u32_sdwa s[8:9], v43, v66 src0_sel:WORD_1 src1_sel:DWORD
	s_and_saveexec_b64 s[30:31], s[8:9]
	s_cbranch_execz .LBB0_1453
	v_and_b32_e32 v68, s8, v100
	s_lshl_b32 s15, s4, 1
	v_and_b32_e32 v67, s9, v1
	v_bcnt_u32_b32 v68, v68, 0
	s_add_i32 s15, s52, s15
	v_bcnt_u32_b32 v67, v67, v68
	v_lshl_add_u32 v67, v67, 1, s15
	ds_write_b16 v67, v202 offset:32768
.LBB0_1453:
	s_or_b64 exec, exec, s[30:31]
	s_bcnt1_i32_b64 s8, s[8:9]
	s_add_i32 s4, s4, s8
	v_cmp_gt_u32_sdwa s[8:9], v44, v66 src0_sel:WORD_0 src1_sel:DWORD
	s_and_saveexec_b64 s[30:31], s[8:9]
	s_cbranch_execz .LBB0_1455
	v_and_b32_e32 v68, s8, v100
	s_lshl_b32 s15, s4, 1
	v_and_b32_e32 v67, s9, v1
	v_bcnt_u32_b32 v68, v68, 0
	s_add_i32 s15, s52, s15
	v_bcnt_u32_b32 v67, v67, v68
	v_lshl_add_u32 v67, v67, 1, s15
	ds_write_b16 v67, v203 offset:32768
.LBB0_1455:
	s_or_b64 exec, exec, s[30:31]
	s_bcnt1_i32_b64 s8, s[8:9]
	s_add_i32 s4, s4, s8
	v_cmp_gt_u32_sdwa s[8:9], v44, v66 src0_sel:WORD_1 src1_sel:DWORD
	s_and_saveexec_b64 s[30:31], s[8:9]
	s_cbranch_execz .LBB0_1457
	v_and_b32_e32 v68, s8, v100
	s_lshl_b32 s15, s4, 1
	v_and_b32_e32 v67, s9, v1
	v_bcnt_u32_b32 v68, v68, 0
	s_add_i32 s15, s52, s15
	v_bcnt_u32_b32 v67, v67, v68
	v_lshl_add_u32 v67, v67, 1, s15
	ds_write_b16 v67, v204 offset:32768
.LBB0_1457:
	s_or_b64 exec, exec, s[30:31]
	s_bcnt1_i32_b64 s8, s[8:9]
	s_add_i32 s4, s4, s8
	v_cmp_gt_u32_sdwa s[8:9], v45, v66 src0_sel:WORD_0 src1_sel:DWORD
	s_and_saveexec_b64 s[30:31], s[8:9]
	s_cbranch_execz .LBB0_1459
	v_and_b32_e32 v68, s8, v100
	s_lshl_b32 s15, s4, 1
	v_and_b32_e32 v67, s9, v1
	v_bcnt_u32_b32 v68, v68, 0
	s_add_i32 s15, s52, s15
	v_bcnt_u32_b32 v67, v67, v68
	v_lshl_add_u32 v67, v67, 1, s15
	ds_write_b16 v67, v205 offset:32768
.LBB0_1459:
	s_or_b64 exec, exec, s[30:31]
	s_bcnt1_i32_b64 s8, s[8:9]
	s_add_i32 s4, s4, s8
	v_cmp_gt_u32_sdwa s[8:9], v45, v66 src0_sel:WORD_1 src1_sel:DWORD
	s_and_saveexec_b64 s[30:31], s[8:9]
	s_cbranch_execz .LBB0_1461
	v_and_b32_e32 v68, s8, v100
	s_lshl_b32 s15, s4, 1
	v_and_b32_e32 v67, s9, v1
	v_bcnt_u32_b32 v68, v68, 0
	s_add_i32 s15, s52, s15
	v_bcnt_u32_b32 v67, v67, v68
	v_lshl_add_u32 v67, v67, 1, s15
	ds_write_b16 v67, v206 offset:32768

.LBB0_1462:
	v_cmp_gt_u32_sdwa s[8:9], v30, v66 src0_sel:WORD_0 src1_sel:DWORD
	s_and_saveexec_b64 s[30:31], s[8:9]
	s_cbranch_execz .LBB0_1464
	v_and_b32_e32 v68, s8, v100
	s_lshl_b32 s15, s4, 1
	v_and_b32_e32 v67, s9, v1
	v_bcnt_u32_b32 v68, v68, 0
	s_add_i32 s15, s52, s15
	v_bcnt_u32_b32 v67, v67, v68
	v_lshl_add_u32 v67, v67, 1, s15
	ds_write_b16 v67, v207 offset:32768
.LBB0_1464:
	s_or_b64 exec, exec, s[30:31]
	s_bcnt1_i32_b64 s8, s[8:9]
	s_add_i32 s4, s4, s8
	v_cmp_gt_u32_sdwa s[8:9], v30, v66 src0_sel:WORD_1 src1_sel:DWORD
	s_and_saveexec_b64 s[30:31], s[8:9]
	s_cbranch_execz .LBB0_1466
	v_and_b32_e32 v68, s8, v100
	s_lshl_b32 s15, s4, 1
	v_and_b32_e32 v67, s9, v1
	v_bcnt_u32_b32 v68, v68, 0
	s_add_i32 s15, s52, s15
	v_bcnt_u32_b32 v67, v67, v68
	v_lshl_add_u32 v67, v67, 1, s15
	ds_write_b16 v67, v208 offset:32768
.LBB0_1466:
	s_or_b64 exec, exec, s[30:31]
	s_bcnt1_i32_b64 s8, s[8:9]
	s_add_i32 s4, s4, s8
	v_cmp_gt_u32_sdwa s[8:9], v31, v66 src0_sel:WORD_0 src1_sel:DWORD
	s_and_saveexec_b64 s[30:31], s[8:9]
	s_cbranch_execz .LBB0_1468
	v_and_b32_e32 v68, s8, v100
	s_lshl_b32 s15, s4, 1
	v_and_b32_e32 v67, s9, v1
	v_bcnt_u32_b32 v68, v68, 0
	s_add_i32 s15, s52, s15
	v_bcnt_u32_b32 v67, v67, v68
	v_lshl_add_u32 v67, v67, 1, s15
	ds_write_b16 v67, v209 offset:32768
.LBB0_1468:
	s_or_b64 exec, exec, s[30:31]
	s_bcnt1_i32_b64 s8, s[8:9]
	s_add_i32 s4, s4, s8
	v_cmp_gt_u32_sdwa s[8:9], v31, v66 src0_sel:WORD_1 src1_sel:DWORD
	s_and_saveexec_b64 s[30:31], s[8:9]
	s_cbranch_execz .LBB0_1470
	v_and_b32_e32 v68, s8, v100
	s_lshl_b32 s15, s4, 1
	v_and_b32_e32 v67, s9, v1
	v_bcnt_u32_b32 v68, v68, 0
	s_add_i32 s15, s52, s15
	v_bcnt_u32_b32 v67, v67, v68
	v_lshl_add_u32 v67, v67, 1, s15
	ds_write_b16 v67, v210 offset:32768
.LBB0_1470:
	s_or_b64 exec, exec, s[30:31]
	s_bcnt1_i32_b64 s8, s[8:9]
	s_add_i32 s4, s4, s8
	v_cmp_gt_u32_sdwa s[8:9], v32, v66 src0_sel:WORD_0 src1_sel:DWORD
	s_and_saveexec_b64 s[30:31], s[8:9]
	s_cbranch_execz .LBB0_1472
	v_and_b32_e32 v68, s8, v100
	s_lshl_b32 s15, s4, 1
	v_and_b32_e32 v67, s9, v1
	v_bcnt_u32_b32 v68, v68, 0
	s_add_i32 s15, s52, s15
	v_bcnt_u32_b32 v67, v67, v68
	v_lshl_add_u32 v67, v67, 1, s15
	ds_write_b16 v67, v211 offset:32768
.LBB0_1472:
	s_or_b64 exec, exec, s[30:31]
	s_bcnt1_i32_b64 s8, s[8:9]
	s_add_i32 s4, s4, s8
	v_cmp_gt_u32_sdwa s[8:9], v32, v66 src0_sel:WORD_1 src1_sel:DWORD
	s_and_saveexec_b64 s[30:31], s[8:9]
	s_cbranch_execz .LBB0_1474
	v_and_b32_e32 v68, s8, v100
	s_lshl_b32 s15, s4, 1
	v_and_b32_e32 v67, s9, v1
	v_bcnt_u32_b32 v68, v68, 0
	s_add_i32 s15, s52, s15
	v_bcnt_u32_b32 v67, v67, v68
	v_lshl_add_u32 v67, v67, 1, s15
	ds_write_b16 v67, v212 offset:32768
.LBB0_1474:
	s_or_b64 exec, exec, s[30:31]
	s_bcnt1_i32_b64 s8, s[8:9]
	s_add_i32 s4, s4, s8
	v_cmp_gt_u32_sdwa s[8:9], v33, v66 src0_sel:WORD_0 src1_sel:DWORD
	s_and_saveexec_b64 s[30:31], s[8:9]
	s_cbranch_execz .LBB0_1476
	v_and_b32_e32 v68, s8, v100
	s_lshl_b32 s15, s4, 1
	v_and_b32_e32 v67, s9, v1
	v_bcnt_u32_b32 v68, v68, 0
	s_add_i32 s15, s52, s15
	v_bcnt_u32_b32 v67, v67, v68
	v_lshl_add_u32 v67, v67, 1, s15
	ds_write_b16 v67, v213 offset:32768
.LBB0_1476:
	s_or_b64 exec, exec, s[30:31]
	s_bcnt1_i32_b64 s8, s[8:9]
	s_add_i32 s4, s4, s8
	v_cmp_gt_u32_sdwa s[8:9], v33, v66 src0_sel:WORD_1 src1_sel:DWORD
	s_and_saveexec_b64 s[30:31], s[8:9]
	s_cbranch_execz .LBB0_1478
	v_and_b32_e32 v68, s8, v100
	s_lshl_b32 s15, s4, 1
	v_and_b32_e32 v67, s9, v1
	v_bcnt_u32_b32 v68, v68, 0
	s_add_i32 s15, s52, s15
	v_bcnt_u32_b32 v67, v67, v68
	v_lshl_add_u32 v67, v67, 1, s15
	ds_write_b16 v67, v214 offset:32768

.LBB0_1479:
	v_cmp_gt_u32_sdwa s[8:9], v14, v66 src0_sel:WORD_0 src1_sel:DWORD
	s_and_saveexec_b64 s[30:31], s[8:9]
	s_cbranch_execz .LBB0_1481
	v_and_b32_e32 v68, s8, v100
	s_lshl_b32 s15, s4, 1
	v_and_b32_e32 v67, s9, v1
	v_bcnt_u32_b32 v68, v68, 0
	s_add_i32 s15, s52, s15
	v_bcnt_u32_b32 v67, v67, v68
	v_lshl_add_u32 v67, v67, 1, s15
	ds_write_b16 v67, v215 offset:32768
.LBB0_1481:
	s_or_b64 exec, exec, s[30:31]
	s_bcnt1_i32_b64 s8, s[8:9]
	s_add_i32 s4, s4, s8
	v_cmp_gt_u32_sdwa s[8:9], v14, v66 src0_sel:WORD_1 src1_sel:DWORD
	s_and_saveexec_b64 s[30:31], s[8:9]
	s_cbranch_execz .LBB0_1483
	v_and_b32_e32 v68, s8, v100
	s_lshl_b32 s15, s4, 1
	v_and_b32_e32 v67, s9, v1
	v_bcnt_u32_b32 v68, v68, 0
	s_add_i32 s15, s52, s15
	v_bcnt_u32_b32 v67, v67, v68
	v_lshl_add_u32 v67, v67, 1, s15
	ds_write_b16 v67, v216 offset:32768
.LBB0_1483:
	s_or_b64 exec, exec, s[30:31]
	s_bcnt1_i32_b64 s8, s[8:9]
	s_add_i32 s4, s4, s8
	v_cmp_gt_u32_sdwa s[8:9], v15, v66 src0_sel:WORD_0 src1_sel:DWORD
	s_and_saveexec_b64 s[30:31], s[8:9]
	s_cbranch_execz .LBB0_1485
	v_and_b32_e32 v68, s8, v100
	s_lshl_b32 s15, s4, 1
	v_and_b32_e32 v67, s9, v1
	v_bcnt_u32_b32 v68, v68, 0
	s_add_i32 s15, s52, s15
	v_bcnt_u32_b32 v67, v67, v68
	v_lshl_add_u32 v67, v67, 1, s15
	ds_write_b16 v67, v217 offset:32768
.LBB0_1485:
	s_or_b64 exec, exec, s[30:31]
	s_bcnt1_i32_b64 s8, s[8:9]
	s_add_i32 s4, s4, s8
	v_cmp_gt_u32_sdwa s[8:9], v15, v66 src0_sel:WORD_1 src1_sel:DWORD
	s_and_saveexec_b64 s[30:31], s[8:9]
	s_cbranch_execz .LBB0_1487
	v_and_b32_e32 v68, s8, v100
	s_lshl_b32 s15, s4, 1
	v_and_b32_e32 v67, s9, v1
	v_bcnt_u32_b32 v68, v68, 0
	s_add_i32 s15, s52, s15
	v_bcnt_u32_b32 v67, v67, v68
	v_lshl_add_u32 v67, v67, 1, s15
	ds_write_b16 v67, v218 offset:32768
.LBB0_1487:
	s_or_b64 exec, exec, s[30:31]
	s_bcnt1_i32_b64 s8, s[8:9]
	s_add_i32 s4, s4, s8
	v_cmp_gt_u32_sdwa s[8:9], v16, v66 src0_sel:WORD_0 src1_sel:DWORD
	s_and_saveexec_b64 s[30:31], s[8:9]
	s_cbranch_execz .LBB0_1489
	v_and_b32_e32 v68, s8, v100
	s_lshl_b32 s15, s4, 1
	v_and_b32_e32 v67, s9, v1
	v_bcnt_u32_b32 v68, v68, 0
	s_add_i32 s15, s52, s15
	v_bcnt_u32_b32 v67, v67, v68
	v_lshl_add_u32 v67, v67, 1, s15
	ds_write_b16 v67, v219 offset:32768
.LBB0_1489:
	s_or_b64 exec, exec, s[30:31]
	s_bcnt1_i32_b64 s8, s[8:9]
	s_add_i32 s4, s4, s8
	v_cmp_gt_u32_sdwa s[8:9], v16, v66 src0_sel:WORD_1 src1_sel:DWORD
	s_and_saveexec_b64 s[30:31], s[8:9]
	s_cbranch_execz .LBB0_1491
	v_and_b32_e32 v68, s8, v100
	s_lshl_b32 s15, s4, 1
	v_and_b32_e32 v67, s9, v1
	v_bcnt_u32_b32 v68, v68, 0
	s_add_i32 s15, s52, s15
	v_bcnt_u32_b32 v67, v67, v68
	v_lshl_add_u32 v67, v67, 1, s15
	ds_write_b16 v67, v220 offset:32768
.LBB0_1491:
	s_or_b64 exec, exec, s[30:31]
	s_bcnt1_i32_b64 s8, s[8:9]
	s_add_i32 s4, s4, s8
	v_cmp_gt_u32_sdwa s[8:9], v17, v66 src0_sel:WORD_0 src1_sel:DWORD
	s_and_saveexec_b64 s[30:31], s[8:9]
	s_cbranch_execz .LBB0_1493
	v_and_b32_e32 v68, s8, v100
	s_lshl_b32 s15, s4, 1
	v_and_b32_e32 v67, s9, v1
	v_bcnt_u32_b32 v68, v68, 0
	s_add_i32 s15, s52, s15
	v_bcnt_u32_b32 v67, v67, v68
	v_lshl_add_u32 v67, v67, 1, s15
	ds_write_b16 v67, v221 offset:32768
.LBB0_1493:
	s_or_b64 exec, exec, s[30:31]
	s_bcnt1_i32_b64 s8, s[8:9]
	s_add_i32 s4, s4, s8
	v_cmp_gt_u32_sdwa s[8:9], v17, v66 src0_sel:WORD_1 src1_sel:DWORD
	s_and_saveexec_b64 s[30:31], s[8:9]
	s_cbranch_execz .LBB0_1495
	v_and_b32_e32 v68, s8, v100
	s_lshl_b32 s15, s4, 1
	v_and_b32_e32 v67, s9, v1
	v_bcnt_u32_b32 v68, v68, 0
	s_add_i32 s15, s52, s15
	v_bcnt_u32_b32 v67, v67, v68
	v_lshl_add_u32 v67, v67, 1, s15
	ds_write_b16 v67, v222 offset:32768

.LBB0_1496:
	v_cmp_gt_u32_sdwa s[8:9], v10, v66 src0_sel:WORD_0 src1_sel:DWORD
	s_and_saveexec_b64 s[30:31], s[8:9]
	s_cbranch_execz .LBB0_1498
	v_and_b32_e32 v68, s8, v100
	s_lshl_b32 s15, s4, 1
	v_and_b32_e32 v67, s9, v1
	v_bcnt_u32_b32 v68, v68, 0
	s_add_i32 s15, s52, s15
	v_bcnt_u32_b32 v67, v67, v68
	v_lshl_add_u32 v67, v67, 1, s15
	ds_write_b16 v67, v223 offset:32768
.LBB0_1498:
	s_or_b64 exec, exec, s[30:31]
	s_bcnt1_i32_b64 s8, s[8:9]
	s_add_i32 s4, s4, s8
	v_cmp_gt_u32_sdwa s[8:9], v10, v66 src0_sel:WORD_1 src1_sel:DWORD
	s_and_saveexec_b64 s[30:31], s[8:9]
	s_cbranch_execz .LBB0_1500
	v_and_b32_e32 v68, s8, v100
	s_lshl_b32 s15, s4, 1
	v_and_b32_e32 v67, s9, v1
	v_bcnt_u32_b32 v68, v68, 0
	s_add_i32 s15, s52, s15
	v_bcnt_u32_b32 v67, v67, v68
	v_lshl_add_u32 v67, v67, 1, s15
	ds_write_b16 v67, v224 offset:32768
.LBB0_1500:
	s_or_b64 exec, exec, s[30:31]
	s_bcnt1_i32_b64 s8, s[8:9]
	s_add_i32 s4, s4, s8
	v_cmp_gt_u32_sdwa s[8:9], v11, v66 src0_sel:WORD_0 src1_sel:DWORD
	s_and_saveexec_b64 s[30:31], s[8:9]
	s_cbranch_execz .LBB0_1502
	v_and_b32_e32 v68, s8, v100
	s_lshl_b32 s15, s4, 1
	v_and_b32_e32 v67, s9, v1
	v_bcnt_u32_b32 v68, v68, 0
	s_add_i32 s15, s52, s15
	v_bcnt_u32_b32 v67, v67, v68
	v_lshl_add_u32 v67, v67, 1, s15
	ds_write_b16 v67, v225 offset:32768
.LBB0_1502:
	s_or_b64 exec, exec, s[30:31]
	s_bcnt1_i32_b64 s8, s[8:9]
	s_add_i32 s4, s4, s8
	v_cmp_gt_u32_sdwa s[8:9], v11, v66 src0_sel:WORD_1 src1_sel:DWORD
	s_and_saveexec_b64 s[30:31], s[8:9]
	s_cbranch_execz .LBB0_1504
	v_and_b32_e32 v68, s8, v100
	s_lshl_b32 s15, s4, 1
	v_and_b32_e32 v67, s9, v1
	v_bcnt_u32_b32 v68, v68, 0
	s_add_i32 s15, s52, s15
	v_bcnt_u32_b32 v67, v67, v68
	v_lshl_add_u32 v67, v67, 1, s15
	ds_write_b16 v67, v226 offset:32768
.LBB0_1504:
	s_or_b64 exec, exec, s[30:31]
	s_bcnt1_i32_b64 s8, s[8:9]
	s_add_i32 s4, s4, s8
	v_cmp_gt_u32_sdwa s[8:9], v12, v66 src0_sel:WORD_0 src1_sel:DWORD
	s_and_saveexec_b64 s[30:31], s[8:9]
	s_cbranch_execz .LBB0_1506
	v_and_b32_e32 v68, s8, v100
	s_lshl_b32 s15, s4, 1
	v_and_b32_e32 v67, s9, v1
	v_bcnt_u32_b32 v68, v68, 0
	s_add_i32 s15, s52, s15
	v_bcnt_u32_b32 v67, v67, v68
	v_lshl_add_u32 v67, v67, 1, s15
	ds_write_b16 v67, v227 offset:32768
.LBB0_1506:
	s_or_b64 exec, exec, s[30:31]
	s_bcnt1_i32_b64 s8, s[8:9]
	s_add_i32 s4, s4, s8
	v_cmp_gt_u32_sdwa s[8:9], v12, v66 src0_sel:WORD_1 src1_sel:DWORD
	s_and_saveexec_b64 s[30:31], s[8:9]
	s_cbranch_execz .LBB0_1508
	v_and_b32_e32 v68, s8, v100
	s_lshl_b32 s15, s4, 1
	v_and_b32_e32 v67, s9, v1
	v_bcnt_u32_b32 v68, v68, 0
	s_add_i32 s15, s52, s15
	v_bcnt_u32_b32 v67, v67, v68
	v_lshl_add_u32 v67, v67, 1, s15
	ds_write_b16 v67, v228 offset:32768
.LBB0_1508:
	s_or_b64 exec, exec, s[30:31]
	s_bcnt1_i32_b64 s8, s[8:9]
	s_add_i32 s4, s4, s8
	v_cmp_gt_u32_sdwa s[8:9], v13, v66 src0_sel:WORD_0 src1_sel:DWORD
	s_and_saveexec_b64 s[30:31], s[8:9]
	s_cbranch_execz .LBB0_1510
	v_and_b32_e32 v68, s8, v100
	s_lshl_b32 s15, s4, 1
	v_and_b32_e32 v67, s9, v1
	v_bcnt_u32_b32 v68, v68, 0
	s_add_i32 s15, s52, s15
	v_bcnt_u32_b32 v67, v67, v68
	v_lshl_add_u32 v67, v67, 1, s15
	ds_write_b16 v67, v229 offset:32768
.LBB0_1510:
	s_or_b64 exec, exec, s[30:31]
	s_bcnt1_i32_b64 s8, s[8:9]
	s_add_i32 s4, s4, s8
	v_cmp_gt_u32_sdwa s[8:9], v13, v66 src0_sel:WORD_1 src1_sel:DWORD
	s_and_saveexec_b64 s[30:31], s[8:9]
	s_cbranch_execz .LBB0_1512
	v_and_b32_e32 v68, s8, v100
	s_lshl_b32 s15, s4, 1
	v_and_b32_e32 v67, s9, v1
	v_bcnt_u32_b32 v68, v68, 0
	s_add_i32 s15, s52, s15
	v_bcnt_u32_b32 v67, v67, v68
	v_lshl_add_u32 v67, v67, 1, s15
	ds_write_b16 v67, v230 offset:32768

.LBB0_1513:
	v_cmp_gt_u32_sdwa s[8:9], v6, v66 src0_sel:WORD_0 src1_sel:DWORD
	s_and_saveexec_b64 s[30:31], s[8:9]
	s_cbranch_execz .LBB0_1515
	v_and_b32_e32 v68, s8, v100
	s_lshl_b32 s15, s4, 1
	v_and_b32_e32 v67, s9, v1
	v_bcnt_u32_b32 v68, v68, 0
	s_add_i32 s15, s52, s15
	v_bcnt_u32_b32 v67, v67, v68
	v_lshl_add_u32 v67, v67, 1, s15
	ds_write_b16 v67, v231 offset:32768
.LBB0_1515:
	s_or_b64 exec, exec, s[30:31]
	s_bcnt1_i32_b64 s8, s[8:9]
	s_add_i32 s4, s4, s8
	v_cmp_gt_u32_sdwa s[8:9], v6, v66 src0_sel:WORD_1 src1_sel:DWORD
	s_and_saveexec_b64 s[30:31], s[8:9]
	s_cbranch_execz .LBB0_1517
	v_and_b32_e32 v68, s8, v100
	s_lshl_b32 s15, s4, 1
	v_and_b32_e32 v67, s9, v1
	v_bcnt_u32_b32 v68, v68, 0
	s_add_i32 s15, s52, s15
	v_bcnt_u32_b32 v67, v67, v68
	v_lshl_add_u32 v67, v67, 1, s15
	ds_write_b16 v67, v232 offset:32768
.LBB0_1517:
	s_or_b64 exec, exec, s[30:31]
	s_bcnt1_i32_b64 s8, s[8:9]
	s_add_i32 s4, s4, s8
	v_cmp_gt_u32_sdwa s[8:9], v7, v66 src0_sel:WORD_0 src1_sel:DWORD
	s_and_saveexec_b64 s[30:31], s[8:9]
	s_cbranch_execz .LBB0_1519
	v_and_b32_e32 v68, s8, v100
	s_lshl_b32 s15, s4, 1
	v_and_b32_e32 v67, s9, v1
	v_bcnt_u32_b32 v68, v68, 0
	s_add_i32 s15, s52, s15
	v_bcnt_u32_b32 v67, v67, v68
	v_lshl_add_u32 v67, v67, 1, s15
	ds_write_b16 v67, v233 offset:32768
.LBB0_1519:
	s_or_b64 exec, exec, s[30:31]
	s_bcnt1_i32_b64 s8, s[8:9]
	s_add_i32 s4, s4, s8
	v_cmp_gt_u32_sdwa s[8:9], v7, v66 src0_sel:WORD_1 src1_sel:DWORD
	s_and_saveexec_b64 s[30:31], s[8:9]
	s_cbranch_execz .LBB0_1521
	v_and_b32_e32 v68, s8, v100
	s_lshl_b32 s15, s4, 1
	v_and_b32_e32 v67, s9, v1
	v_bcnt_u32_b32 v68, v68, 0
	s_add_i32 s15, s52, s15
	v_bcnt_u32_b32 v67, v67, v68
	v_lshl_add_u32 v67, v67, 1, s15
	ds_write_b16 v67, v234 offset:32768
.LBB0_1521:
	s_or_b64 exec, exec, s[30:31]
	s_bcnt1_i32_b64 s8, s[8:9]
	s_add_i32 s4, s4, s8
	v_cmp_gt_u32_sdwa s[8:9], v8, v66 src0_sel:WORD_0 src1_sel:DWORD
	s_and_saveexec_b64 s[30:31], s[8:9]
	s_cbranch_execz .LBB0_1523
	v_and_b32_e32 v68, s8, v100
	s_lshl_b32 s15, s4, 1
	v_and_b32_e32 v67, s9, v1
	v_bcnt_u32_b32 v68, v68, 0
	s_add_i32 s15, s52, s15
	v_bcnt_u32_b32 v67, v67, v68
	v_lshl_add_u32 v67, v67, 1, s15
	ds_write_b16 v67, v235 offset:32768
.LBB0_1523:
	s_or_b64 exec, exec, s[30:31]
	s_bcnt1_i32_b64 s8, s[8:9]
	s_add_i32 s4, s4, s8
	v_cmp_gt_u32_sdwa s[8:9], v8, v66 src0_sel:WORD_1 src1_sel:DWORD
	s_and_saveexec_b64 s[30:31], s[8:9]
	s_cbranch_execz .LBB0_1525
	v_and_b32_e32 v68, s8, v100
	s_lshl_b32 s15, s4, 1
	v_and_b32_e32 v67, s9, v1
	v_bcnt_u32_b32 v68, v68, 0
	s_add_i32 s15, s52, s15
	v_bcnt_u32_b32 v67, v67, v68
	v_lshl_add_u32 v67, v67, 1, s15
	ds_write_b16 v67, v236 offset:32768
.LBB0_1525:
	s_or_b64 exec, exec, s[30:31]
	s_bcnt1_i32_b64 s8, s[8:9]
	s_add_i32 s4, s4, s8
	v_cmp_gt_u32_sdwa s[8:9], v9, v66 src0_sel:WORD_0 src1_sel:DWORD
	s_and_saveexec_b64 s[30:31], s[8:9]
	s_cbranch_execz .LBB0_1527
	v_and_b32_e32 v68, s8, v100
	s_lshl_b32 s15, s4, 1
	v_and_b32_e32 v67, s9, v1
	v_bcnt_u32_b32 v68, v68, 0
	s_add_i32 s15, s52, s15
	v_bcnt_u32_b32 v67, v67, v68
	v_lshl_add_u32 v67, v67, 1, s15
	ds_write_b16 v67, v237 offset:32768
.LBB0_1527:
	s_or_b64 exec, exec, s[30:31]
	s_bcnt1_i32_b64 s8, s[8:9]
	s_add_i32 s4, s4, s8
	v_cmp_gt_u32_sdwa s[8:9], v9, v66 src0_sel:WORD_1 src1_sel:DWORD
	s_and_saveexec_b64 s[30:31], s[8:9]
	s_cbranch_execz .LBB0_1529
	v_and_b32_e32 v68, s8, v100
	s_lshl_b32 s15, s4, 1
	v_and_b32_e32 v67, s9, v1
	v_bcnt_u32_b32 v68, v68, 0
	s_add_i32 s15, s52, s15
	v_bcnt_u32_b32 v67, v67, v68
	v_lshl_add_u32 v67, v67, 1, s15
	ds_write_b16 v67, v238 offset:32768

.LBB0_1530:
	v_cmp_gt_u32_sdwa s[8:9], v2, v66 src0_sel:WORD_0 src1_sel:DWORD
	s_and_saveexec_b64 vcc, s[8:9]
	s_cbranch_execz .LBB0_1532
	v_and_b32_e32 v68, s8, v100
	s_lshl_b32 s14, s4, 1
	v_and_b32_e32 v67, s9, v1
	v_bcnt_u32_b32 v68, v68, 0
	s_add_i32 s14, s52, s14
	v_bcnt_u32_b32 v67, v67, v68
	v_lshl_add_u32 v67, v67, 1, s14
	ds_write_b16 v67, v239 offset:32768
.LBB0_1532:
	s_or_b64 exec, exec, vcc
	s_bcnt1_i32_b64 s8, s[8:9]
	s_add_i32 s4, s4, s8
	v_cmp_gt_u32_sdwa s[8:9], v2, v66 src0_sel:WORD_1 src1_sel:DWORD
	s_and_saveexec_b64 vcc, s[8:9]
	s_cbranch_execz .LBB0_1534
	v_and_b32_e32 v68, s8, v100
	s_lshl_b32 s14, s4, 1
	v_and_b32_e32 v67, s9, v1
	v_bcnt_u32_b32 v68, v68, 0
	s_add_i32 s14, s52, s14
	v_bcnt_u32_b32 v67, v67, v68
	v_lshl_add_u32 v67, v67, 1, s14
	ds_write_b16 v67, v240 offset:32768
.LBB0_1534:
	s_or_b64 exec, exec, vcc
	s_bcnt1_i32_b64 s8, s[8:9]
	s_add_i32 s4, s4, s8
	v_cmp_gt_u32_sdwa s[8:9], v3, v66 src0_sel:WORD_0 src1_sel:DWORD
	s_and_saveexec_b64 vcc, s[8:9]
	s_cbranch_execz .LBB0_1536
	v_and_b32_e32 v68, s8, v100
	s_lshl_b32 s14, s4, 1
	v_and_b32_e32 v67, s9, v1
	v_bcnt_u32_b32 v68, v68, 0
	s_add_i32 s14, s52, s14
	v_bcnt_u32_b32 v67, v67, v68
	v_lshl_add_u32 v67, v67, 1, s14
	ds_write_b16 v67, v241 offset:32768
.LBB0_1536:
	s_or_b64 exec, exec, vcc
	s_bcnt1_i32_b64 s8, s[8:9]
	s_add_i32 s4, s4, s8
	v_cmp_gt_u32_sdwa s[8:9], v3, v66 src0_sel:WORD_1 src1_sel:DWORD
	s_and_saveexec_b64 vcc, s[8:9]
	s_cbranch_execz .LBB0_1538
	v_and_b32_e32 v68, s8, v100
	s_lshl_b32 s14, s4, 1
	v_and_b32_e32 v67, s9, v1
	v_bcnt_u32_b32 v68, v68, 0
	s_add_i32 s14, s52, s14
	v_bcnt_u32_b32 v67, v67, v68
	v_lshl_add_u32 v67, v67, 1, s14
	ds_write_b16 v67, v242 offset:32768
.LBB0_1538:
	s_or_b64 exec, exec, vcc
	s_bcnt1_i32_b64 s8, s[8:9]
	s_add_i32 s4, s4, s8
	v_cmp_gt_u32_sdwa s[8:9], v4, v66 src0_sel:WORD_0 src1_sel:DWORD
	s_and_saveexec_b64 vcc, s[8:9]
	s_cbranch_execz .LBB0_1540
	v_and_b32_e32 v68, s8, v100
	s_lshl_b32 s14, s4, 1
	v_and_b32_e32 v67, s9, v1
	v_bcnt_u32_b32 v68, v68, 0
	s_add_i32 s14, s52, s14
	v_bcnt_u32_b32 v67, v67, v68
	v_lshl_add_u32 v67, v67, 1, s14
	ds_write_b16 v67, v243 offset:32768
.LBB0_1540:
	s_or_b64 exec, exec, vcc
	s_bcnt1_i32_b64 s8, s[8:9]
	s_add_i32 s4, s4, s8
	v_cmp_gt_u32_sdwa s[8:9], v4, v66 src0_sel:WORD_1 src1_sel:DWORD
	s_and_saveexec_b64 vcc, s[8:9]
	s_cbranch_execz .LBB0_1542
	v_and_b32_e32 v68, s8, v100
	s_lshl_b32 s14, s4, 1
	v_and_b32_e32 v67, s9, v1
	v_bcnt_u32_b32 v68, v68, 0
	s_add_i32 s14, s52, s14
	v_bcnt_u32_b32 v67, v67, v68
	v_lshl_add_u32 v67, v67, 1, s14
	ds_write_b16 v67, v244 offset:32768
.LBB0_1542:
	s_or_b64 exec, exec, vcc
	s_bcnt1_i32_b64 s8, s[8:9]
	s_add_i32 s4, s4, s8
	v_cmp_gt_u32_sdwa s[8:9], v5, v66 src0_sel:WORD_0 src1_sel:DWORD
	s_and_saveexec_b64 vcc, s[8:9]
	s_cbranch_execz .LBB0_1544
	v_and_b32_e32 v68, s8, v100
	s_lshl_b32 s14, s4, 1
	v_and_b32_e32 v67, s9, v1
	v_bcnt_u32_b32 v68, v68, 0
	s_add_i32 s14, s52, s14
	v_bcnt_u32_b32 v67, v67, v68
	v_lshl_add_u32 v67, v67, 1, s14
	ds_write_b16 v67, v245 offset:32768
.LBB0_1544:
	s_or_b64 exec, exec, vcc
	s_bcnt1_i32_b64 s8, s[8:9]
	s_add_i32 s4, s4, s8
	v_cmp_gt_u32_sdwa s[8:9], v5, v66 src0_sel:WORD_1 src1_sel:DWORD
	s_and_saveexec_b64 vcc, s[8:9]
	s_cbranch_execz .LBB0_1546
	v_and_b32_e32 v68, s8, v100
	s_lshl_b32 s14, s4, 1
	v_and_b32_e32 v67, s9, v1
	v_bcnt_u32_b32 v68, v68, 0
	s_add_i32 s14, s52, s14
	v_bcnt_u32_b32 v67, v67, v68
	v_lshl_add_u32 v67, v67, 1, s14
	ds_write_b16 v67, v246 offset:32768

.LBB0_1547:
	s_sub_i32 s14, 0x100, s4
	s_cmpk_lt_u32 s4, 0x100
	s_cselect_b64 s[8:9], -1, 0
	v_lshlrev_b32_e32 v67, 16, v66
	s_and_b64 s[8:9], s[42:43], s[8:9]
	s_andn2_b64 vcc, exec, s[8:9]
	v_or_b32_e32 v67, v67, v66
	s_cbranch_vccnz .LBB0_1566
	v_xor_b32_e32 v68, v67, v50
	v_bitop3_b32 v69, v67, s51, v50 bitop3:0x48
	v_cmp_eq_u32_e32 vcc, 0, v69
	v_cmp_gt_u32_e64 s[8:9], s49, v68
	v_xor_b32_e32 v68, v67, v51
	v_bitop3_b32 v69, v67, s51, v51 bitop3:0x48
	s_or_b64 s[42:43], s[8:9], vcc
	v_cmp_eq_u32_e32 vcc, 0, v69
	v_cmp_gt_u32_e64 s[8:9], s49, v68
	s_or_b64 s[8:9], s[8:9], vcc
	v_xor_b32_e32 v68, v67, v52
	v_bitop3_b32 v69, v67, s51, v52 bitop3:0x48
	s_or_b64 s[42:43], s[42:43], s[8:9]
	v_cmp_eq_u32_e32 vcc, 0, v69
	v_cmp_gt_u32_e64 s[8:9], s49, v68
	s_or_b64 s[8:9], s[8:9], vcc
	v_xor_b32_e32 v68, v67, v53
	v_bitop3_b32 v69, v67, s51, v53 bitop3:0x48
	s_or_b64 s[42:43], s[8:9], s[42:43]
	v_cmp_eq_u32_e32 vcc, 0, v69
	v_cmp_gt_u32_e64 s[8:9], s49, v68
	s_or_b64 s[8:9], s[8:9], vcc
	s_or_b64 vcc, s[8:9], s[42:43]
	s_cbranch_vccz .LBB0_1566
	v_cmp_eq_u32_sdwa s[8:9], v50, v66 src0_sel:WORD_0 src1_sel:DWORD
	s_nop 1
	v_and_b32_e32 v69, s8, v100
	v_and_b32_e32 v68, s9, v1
	v_bcnt_u32_b32 v69, v69, 0
	v_bcnt_u32_b32 v68, v68, v69
	v_cmp_gt_i32_e32 vcc, s14, v68
	s_and_b64 vcc, s[8:9], vcc
	s_and_saveexec_b64 s[42:43], vcc
	s_lshl_b32 s15, s4, 1
	s_add_i32 s15, s52, s15
	v_lshl_add_u32 v68, v68, 1, s15
	ds_write_b16 v68, v119 offset:32768
	s_or_b64 exec, exec, s[42:43]
	s_bcnt1_i32_b64 s8, s[8:9]
	s_min_i32 s8, s8, s14
	s_add_i32 s4, s8, s4
	s_sub_i32 s14, s14, s8
	v_cmp_eq_u32_sdwa s[8:9], v50, v66 src0_sel:WORD_1 src1_sel:DWORD
	s_nop 1
	v_and_b32_e32 v68, s8, v100
	v_and_b32_e32 v50, s9, v1
	v_bcnt_u32_b32 v68, v68, 0
	v_bcnt_u32_b32 v50, v50, v68
	v_cmp_gt_i32_e32 vcc, s14, v50
	s_and_b64 vcc, s[8:9], vcc
	s_and_saveexec_b64 s[42:43], vcc
	s_lshl_b32 s15, s4, 1
	s_add_i32 s15, s52, s15
	v_lshl_add_u32 v50, v50, 1, s15
	ds_write_b16 v50, v120 offset:32768
	s_or_b64 exec, exec, s[42:43]
	s_bcnt1_i32_b64 s8, s[8:9]
	s_min_i32 s8, s8, s14
	s_add_i32 s4, s8, s4
	s_sub_i32 s14, s14, s8
	v_cmp_eq_u32_sdwa s[8:9], v51, v66 src0_sel:WORD_0 src1_sel:DWORD
	s_nop 1
	v_and_b32_e32 v68, s8, v100
	v_and_b32_e32 v50, s9, v1
	v_bcnt_u32_b32 v68, v68, 0
	v_bcnt_u32_b32 v50, v50, v68
	v_cmp_gt_i32_e32 vcc, s14, v50
	s_and_b64 vcc, s[8:9], vcc
	s_and_saveexec_b64 s[42:43], vcc
	s_lshl_b32 s15, s4, 1
	s_add_i32 s15, s52, s15
	v_lshl_add_u32 v50, v50, 1, s15
	ds_write_b16 v50, v121 offset:32768
	s_or_b64 exec, exec, s[42:43]
	s_bcnt1_i32_b64 s8, s[8:9]
	s_min_i32 s8, s8, s14
	s_add_i32 s4, s8, s4
	s_sub_i32 s14, s14, s8
	v_cmp_eq_u32_sdwa s[8:9], v51, v66 src0_sel:WORD_1 src1_sel:DWORD
	s_nop 1
	v_and_b32_e32 v51, s8, v100
	v_and_b32_e32 v50, s9, v1
	v_bcnt_u32_b32 v51, v51, 0
	v_bcnt_u32_b32 v50, v50, v51
	v_cmp_gt_i32_e32 vcc, s14, v50
	s_and_b64 vcc, s[8:9], vcc
	s_and_saveexec_b64 s[42:43], vcc
	s_lshl_b32 s15, s4, 1
	s_add_i32 s15, s52, s15
	v_lshl_add_u32 v50, v50, 1, s15
	ds_write_b16 v50, v122 offset:32768
	s_or_b64 exec, exec, s[42:43]
	s_bcnt1_i32_b64 s8, s[8:9]
	s_min_i32 s8, s8, s14
	s_add_i32 s4, s8, s4
	s_sub_i32 s14, s14, s8
	v_cmp_eq_u32_sdwa s[8:9], v52, v66 src0_sel:WORD_0 src1_sel:DWORD
	s_nop 1
	v_and_b32_e32 v51, s8, v100
	v_and_b32_e32 v50, s9, v1
	v_bcnt_u32_b32 v51, v51, 0
	v_bcnt_u32_b32 v50, v50, v51
	v_cmp_gt_i32_e32 vcc, s14, v50
	s_and_b64 vcc, s[8:9], vcc
	s_and_saveexec_b64 s[42:43], vcc
	s_lshl_b32 s15, s4, 1
	s_add_i32 s15, s52, s15
	v_lshl_add_u32 v50, v50, 1, s15
	ds_write_b16 v50, v123 offset:32768
	s_or_b64 exec, exec, s[42:43]
	s_bcnt1_i32_b64 s8, s[8:9]
	s_min_i32 s8, s8, s14
	s_add_i32 s4, s8, s4
	s_sub_i32 s14, s14, s8
	v_cmp_eq_u32_sdwa s[8:9], v52, v66 src0_sel:WORD_1 src1_sel:DWORD
	s_nop 1
	v_and_b32_e32 v51, s8, v100
	v_and_b32_e32 v50, s9, v1
	v_bcnt_u32_b32 v51, v51, 0
	v_bcnt_u32_b32 v50, v50, v51
	v_cmp_gt_i32_e32 vcc, s14, v50
	s_and_b64 vcc, s[8:9], vcc
	s_and_saveexec_b64 s[42:43], vcc
	s_lshl_b32 s15, s4, 1
	s_add_i32 s15, s52, s15
	v_lshl_add_u32 v50, v50, 1, s15
	ds_write_b16 v50, v124 offset:32768
	s_or_b64 exec, exec, s[42:43]
	s_bcnt1_i32_b64 s8, s[8:9]
	s_min_i32 s8, s8, s14
	s_add_i32 s4, s8, s4
	s_sub_i32 s14, s14, s8
	v_cmp_eq_u32_sdwa s[8:9], v53, v66 src0_sel:WORD_0 src1_sel:DWORD
	s_nop 1
	v_and_b32_e32 v51, s8, v100
	v_and_b32_e32 v50, s9, v1
	v_bcnt_u32_b32 v51, v51, 0
	v_bcnt_u32_b32 v50, v50, v51
	v_cmp_gt_i32_e32 vcc, s14, v50
	s_and_b64 vcc, s[8:9], vcc
	s_and_saveexec_b64 s[42:43], vcc
	s_lshl_b32 s15, s4, 1
	s_add_i32 s15, s52, s15
	v_lshl_add_u32 v50, v50, 1, s15
	ds_write_b16 v50, v125 offset:32768
	s_or_b64 exec, exec, s[42:43]
	s_bcnt1_i32_b64 s8, s[8:9]
	s_min_i32 s8, s8, s14
	s_add_i32 s4, s8, s4
	s_sub_i32 s14, s14, s8
	v_cmp_eq_u32_sdwa s[8:9], v53, v66 src0_sel:WORD_1 src1_sel:DWORD
	s_nop 1
	v_and_b32_e32 v51, s8, v100
	v_and_b32_e32 v50, s9, v1
	v_bcnt_u32_b32 v51, v51, 0
	v_bcnt_u32_b32 v50, v50, v51
	v_cmp_gt_i32_e32 vcc, s14, v50
	s_and_b64 vcc, s[8:9], vcc
	s_and_saveexec_b64 s[42:43], vcc
	s_lshl_b32 s15, s4, 1
	s_add_i32 s15, s52, s15
	v_lshl_add_u32 v50, v50, 1, s15
	ds_write_b16 v50, v126 offset:32768
	s_or_b64 exec, exec, s[42:43]
	s_bcnt1_i32_b64 s8, s[8:9]
	s_min_i32 s8, s8, s14
	s_add_i32 s4, s8, s4
	s_sub_i32 s14, s14, s8

.LBB0_1623:
	s_cmp_gt_i32 s14, 0
	s_cselect_b64 s[8:9], -1, 0
	s_and_b64 s[8:9], s[28:29], s[8:9]
	s_andn2_b64 vcc, exec, s[8:9]
	s_cbranch_vccnz .LBB0_1642
	v_xor_b32_e32 v18, v67, v58
	v_bitop3_b32 v19, v67, s51, v58 bitop3:0x48
	v_cmp_eq_u32_e32 vcc, 0, v19
	v_cmp_gt_u32_e64 s[8:9], s49, v18
	v_xor_b32_e32 v18, v67, v59
	v_bitop3_b32 v19, v67, s51, v59 bitop3:0x48
	s_or_b64 s[28:29], s[8:9], vcc
	v_cmp_eq_u32_e32 vcc, 0, v19
	v_cmp_gt_u32_e64 s[8:9], s49, v18
	s_or_b64 s[8:9], s[8:9], vcc
	v_xor_b32_e32 v18, v67, v60
	v_bitop3_b32 v19, v67, s51, v60 bitop3:0x48
	s_or_b64 s[28:29], s[28:29], s[8:9]
	v_cmp_eq_u32_e32 vcc, 0, v19
	v_cmp_gt_u32_e64 s[8:9], s49, v18
	s_or_b64 s[8:9], s[8:9], vcc
	v_xor_b32_e32 v18, v67, v61
	v_bitop3_b32 v19, v67, s51, v61 bitop3:0x48
	s_or_b64 s[28:29], s[8:9], s[28:29]
	v_cmp_eq_u32_e32 vcc, 0, v19
	v_cmp_gt_u32_e64 s[8:9], s49, v18
	s_or_b64 s[8:9], s[8:9], vcc
	s_or_b64 vcc, s[8:9], s[28:29]
	s_cbranch_vccz .LBB0_1642
	v_cmp_eq_u32_sdwa s[8:9], v58, v66 src0_sel:WORD_0 src1_sel:DWORD
	s_nop 1
	v_and_b32_e32 v19, s8, v100
	v_and_b32_e32 v18, s9, v1
	v_bcnt_u32_b32 v19, v19, 0
	v_bcnt_u32_b32 v18, v18, v19
	v_cmp_gt_u32_e32 vcc, s14, v18
	s_and_b64 s[42:43], s[8:9], vcc
	s_and_saveexec_b64 s[28:29], s[42:43]
	s_lshl_b32 s15, s4, 1
	s_add_i32 s15, s52, s15
	v_lshl_add_u32 v18, v18, 1, s15
	v_or_b32_e32 v19, 0x800, v119
	ds_write_b16 v18, v19 offset:32768
	s_or_b64 exec, exec, s[28:29]
	s_bcnt1_i32_b64 s8, s[8:9]
	s_min_u32 s8, s8, s14
	s_add_i32 s4, s8, s4
	s_sub_i32 s14, s14, s8
	v_cmp_eq_u32_sdwa s[8:9], v58, v66 src0_sel:WORD_1 src1_sel:DWORD
	s_nop 1
	v_and_b32_e32 v19, s8, v100
	v_and_b32_e32 v18, s9, v1
	v_bcnt_u32_b32 v19, v19, 0
	v_bcnt_u32_b32 v18, v18, v19
	v_cmp_gt_i32_e32 vcc, s14, v18
	s_and_b64 s[42:43], s[8:9], vcc
	s_and_saveexec_b64 s[28:29], s[42:43]
	s_lshl_b32 s15, s4, 1
	s_add_i32 s15, s52, s15
	v_lshl_add_u32 v18, v18, 1, s15
	ds_write_b16 v18, v152 offset:32768
	s_or_b64 exec, exec, s[28:29]
	s_bcnt1_i32_b64 s8, s[8:9]
	s_min_i32 s8, s8, s14
	s_add_i32 s4, s8, s4
	s_sub_i32 s14, s14, s8
	v_cmp_eq_u32_sdwa s[8:9], v59, v66 src0_sel:WORD_0 src1_sel:DWORD
	s_nop 1
	v_and_b32_e32 v19, s8, v100
	v_and_b32_e32 v18, s9, v1
	v_bcnt_u32_b32 v19, v19, 0
	v_bcnt_u32_b32 v18, v18, v19
	v_cmp_gt_i32_e32 vcc, s14, v18
	s_and_b64 s[42:43], s[8:9], vcc
	s_and_saveexec_b64 s[28:29], s[42:43]
	s_lshl_b32 s15, s4, 1
	s_add_i32 s15, s52, s15
	v_lshl_add_u32 v18, v18, 1, s15
	ds_write_b16 v18, v153 offset:32768
	s_or_b64 exec, exec, s[28:29]
	s_bcnt1_i32_b64 s8, s[8:9]
	s_min_i32 s8, s8, s14
	s_add_i32 s4, s8, s4
	s_sub_i32 s14, s14, s8
	v_cmp_eq_u32_sdwa s[8:9], v59, v66 src0_sel:WORD_1 src1_sel:DWORD
	s_nop 1
	v_and_b32_e32 v19, s8, v100
	v_and_b32_e32 v18, s9, v1
	v_bcnt_u32_b32 v19, v19, 0
	v_bcnt_u32_b32 v18, v18, v19
	v_cmp_gt_i32_e32 vcc, s14, v18
	s_and_b64 s[42:43], s[8:9], vcc
	s_and_saveexec_b64 s[28:29], s[42:43]
	s_lshl_b32 s15, s4, 1
	s_add_i32 s15, s52, s15
	v_lshl_add_u32 v18, v18, 1, s15
	ds_write_b16 v18, v154 offset:32768
	s_or_b64 exec, exec, s[28:29]
	s_bcnt1_i32_b64 s8, s[8:9]
	s_min_i32 s8, s8, s14
	s_add_i32 s4, s8, s4
	s_sub_i32 s14, s14, s8
	v_cmp_eq_u32_sdwa s[8:9], v60, v66 src0_sel:WORD_0 src1_sel:DWORD
	s_nop 1
	v_and_b32_e32 v19, s8, v100
	v_and_b32_e32 v18, s9, v1
	v_bcnt_u32_b32 v19, v19, 0
	v_bcnt_u32_b32 v18, v18, v19
	v_cmp_gt_i32_e32 vcc, s14, v18
	s_and_b64 s[42:43], s[8:9], vcc
	s_and_saveexec_b64 s[28:29], s[42:43]
	s_lshl_b32 s15, s4, 1
	s_add_i32 s15, s52, s15
	v_lshl_add_u32 v18, v18, 1, s15
	ds_write_b16 v18, v155 offset:32768
	s_or_b64 exec, exec, s[28:29]
	s_bcnt1_i32_b64 s8, s[8:9]
	s_min_i32 s8, s8, s14
	s_add_i32 s4, s8, s4
	s_sub_i32 s14, s14, s8
	v_cmp_eq_u32_sdwa s[8:9], v60, v66 src0_sel:WORD_1 src1_sel:DWORD
	s_nop 1
	v_and_b32_e32 v19, s8, v100
	v_and_b32_e32 v18, s9, v1
	v_bcnt_u32_b32 v19, v19, 0
	v_bcnt_u32_b32 v18, v18, v19
	v_cmp_gt_i32_e32 vcc, s14, v18
	s_and_b64 s[42:43], s[8:9], vcc
	s_and_saveexec_b64 s[28:29], s[42:43]
	s_lshl_b32 s15, s4, 1
	s_add_i32 s15, s52, s15
	v_lshl_add_u32 v18, v18, 1, s15
	ds_write_b16 v18, v156 offset:32768
	s_or_b64 exec, exec, s[28:29]
	s_bcnt1_i32_b64 s8, s[8:9]
	s_min_i32 s8, s8, s14
	s_add_i32 s4, s8, s4
	s_sub_i32 s14, s14, s8
	v_cmp_eq_u32_sdwa s[8:9], v61, v66 src0_sel:WORD_0 src1_sel:DWORD
	s_nop 1
	v_and_b32_e32 v19, s8, v100
	v_and_b32_e32 v18, s9, v1
	v_bcnt_u32_b32 v19, v19, 0
	v_bcnt_u32_b32 v18, v18, v19
	v_cmp_gt_i32_e32 vcc, s14, v18
	s_and_b64 s[42:43], s[8:9], vcc
	s_and_saveexec_b64 s[28:29], s[42:43]
	s_lshl_b32 s15, s4, 1
	s_add_i32 s15, s52, s15
	v_lshl_add_u32 v18, v18, 1, s15
	ds_write_b16 v18, v157 offset:32768
	s_or_b64 exec, exec, s[28:29]
	s_bcnt1_i32_b64 s8, s[8:9]
	s_min_i32 s8, s8, s14
	s_add_i32 s4, s8, s4
	s_sub_i32 s14, s14, s8
	v_cmp_eq_u32_sdwa s[8:9], v61, v66 src0_sel:WORD_1 src1_sel:DWORD
	s_nop 1
	v_and_b32_e32 v19, s8, v100
	v_and_b32_e32 v18, s9, v1
	v_bcnt_u32_b32 v19, v19, 0
	v_bcnt_u32_b32 v18, v18, v19
	v_cmp_gt_i32_e32 vcc, s14, v18
	s_and_b64 s[42:43], s[8:9], vcc
	s_and_saveexec_b64 s[28:29], s[42:43]
	s_lshl_b32 s15, s4, 1
	s_add_i32 s15, s52, s15
	v_lshl_add_u32 v18, v18, 1, s15
	ds_write_b16 v18, v158 offset:32768
	s_or_b64 exec, exec, s[28:29]
	s_bcnt1_i32_b64 s8, s[8:9]
	s_min_i32 s8, s8, s14
	s_add_i32 s4, s8, s4
	s_sub_i32 s14, s14, s8
.LBB0_1642:
	s_cmp_gt_i32 s14, 0
	s_cselect_b64 s[8:9], -1, 0
	s_and_b64 s[8:9], s[66:67], s[8:9]
	s_andn2_b64 vcc, exec, s[8:9]
	s_cbranch_vccnz .LBB0_1661
	v_xor_b32_e32 v18, v67, v46
	v_bitop3_b32 v19, v67, s51, v46 bitop3:0x48
	v_cmp_eq_u32_e32 vcc, 0, v19
	v_cmp_gt_u32_e64 s[8:9], s49, v18
	v_xor_b32_e32 v18, v67, v47
	v_bitop3_b32 v19, v67, s51, v47 bitop3:0x48
	s_or_b64 s[28:29], s[8:9], vcc
	v_cmp_eq_u32_e32 vcc, 0, v19
	v_cmp_gt_u32_e64 s[8:9], s49, v18
	s_or_b64 s[8:9], s[8:9], vcc
	v_xor_b32_e32 v18, v67, v48
	v_bitop3_b32 v19, v67, s51, v48 bitop3:0x48
	s_or_b64 s[28:29], s[28:29], s[8:9]
	v_cmp_eq_u32_e32 vcc, 0, v19
	v_cmp_gt_u32_e64 s[8:9], s49, v18
	s_or_b64 s[8:9], s[8:9], vcc
	v_xor_b32_e32 v18, v67, v49
	v_bitop3_b32 v19, v67, s51, v49 bitop3:0x48
	s_or_b64 s[28:29], s[8:9], s[28:29]
	v_cmp_eq_u32_e32 vcc, 0, v19
	v_cmp_gt_u32_e64 s[8:9], s49, v18
	s_or_b64 s[8:9], s[8:9], vcc
	s_or_b64 vcc, s[8:9], s[28:29]
	s_cbranch_vccz .LBB0_1661
	v_cmp_eq_u32_sdwa s[8:9], v46, v66 src0_sel:WORD_0 src1_sel:DWORD
	s_nop 1
	v_and_b32_e32 v19, s8, v100
	v_and_b32_e32 v18, s9, v1
	v_bcnt_u32_b32 v19, v19, 0
	v_bcnt_u32_b32 v18, v18, v19
	v_cmp_gt_u32_e32 vcc, s14, v18
	s_and_b64 s[42:43], s[8:9], vcc
	s_and_saveexec_b64 s[28:29], s[42:43]
	s_lshl_b32 s15, s4, 1
	s_add_i32 s15, s52, s15
	v_lshl_add_u32 v18, v18, 1, s15
	ds_write_b16 v18, v159 offset:32768
	s_or_b64 exec, exec, s[28:29]
	s_bcnt1_i32_b64 s8, s[8:9]
	s_min_u32 s8, s8, s14
	s_add_i32 s4, s8, s4
	s_sub_i32 s14, s14, s8
	v_cmp_eq_u32_sdwa s[8:9], v46, v66 src0_sel:WORD_1 src1_sel:DWORD
	s_nop 1
	v_and_b32_e32 v19, s8, v100
	v_and_b32_e32 v18, s9, v1
	v_bcnt_u32_b32 v19, v19, 0
	v_bcnt_u32_b32 v18, v18, v19
	v_cmp_gt_i32_e32 vcc, s14, v18
	s_and_b64 s[42:43], s[8:9], vcc
	s_and_saveexec_b64 s[28:29], s[42:43]
	s_lshl_b32 s15, s4, 1
	s_add_i32 s15, s52, s15
	v_lshl_add_u32 v18, v18, 1, s15
	ds_write_b16 v18, v160 offset:32768
	s_or_b64 exec, exec, s[28:29]
	s_bcnt1_i32_b64 s8, s[8:9]
	s_min_i32 s8, s8, s14
	s_add_i32 s4, s8, s4
	s_sub_i32 s14, s14, s8
	v_cmp_eq_u32_sdwa s[8:9], v47, v66 src0_sel:WORD_0 src1_sel:DWORD
	s_nop 1
	v_and_b32_e32 v19, s8, v100
	v_and_b32_e32 v18, s9, v1
	v_bcnt_u32_b32 v19, v19, 0
	v_bcnt_u32_b32 v18, v18, v19
	v_cmp_gt_i32_e32 vcc, s14, v18
	s_and_b64 s[42:43], s[8:9], vcc
	s_and_saveexec_b64 s[28:29], s[42:43]
	s_lshl_b32 s15, s4, 1
	s_add_i32 s15, s52, s15
	v_lshl_add_u32 v18, v18, 1, s15
	ds_write_b16 v18, v161 offset:32768
	s_or_b64 exec, exec, s[28:29]
	s_bcnt1_i32_b64 s8, s[8:9]
	s_min_i32 s8, s8, s14
	s_add_i32 s4, s8, s4
	s_sub_i32 s14, s14, s8
	v_cmp_eq_u32_sdwa s[8:9], v47, v66 src0_sel:WORD_1 src1_sel:DWORD
	s_nop 1
	v_and_b32_e32 v19, s8, v100
	v_and_b32_e32 v18, s9, v1
	v_bcnt_u32_b32 v19, v19, 0
	v_bcnt_u32_b32 v18, v18, v19
	v_cmp_gt_i32_e32 vcc, s14, v18
	s_and_b64 s[42:43], s[8:9], vcc
	s_and_saveexec_b64 s[28:29], s[42:43]
	s_lshl_b32 s15, s4, 1
	s_add_i32 s15, s52, s15
	v_lshl_add_u32 v18, v18, 1, s15
	ds_write_b16 v18, v162 offset:32768
	s_or_b64 exec, exec, s[28:29]
	s_bcnt1_i32_b64 s8, s[8:9]
	s_min_i32 s8, s8, s14
	s_add_i32 s4, s8, s4
	s_sub_i32 s14, s14, s8
	v_cmp_eq_u32_sdwa s[8:9], v48, v66 src0_sel:WORD_0 src1_sel:DWORD
	s_nop 1
	v_and_b32_e32 v19, s8, v100
	v_and_b32_e32 v18, s9, v1
	v_bcnt_u32_b32 v19, v19, 0
	v_bcnt_u32_b32 v18, v18, v19
	v_cmp_gt_i32_e32 vcc, s14, v18
	s_and_b64 s[42:43], s[8:9], vcc
	s_and_saveexec_b64 s[28:29], s[42:43]
	s_lshl_b32 s15, s4, 1
	s_add_i32 s15, s52, s15
	v_lshl_add_u32 v18, v18, 1, s15
	ds_write_b16 v18, v163 offset:32768
	s_or_b64 exec, exec, s[28:29]
	s_bcnt1_i32_b64 s8, s[8:9]
	s_min_i32 s8, s8, s14
	s_add_i32 s4, s8, s4
	s_sub_i32 s14, s14, s8
	v_cmp_eq_u32_sdwa s[8:9], v48, v66 src0_sel:WORD_1 src1_sel:DWORD
	s_nop 1
	v_and_b32_e32 v19, s8, v100
	v_and_b32_e32 v18, s9, v1
	v_bcnt_u32_b32 v19, v19, 0
	v_bcnt_u32_b32 v18, v18, v19
	v_cmp_gt_i32_e32 vcc, s14, v18
	s_and_b64 s[42:43], s[8:9], vcc
	s_and_saveexec_b64 s[28:29], s[42:43]
	s_lshl_b32 s15, s4, 1
	s_add_i32 s15, s52, s15
	v_lshl_add_u32 v18, v18, 1, s15
	ds_write_b16 v18, v164 offset:32768
	s_or_b64 exec, exec, s[28:29]
	s_bcnt1_i32_b64 s8, s[8:9]
	s_min_i32 s8, s8, s14
	s_add_i32 s4, s8, s4
	s_sub_i32 s14, s14, s8
	v_cmp_eq_u32_sdwa s[8:9], v49, v66 src0_sel:WORD_0 src1_sel:DWORD
	s_nop 1
	v_and_b32_e32 v19, s8, v100
	v_and_b32_e32 v18, s9, v1
	v_bcnt_u32_b32 v19, v19, 0
	v_bcnt_u32_b32 v18, v18, v19
	v_cmp_gt_i32_e32 vcc, s14, v18
	s_and_b64 s[42:43], s[8:9], vcc
	s_and_saveexec_b64 s[28:29], s[42:43]
	s_lshl_b32 s15, s4, 1
	s_add_i32 s15, s52, s15
	v_lshl_add_u32 v18, v18, 1, s15
	ds_write_b16 v18, v165 offset:32768
	s_or_b64 exec, exec, s[28:29]
	s_bcnt1_i32_b64 s8, s[8:9]
	s_min_i32 s8, s8, s14
	s_add_i32 s4, s8, s4
	s_sub_i32 s14, s14, s8
	v_cmp_eq_u32_sdwa s[8:9], v49, v66 src0_sel:WORD_1 src1_sel:DWORD
	s_nop 1
	v_and_b32_e32 v19, s8, v100
	v_and_b32_e32 v18, s9, v1
	v_bcnt_u32_b32 v19, v19, 0
	v_bcnt_u32_b32 v18, v18, v19
	v_cmp_gt_i32_e32 vcc, s14, v18
	s_and_b64 s[42:43], s[8:9], vcc
	s_and_saveexec_b64 s[28:29], s[42:43]
	s_lshl_b32 s15, s4, 1
	s_add_i32 s15, s52, s15
	v_lshl_add_u32 v18, v18, 1, s15
	ds_write_b16 v18, v166 offset:32768
	s_or_b64 exec, exec, s[28:29]
	s_bcnt1_i32_b64 s8, s[8:9]
	s_min_i32 s8, s8, s14
	s_add_i32 s4, s8, s4
	s_sub_i32 s14, s14, s8
.LBB0_1661:
	s_cmp_gt_i32 s14, 0
	s_cselect_b64 s[8:9], -1, 0
	s_and_b64 s[8:9], s[64:65], s[8:9]
	s_andn2_b64 vcc, exec, s[8:9]
	s_cbranch_vccnz .LBB0_1680
	v_xor_b32_e32 v18, v67, v34
	v_bitop3_b32 v19, v67, s51, v34 bitop3:0x48
	v_cmp_eq_u32_e32 vcc, 0, v19
	v_cmp_gt_u32_e64 s[8:9], s49, v18
	v_xor_b32_e32 v18, v67, v35
	v_bitop3_b32 v19, v67, s51, v35 bitop3:0x48
	s_or_b64 s[28:29], s[8:9], vcc
	v_cmp_eq_u32_e32 vcc, 0, v19
	v_cmp_gt_u32_e64 s[8:9], s49, v18
	s_or_b64 s[8:9], s[8:9], vcc
	v_xor_b32_e32 v18, v67, v36
	v_bitop3_b32 v19, v67, s51, v36 bitop3:0x48
	s_or_b64 s[28:29], s[28:29], s[8:9]
	v_cmp_eq_u32_e32 vcc, 0, v19
	v_cmp_gt_u32_e64 s[8:9], s49, v18
	s_or_b64 s[8:9], s[8:9], vcc
	v_xor_b32_e32 v18, v67, v37
	v_bitop3_b32 v19, v67, s51, v37 bitop3:0x48
	s_or_b64 s[28:29], s[8:9], s[28:29]
	v_cmp_eq_u32_e32 vcc, 0, v19
	v_cmp_gt_u32_e64 s[8:9], s49, v18
	s_or_b64 s[8:9], s[8:9], vcc
	s_or_b64 vcc, s[8:9], s[28:29]
	s_cbranch_vccz .LBB0_1680
	v_cmp_eq_u32_sdwa s[8:9], v34, v66 src0_sel:WORD_0 src1_sel:DWORD
	s_nop 1
	v_and_b32_e32 v19, s8, v100
	v_and_b32_e32 v18, s9, v1
	v_bcnt_u32_b32 v19, v19, 0
	v_bcnt_u32_b32 v18, v18, v19
	v_cmp_gt_u32_e32 vcc, s14, v18
	s_and_b64 s[42:43], s[8:9], vcc
	s_and_saveexec_b64 s[28:29], s[42:43]
	s_lshl_b32 s15, s4, 1
	s_add_i32 s15, s52, s15
	v_lshl_add_u32 v18, v18, 1, s15
	ds_write_b16 v18, v167 offset:32768
	s_or_b64 exec, exec, s[28:29]
	s_bcnt1_i32_b64 s8, s[8:9]
	s_min_u32 s8, s8, s14
	s_add_i32 s4, s8, s4
	s_sub_i32 s14, s14, s8
	v_cmp_eq_u32_sdwa s[8:9], v34, v66 src0_sel:WORD_1 src1_sel:DWORD
	s_nop 1
	v_and_b32_e32 v19, s8, v100
	v_and_b32_e32 v18, s9, v1
	v_bcnt_u32_b32 v19, v19, 0
	v_bcnt_u32_b32 v18, v18, v19
	v_cmp_gt_i32_e32 vcc, s14, v18
	s_and_b64 s[42:43], s[8:9], vcc
	s_and_saveexec_b64 s[28:29], s[42:43]
	s_lshl_b32 s15, s4, 1
	s_add_i32 s15, s52, s15
	v_lshl_add_u32 v18, v18, 1, s15
	ds_write_b16 v18, v168 offset:32768
	s_or_b64 exec, exec, s[28:29]
	s_bcnt1_i32_b64 s8, s[8:9]
	s_min_i32 s8, s8, s14
	s_add_i32 s4, s8, s4
	s_sub_i32 s14, s14, s8
	v_cmp_eq_u32_sdwa s[8:9], v35, v66 src0_sel:WORD_0 src1_sel:DWORD
	s_nop 1
	v_and_b32_e32 v19, s8, v100
	v_and_b32_e32 v18, s9, v1
	v_bcnt_u32_b32 v19, v19, 0
	v_bcnt_u32_b32 v18, v18, v19
	v_cmp_gt_i32_e32 vcc, s14, v18
	s_and_b64 s[42:43], s[8:9], vcc
	s_and_saveexec_b64 s[28:29], s[42:43]
	s_lshl_b32 s15, s4, 1
	s_add_i32 s15, s52, s15
	v_lshl_add_u32 v18, v18, 1, s15
	ds_write_b16 v18, v169 offset:32768
	s_or_b64 exec, exec, s[28:29]
	s_bcnt1_i32_b64 s8, s[8:9]
	s_min_i32 s8, s8, s14
	s_add_i32 s4, s8, s4
	s_sub_i32 s14, s14, s8
	v_cmp_eq_u32_sdwa s[8:9], v35, v66 src0_sel:WORD_1 src1_sel:DWORD
	s_nop 1
	v_and_b32_e32 v19, s8, v100
	v_and_b32_e32 v18, s9, v1
	v_bcnt_u32_b32 v19, v19, 0
	v_bcnt_u32_b32 v18, v18, v19
	v_cmp_gt_i32_e32 vcc, s14, v18
	s_and_b64 s[42:43], s[8:9], vcc
	s_and_saveexec_b64 s[28:29], s[42:43]
	s_lshl_b32 s15, s4, 1
	s_add_i32 s15, s52, s15
	v_lshl_add_u32 v18, v18, 1, s15
	ds_write_b16 v18, v170 offset:32768
	s_or_b64 exec, exec, s[28:29]
	s_bcnt1_i32_b64 s8, s[8:9]
	s_min_i32 s8, s8, s14
	s_add_i32 s4, s8, s4
	s_sub_i32 s14, s14, s8
	v_cmp_eq_u32_sdwa s[8:9], v36, v66 src0_sel:WORD_0 src1_sel:DWORD
	s_nop 1
	v_and_b32_e32 v19, s8, v100
	v_and_b32_e32 v18, s9, v1
	v_bcnt_u32_b32 v19, v19, 0
	v_bcnt_u32_b32 v18, v18, v19
	v_cmp_gt_i32_e32 vcc, s14, v18
	s_and_b64 s[42:43], s[8:9], vcc
	s_and_saveexec_b64 s[28:29], s[42:43]
	s_lshl_b32 s15, s4, 1
	s_add_i32 s15, s52, s15
	v_lshl_add_u32 v18, v18, 1, s15
	ds_write_b16 v18, v171 offset:32768
	s_or_b64 exec, exec, s[28:29]
	s_bcnt1_i32_b64 s8, s[8:9]
	s_min_i32 s8, s8, s14
	s_add_i32 s4, s8, s4
	s_sub_i32 s14, s14, s8
	v_cmp_eq_u32_sdwa s[8:9], v36, v66 src0_sel:WORD_1 src1_sel:DWORD
	s_nop 1
	v_and_b32_e32 v19, s8, v100
	v_and_b32_e32 v18, s9, v1
	v_bcnt_u32_b32 v19, v19, 0
	v_bcnt_u32_b32 v18, v18, v19
	v_cmp_gt_i32_e32 vcc, s14, v18
	s_and_b64 s[42:43], s[8:9], vcc
	s_and_saveexec_b64 s[28:29], s[42:43]
	s_lshl_b32 s15, s4, 1
	s_add_i32 s15, s52, s15
	v_lshl_add_u32 v18, v18, 1, s15
	ds_write_b16 v18, v172 offset:32768
	s_or_b64 exec, exec, s[28:29]
	s_bcnt1_i32_b64 s8, s[8:9]
	s_min_i32 s8, s8, s14
	s_add_i32 s4, s8, s4
	s_sub_i32 s14, s14, s8
	v_cmp_eq_u32_sdwa s[8:9], v37, v66 src0_sel:WORD_0 src1_sel:DWORD
	s_nop 1
	v_and_b32_e32 v19, s8, v100
	v_and_b32_e32 v18, s9, v1
	v_bcnt_u32_b32 v19, v19, 0
	v_bcnt_u32_b32 v18, v18, v19
	v_cmp_gt_i32_e32 vcc, s14, v18
	s_and_b64 s[42:43], s[8:9], vcc
	s_and_saveexec_b64 s[28:29], s[42:43]
	s_lshl_b32 s15, s4, 1
	s_add_i32 s15, s52, s15
	v_lshl_add_u32 v18, v18, 1, s15
	ds_write_b16 v18, v173 offset:32768
	s_or_b64 exec, exec, s[28:29]
	s_bcnt1_i32_b64 s8, s[8:9]
	s_min_i32 s8, s8, s14
	s_add_i32 s4, s8, s4
	s_sub_i32 s14, s14, s8
	v_cmp_eq_u32_sdwa s[8:9], v37, v66 src0_sel:WORD_1 src1_sel:DWORD
	s_nop 1
	v_and_b32_e32 v19, s8, v100
	v_and_b32_e32 v18, s9, v1
	v_bcnt_u32_b32 v19, v19, 0
	v_bcnt_u32_b32 v18, v18, v19
	v_cmp_gt_i32_e32 vcc, s14, v18
	s_and_b64 s[42:43], s[8:9], vcc
	s_and_saveexec_b64 s[28:29], s[42:43]
	s_lshl_b32 s15, s4, 1
	s_add_i32 s15, s52, s15
	v_lshl_add_u32 v18, v18, 1, s15
	ds_write_b16 v18, v174 offset:32768
	s_or_b64 exec, exec, s[28:29]
	s_bcnt1_i32_b64 s8, s[8:9]
	s_min_i32 s8, s8, s14
	s_add_i32 s4, s8, s4
	s_sub_i32 s14, s14, s8
.LBB0_1680:
	s_cmp_gt_i32 s14, 0
	s_cselect_b64 s[8:9], -1, 0
	s_and_b64 s[8:9], s[58:59], s[8:9]
	s_andn2_b64 vcc, exec, s[8:9]
	s_cbranch_vccnz .LBB0_1699
	v_xor_b32_e32 v18, v67, v22
	v_bitop3_b32 v19, v67, s51, v22 bitop3:0x48
	v_cmp_eq_u32_e32 vcc, 0, v19
	v_cmp_gt_u32_e64 s[8:9], s49, v18
	v_xor_b32_e32 v18, v67, v23
	v_bitop3_b32 v19, v67, s51, v23 bitop3:0x48
	s_or_b64 s[28:29], s[8:9], vcc
	v_cmp_eq_u32_e32 vcc, 0, v19
	v_cmp_gt_u32_e64 s[8:9], s49, v18
	s_or_b64 s[8:9], s[8:9], vcc
	v_xor_b32_e32 v18, v67, v24
	v_bitop3_b32 v19, v67, s51, v24 bitop3:0x48
	s_or_b64 s[28:29], s[28:29], s[8:9]
	v_cmp_eq_u32_e32 vcc, 0, v19
	v_cmp_gt_u32_e64 s[8:9], s49, v18
	s_or_b64 s[8:9], s[8:9], vcc
	v_xor_b32_e32 v18, v67, v25
	v_bitop3_b32 v19, v67, s51, v25 bitop3:0x48
	s_or_b64 s[28:29], s[8:9], s[28:29]
	v_cmp_eq_u32_e32 vcc, 0, v19
	v_cmp_gt_u32_e64 s[8:9], s49, v18
	s_or_b64 s[8:9], s[8:9], vcc
	s_or_b64 vcc, s[8:9], s[28:29]
	s_cbranch_vccz .LBB0_1699
	v_cmp_eq_u32_sdwa s[8:9], v22, v66 src0_sel:WORD_0 src1_sel:DWORD
	s_nop 1
	v_and_b32_e32 v19, s8, v100
	v_and_b32_e32 v18, s9, v1
	v_bcnt_u32_b32 v19, v19, 0
	v_bcnt_u32_b32 v18, v18, v19
	v_cmp_gt_u32_e32 vcc, s14, v18
	s_and_b64 s[42:43], s[8:9], vcc
	s_and_saveexec_b64 s[28:29], s[42:43]
	s_lshl_b32 s15, s4, 1
	s_add_i32 s15, s52, s15
	v_lshl_add_u32 v18, v18, 1, s15
	ds_write_b16 v18, v175 offset:32768
	s_or_b64 exec, exec, s[28:29]
	s_bcnt1_i32_b64 s8, s[8:9]
	s_min_u32 s8, s8, s14
	s_add_i32 s4, s8, s4
	s_sub_i32 s14, s14, s8
	v_cmp_eq_u32_sdwa s[8:9], v22, v66 src0_sel:WORD_1 src1_sel:DWORD
	s_nop 1
	v_and_b32_e32 v19, s8, v100
	v_and_b32_e32 v18, s9, v1
	v_bcnt_u32_b32 v19, v19, 0
	v_bcnt_u32_b32 v18, v18, v19
	v_cmp_gt_i32_e32 vcc, s14, v18
	s_and_b64 s[42:43], s[8:9], vcc
	s_and_saveexec_b64 s[28:29], s[42:43]
	s_lshl_b32 s15, s4, 1
	s_add_i32 s15, s52, s15
	v_lshl_add_u32 v18, v18, 1, s15
	ds_write_b16 v18, v176 offset:32768
	s_or_b64 exec, exec, s[28:29]
	s_bcnt1_i32_b64 s8, s[8:9]
	s_min_i32 s8, s8, s14
	s_add_i32 s4, s8, s4
	s_sub_i32 s14, s14, s8
	v_cmp_eq_u32_sdwa s[8:9], v23, v66 src0_sel:WORD_0 src1_sel:DWORD
	s_nop 1
	v_and_b32_e32 v19, s8, v100
	v_and_b32_e32 v18, s9, v1
	v_bcnt_u32_b32 v19, v19, 0
	v_bcnt_u32_b32 v18, v18, v19
	v_cmp_gt_i32_e32 vcc, s14, v18
	s_and_b64 s[42:43], s[8:9], vcc
	s_and_saveexec_b64 s[28:29], s[42:43]
	s_lshl_b32 s15, s4, 1
	s_add_i32 s15, s52, s15
	v_lshl_add_u32 v18, v18, 1, s15
	ds_write_b16 v18, v177 offset:32768
	s_or_b64 exec, exec, s[28:29]
	s_bcnt1_i32_b64 s8, s[8:9]
	s_min_i32 s8, s8, s14
	s_add_i32 s4, s8, s4
	s_sub_i32 s14, s14, s8
	v_cmp_eq_u32_sdwa s[8:9], v23, v66 src0_sel:WORD_1 src1_sel:DWORD
	s_nop 1
	v_and_b32_e32 v19, s8, v100
	v_and_b32_e32 v18, s9, v1
	v_bcnt_u32_b32 v19, v19, 0
	v_bcnt_u32_b32 v18, v18, v19
	v_cmp_gt_i32_e32 vcc, s14, v18
	s_and_b64 s[42:43], s[8:9], vcc
	s_and_saveexec_b64 s[28:29], s[42:43]
	s_lshl_b32 s15, s4, 1
	s_add_i32 s15, s52, s15
	v_lshl_add_u32 v18, v18, 1, s15
	ds_write_b16 v18, v178 offset:32768
	s_or_b64 exec, exec, s[28:29]
	s_bcnt1_i32_b64 s8, s[8:9]
	s_min_i32 s8, s8, s14
	s_add_i32 s4, s8, s4
	s_sub_i32 s14, s14, s8
	v_cmp_eq_u32_sdwa s[8:9], v24, v66 src0_sel:WORD_0 src1_sel:DWORD
	s_nop 1
	v_and_b32_e32 v19, s8, v100
	v_and_b32_e32 v18, s9, v1
	v_bcnt_u32_b32 v19, v19, 0
	v_bcnt_u32_b32 v18, v18, v19
	v_cmp_gt_i32_e32 vcc, s14, v18
	s_and_b64 s[42:43], s[8:9], vcc
	s_and_saveexec_b64 s[28:29], s[42:43]
	s_lshl_b32 s15, s4, 1
	s_add_i32 s15, s52, s15
	v_lshl_add_u32 v18, v18, 1, s15
	ds_write_b16 v18, v179 offset:32768
	s_or_b64 exec, exec, s[28:29]
	s_bcnt1_i32_b64 s8, s[8:9]
	s_min_i32 s8, s8, s14
	s_add_i32 s4, s8, s4
	s_sub_i32 s14, s14, s8
	v_cmp_eq_u32_sdwa s[8:9], v24, v66 src0_sel:WORD_1 src1_sel:DWORD
	s_nop 1
	v_and_b32_e32 v19, s8, v100
	v_and_b32_e32 v18, s9, v1
	v_bcnt_u32_b32 v19, v19, 0
	v_bcnt_u32_b32 v18, v18, v19
	v_cmp_gt_i32_e32 vcc, s14, v18
	s_and_b64 s[42:43], s[8:9], vcc
	s_and_saveexec_b64 s[28:29], s[42:43]
	s_lshl_b32 s15, s4, 1
	s_add_i32 s15, s52, s15
	v_lshl_add_u32 v18, v18, 1, s15
	ds_write_b16 v18, v180 offset:32768
	s_or_b64 exec, exec, s[28:29]
	s_bcnt1_i32_b64 s8, s[8:9]
	s_min_i32 s8, s8, s14
	s_add_i32 s4, s8, s4
	s_sub_i32 s14, s14, s8
	v_cmp_eq_u32_sdwa s[8:9], v25, v66 src0_sel:WORD_0 src1_sel:DWORD
	s_nop 1
	v_and_b32_e32 v19, s8, v100
	v_and_b32_e32 v18, s9, v1
	v_bcnt_u32_b32 v19, v19, 0
	v_bcnt_u32_b32 v18, v18, v19
	v_cmp_gt_i32_e32 vcc, s14, v18
	s_and_b64 s[42:43], s[8:9], vcc
	s_and_saveexec_b64 s[28:29], s[42:43]
	s_lshl_b32 s15, s4, 1
	s_add_i32 s15, s52, s15
	v_lshl_add_u32 v18, v18, 1, s15
	ds_write_b16 v18, v181 offset:32768
	s_or_b64 exec, exec, s[28:29]
	s_bcnt1_i32_b64 s8, s[8:9]
	s_min_i32 s8, s8, s14
	s_add_i32 s4, s8, s4
	s_sub_i32 s14, s14, s8
	v_cmp_eq_u32_sdwa s[8:9], v25, v66 src0_sel:WORD_1 src1_sel:DWORD
	s_nop 1
	v_and_b32_e32 v19, s8, v100
	v_and_b32_e32 v18, s9, v1
	v_bcnt_u32_b32 v19, v19, 0
	v_bcnt_u32_b32 v18, v18, v19
	v_cmp_gt_i32_e32 vcc, s14, v18
	s_and_b64 s[42:43], s[8:9], vcc
	s_and_saveexec_b64 s[28:29], s[42:43]
	s_lshl_b32 s15, s4, 1
	s_add_i32 s15, s52, s15
	v_lshl_add_u32 v18, v18, 1, s15
	ds_write_b16 v18, v182 offset:32768
	s_or_b64 exec, exec, s[28:29]
	s_bcnt1_i32_b64 s8, s[8:9]
	s_min_i32 s8, s8, s14
	s_add_i32 s4, s8, s4
	s_sub_i32 s14, s14, s8
.LBB0_1699:
	s_cmp_gt_i32 s14, 0
	s_cselect_b64 s[8:9], -1, 0
	s_and_b64 s[8:9], s[26:27], s[8:9]
	s_andn2_b64 vcc, exec, s[8:9]
	s_cbranch_vccnz .LBB0_1718
	v_xor_b32_e32 v18, v67, v62
	v_bitop3_b32 v19, v67, s51, v62 bitop3:0x48
	v_cmp_eq_u32_e32 vcc, 0, v19
	v_cmp_gt_u32_e64 s[8:9], s49, v18
	v_xor_b32_e32 v18, v67, v63
	v_bitop3_b32 v19, v67, s51, v63 bitop3:0x48
	s_or_b64 s[26:27], s[8:9], vcc
	v_cmp_eq_u32_e32 vcc, 0, v19
	v_cmp_gt_u32_e64 s[8:9], s49, v18
	s_or_b64 s[8:9], s[8:9], vcc
	v_xor_b32_e32 v18, v67, v64
	v_bitop3_b32 v19, v67, s51, v64 bitop3:0x48
	s_or_b64 s[26:27], s[26:27], s[8:9]
	v_cmp_eq_u32_e32 vcc, 0, v19
	v_cmp_gt_u32_e64 s[8:9], s49, v18
	s_or_b64 s[8:9], s[8:9], vcc
	v_xor_b32_e32 v18, v67, v65
	v_bitop3_b32 v19, v67, s51, v65 bitop3:0x48
	s_or_b64 s[26:27], s[8:9], s[26:27]
	v_cmp_eq_u32_e32 vcc, 0, v19
	v_cmp_gt_u32_e64 s[8:9], s49, v18
	s_or_b64 s[8:9], s[8:9], vcc
	s_or_b64 vcc, s[8:9], s[26:27]
	s_cbranch_vccz .LBB0_1718
	v_cmp_eq_u32_sdwa s[8:9], v62, v66 src0_sel:WORD_0 src1_sel:DWORD
	s_nop 1
	v_and_b32_e32 v19, s8, v100
	v_and_b32_e32 v18, s9, v1
	v_bcnt_u32_b32 v19, v19, 0
	v_bcnt_u32_b32 v18, v18, v19
	v_cmp_gt_u32_e32 vcc, s14, v18
	s_and_b64 s[28:29], s[8:9], vcc
	s_and_saveexec_b64 s[26:27], s[28:29]
	s_lshl_b32 s15, s4, 1
	s_add_i32 s15, s52, s15
	v_lshl_add_u32 v18, v18, 1, s15
	ds_write_b16 v18, v183 offset:32768
	s_or_b64 exec, exec, s[26:27]
	s_bcnt1_i32_b64 s8, s[8:9]
	s_min_u32 s8, s8, s14
	s_add_i32 s4, s8, s4
	s_sub_i32 s14, s14, s8
	v_cmp_eq_u32_sdwa s[8:9], v62, v66 src0_sel:WORD_1 src1_sel:DWORD
	s_nop 1
	v_and_b32_e32 v19, s8, v100
	v_and_b32_e32 v18, s9, v1
	v_bcnt_u32_b32 v19, v19, 0
	v_bcnt_u32_b32 v18, v18, v19
	v_cmp_gt_i32_e32 vcc, s14, v18
	s_and_b64 s[28:29], s[8:9], vcc
	s_and_saveexec_b64 s[26:27], s[28:29]
	s_lshl_b32 s15, s4, 1
	s_add_i32 s15, s52, s15
	v_lshl_add_u32 v18, v18, 1, s15
	ds_write_b16 v18, v184 offset:32768
	s_or_b64 exec, exec, s[26:27]
	s_bcnt1_i32_b64 s8, s[8:9]
	s_min_i32 s8, s8, s14
	s_add_i32 s4, s8, s4
	s_sub_i32 s14, s14, s8
	v_cmp_eq_u32_sdwa s[8:9], v63, v66 src0_sel:WORD_0 src1_sel:DWORD
	s_nop 1
	v_and_b32_e32 v19, s8, v100
	v_and_b32_e32 v18, s9, v1
	v_bcnt_u32_b32 v19, v19, 0
	v_bcnt_u32_b32 v18, v18, v19
	v_cmp_gt_i32_e32 vcc, s14, v18
	s_and_b64 s[28:29], s[8:9], vcc
	s_and_saveexec_b64 s[26:27], s[28:29]
	s_lshl_b32 s15, s4, 1
	s_add_i32 s15, s52, s15
	v_lshl_add_u32 v18, v18, 1, s15
	ds_write_b16 v18, v185 offset:32768
	s_or_b64 exec, exec, s[26:27]
	s_bcnt1_i32_b64 s8, s[8:9]
	s_min_i32 s8, s8, s14
	s_add_i32 s4, s8, s4
	s_sub_i32 s14, s14, s8
	v_cmp_eq_u32_sdwa s[8:9], v63, v66 src0_sel:WORD_1 src1_sel:DWORD
	s_nop 1
	v_and_b32_e32 v19, s8, v100
	v_and_b32_e32 v18, s9, v1
	v_bcnt_u32_b32 v19, v19, 0
	v_bcnt_u32_b32 v18, v18, v19
	v_cmp_gt_i32_e32 vcc, s14, v18
	s_and_b64 s[28:29], s[8:9], vcc
	s_and_saveexec_b64 s[26:27], s[28:29]
	s_lshl_b32 s15, s4, 1
	s_add_i32 s15, s52, s15
	v_lshl_add_u32 v18, v18, 1, s15
	ds_write_b16 v18, v186 offset:32768
	s_or_b64 exec, exec, s[26:27]
	s_bcnt1_i32_b64 s8, s[8:9]
	s_min_i32 s8, s8, s14
	s_add_i32 s4, s8, s4
	s_sub_i32 s14, s14, s8
	v_cmp_eq_u32_sdwa s[8:9], v64, v66 src0_sel:WORD_0 src1_sel:DWORD
	s_nop 1
	v_and_b32_e32 v19, s8, v100
	v_and_b32_e32 v18, s9, v1
	v_bcnt_u32_b32 v19, v19, 0
	v_bcnt_u32_b32 v18, v18, v19
	v_cmp_gt_i32_e32 vcc, s14, v18
	s_and_b64 s[28:29], s[8:9], vcc
	s_and_saveexec_b64 s[26:27], s[28:29]
	s_lshl_b32 s15, s4, 1
	s_add_i32 s15, s52, s15
	v_lshl_add_u32 v18, v18, 1, s15
	ds_write_b16 v18, v187 offset:32768
	s_or_b64 exec, exec, s[26:27]
	s_bcnt1_i32_b64 s8, s[8:9]
	s_min_i32 s8, s8, s14
	s_add_i32 s4, s8, s4
	s_sub_i32 s14, s14, s8
	v_cmp_eq_u32_sdwa s[8:9], v64, v66 src0_sel:WORD_1 src1_sel:DWORD
	s_nop 1
	v_and_b32_e32 v19, s8, v100
	v_and_b32_e32 v18, s9, v1
	v_bcnt_u32_b32 v19, v19, 0
	v_bcnt_u32_b32 v18, v18, v19
	v_cmp_gt_i32_e32 vcc, s14, v18
	s_and_b64 s[28:29], s[8:9], vcc
	s_and_saveexec_b64 s[26:27], s[28:29]
	s_lshl_b32 s15, s4, 1
	s_add_i32 s15, s52, s15
	v_lshl_add_u32 v18, v18, 1, s15
	ds_write_b16 v18, v188 offset:32768
	s_or_b64 exec, exec, s[26:27]
	s_bcnt1_i32_b64 s8, s[8:9]
	s_min_i32 s8, s8, s14
	s_add_i32 s4, s8, s4
	s_sub_i32 s14, s14, s8
	v_cmp_eq_u32_sdwa s[8:9], v65, v66 src0_sel:WORD_0 src1_sel:DWORD
	s_nop 1
	v_and_b32_e32 v19, s8, v100
	v_and_b32_e32 v18, s9, v1
	v_bcnt_u32_b32 v19, v19, 0
	v_bcnt_u32_b32 v18, v18, v19
	v_cmp_gt_i32_e32 vcc, s14, v18
	s_and_b64 s[28:29], s[8:9], vcc
	s_and_saveexec_b64 s[26:27], s[28:29]
	s_lshl_b32 s15, s4, 1
	s_add_i32 s15, s52, s15
	v_lshl_add_u32 v18, v18, 1, s15
	ds_write_b16 v18, v189 offset:32768
	s_or_b64 exec, exec, s[26:27]
	s_bcnt1_i32_b64 s8, s[8:9]
	s_min_i32 s8, s8, s14
	s_add_i32 s4, s8, s4
	s_sub_i32 s14, s14, s8
	v_cmp_eq_u32_sdwa s[8:9], v65, v66 src0_sel:WORD_1 src1_sel:DWORD
	s_nop 1
	v_and_b32_e32 v19, s8, v100
	v_and_b32_e32 v18, s9, v1
	v_bcnt_u32_b32 v19, v19, 0
	v_bcnt_u32_b32 v18, v18, v19
	v_cmp_gt_i32_e32 vcc, s14, v18
	s_and_b64 s[28:29], s[8:9], vcc
	s_and_saveexec_b64 s[26:27], s[28:29]
	s_lshl_b32 s15, s4, 1
	s_add_i32 s15, s52, s15
	v_lshl_add_u32 v18, v18, 1, s15
	ds_write_b16 v18, v190 offset:32768
	s_or_b64 exec, exec, s[26:27]
	s_bcnt1_i32_b64 s8, s[8:9]
	s_min_i32 s8, s8, s14
	s_add_i32 s4, s8, s4
	s_sub_i32 s14, s14, s8
.LBB0_1718:
	s_cmp_gt_i32 s14, 0
	s_cselect_b64 s[8:9], -1, 0
	s_and_b64 s[8:9], s[44:45], s[8:9]
	s_andn2_b64 vcc, exec, s[8:9]
	s_cbranch_vccnz .LBB0_1737
	v_xor_b32_e32 v18, v67, v54
	v_bitop3_b32 v19, v67, s51, v54 bitop3:0x48
	v_cmp_eq_u32_e32 vcc, 0, v19
	v_cmp_gt_u32_e64 s[8:9], s49, v18
	v_xor_b32_e32 v18, v67, v55
	v_bitop3_b32 v19, v67, s51, v55 bitop3:0x48
	s_or_b64 s[26:27], s[8:9], vcc
	v_cmp_eq_u32_e32 vcc, 0, v19
	v_cmp_gt_u32_e64 s[8:9], s49, v18
	s_or_b64 s[8:9], s[8:9], vcc
	v_xor_b32_e32 v18, v67, v56
	v_bitop3_b32 v19, v67, s51, v56 bitop3:0x48
	s_or_b64 s[26:27], s[26:27], s[8:9]
	v_cmp_eq_u32_e32 vcc, 0, v19
	v_cmp_gt_u32_e64 s[8:9], s49, v18
	s_or_b64 s[8:9], s[8:9], vcc
	v_xor_b32_e32 v18, v67, v57
	v_bitop3_b32 v19, v67, s51, v57 bitop3:0x48
	s_or_b64 s[26:27], s[8:9], s[26:27]
	v_cmp_eq_u32_e32 vcc, 0, v19
	v_cmp_gt_u32_e64 s[8:9], s49, v18
	s_or_b64 s[8:9], s[8:9], vcc
	s_or_b64 vcc, s[8:9], s[26:27]
	s_cbranch_vccz .LBB0_1737
	v_cmp_eq_u32_sdwa s[8:9], v54, v66 src0_sel:WORD_0 src1_sel:DWORD
	s_nop 1
	v_and_b32_e32 v19, s8, v100
	v_and_b32_e32 v18, s9, v1
	v_bcnt_u32_b32 v19, v19, 0
	v_bcnt_u32_b32 v18, v18, v19
	v_cmp_gt_u32_e32 vcc, s14, v18
	s_and_b64 s[28:29], s[8:9], vcc
	s_and_saveexec_b64 s[26:27], s[28:29]
	s_lshl_b32 s15, s4, 1
	s_add_i32 s15, s52, s15
	v_lshl_add_u32 v18, v18, 1, s15
	ds_write_b16 v18, v191 offset:32768
	s_or_b64 exec, exec, s[26:27]
	s_bcnt1_i32_b64 s8, s[8:9]
	s_min_u32 s8, s8, s14
	s_add_i32 s4, s8, s4
	s_sub_i32 s14, s14, s8
	v_cmp_eq_u32_sdwa s[8:9], v54, v66 src0_sel:WORD_1 src1_sel:DWORD
	s_nop 1
	v_and_b32_e32 v19, s8, v100
	v_and_b32_e32 v18, s9, v1
	v_bcnt_u32_b32 v19, v19, 0
	v_bcnt_u32_b32 v18, v18, v19
	v_cmp_gt_i32_e32 vcc, s14, v18
	s_and_b64 s[28:29], s[8:9], vcc
	s_and_saveexec_b64 s[26:27], s[28:29]
	s_lshl_b32 s15, s4, 1
	s_add_i32 s15, s52, s15
	v_lshl_add_u32 v18, v18, 1, s15
	ds_write_b16 v18, v192 offset:32768
	s_or_b64 exec, exec, s[26:27]
	s_bcnt1_i32_b64 s8, s[8:9]
	s_min_i32 s8, s8, s14
	s_add_i32 s4, s8, s4
	s_sub_i32 s14, s14, s8
	v_cmp_eq_u32_sdwa s[8:9], v55, v66 src0_sel:WORD_0 src1_sel:DWORD
	s_nop 1
	v_and_b32_e32 v19, s8, v100
	v_and_b32_e32 v18, s9, v1
	v_bcnt_u32_b32 v19, v19, 0
	v_bcnt_u32_b32 v18, v18, v19
	v_cmp_gt_i32_e32 vcc, s14, v18
	s_and_b64 s[28:29], s[8:9], vcc
	s_and_saveexec_b64 s[26:27], s[28:29]
	s_lshl_b32 s15, s4, 1
	s_add_i32 s15, s52, s15
	v_lshl_add_u32 v18, v18, 1, s15
	ds_write_b16 v18, v193 offset:32768
	s_or_b64 exec, exec, s[26:27]
	s_bcnt1_i32_b64 s8, s[8:9]
	s_min_i32 s8, s8, s14
	s_add_i32 s4, s8, s4
	s_sub_i32 s14, s14, s8
	v_cmp_eq_u32_sdwa s[8:9], v55, v66 src0_sel:WORD_1 src1_sel:DWORD
	s_nop 1
	v_and_b32_e32 v19, s8, v100
	v_and_b32_e32 v18, s9, v1
	v_bcnt_u32_b32 v19, v19, 0
	v_bcnt_u32_b32 v18, v18, v19
	v_cmp_gt_i32_e32 vcc, s14, v18
	s_and_b64 s[28:29], s[8:9], vcc
	s_and_saveexec_b64 s[26:27], s[28:29]
	s_lshl_b32 s15, s4, 1
	s_add_i32 s15, s52, s15
	v_lshl_add_u32 v18, v18, 1, s15
	ds_write_b16 v18, v194 offset:32768
	s_or_b64 exec, exec, s[26:27]
	s_bcnt1_i32_b64 s8, s[8:9]
	s_min_i32 s8, s8, s14
	s_add_i32 s4, s8, s4
	s_sub_i32 s14, s14, s8
	v_cmp_eq_u32_sdwa s[8:9], v56, v66 src0_sel:WORD_0 src1_sel:DWORD
	s_nop 1
	v_and_b32_e32 v19, s8, v100
	v_and_b32_e32 v18, s9, v1
	v_bcnt_u32_b32 v19, v19, 0
	v_bcnt_u32_b32 v18, v18, v19
	v_cmp_gt_i32_e32 vcc, s14, v18
	s_and_b64 s[28:29], s[8:9], vcc
	s_and_saveexec_b64 s[26:27], s[28:29]
	s_lshl_b32 s15, s4, 1
	s_add_i32 s15, s52, s15
	v_lshl_add_u32 v18, v18, 1, s15
	ds_write_b16 v18, v195 offset:32768
	s_or_b64 exec, exec, s[26:27]
	s_bcnt1_i32_b64 s8, s[8:9]
	s_min_i32 s8, s8, s14
	s_add_i32 s4, s8, s4
	s_sub_i32 s14, s14, s8
	v_cmp_eq_u32_sdwa s[8:9], v56, v66 src0_sel:WORD_1 src1_sel:DWORD
	s_nop 1
	v_and_b32_e32 v19, s8, v100
	v_and_b32_e32 v18, s9, v1
	v_bcnt_u32_b32 v19, v19, 0
	v_bcnt_u32_b32 v18, v18, v19
	v_cmp_gt_i32_e32 vcc, s14, v18
	s_and_b64 s[28:29], s[8:9], vcc
	s_and_saveexec_b64 s[26:27], s[28:29]
	s_lshl_b32 s15, s4, 1
	s_add_i32 s15, s52, s15
	v_lshl_add_u32 v18, v18, 1, s15
	ds_write_b16 v18, v196 offset:32768
	s_or_b64 exec, exec, s[26:27]
	s_bcnt1_i32_b64 s8, s[8:9]
	s_min_i32 s8, s8, s14
	s_add_i32 s4, s8, s4
	s_sub_i32 s14, s14, s8
	v_cmp_eq_u32_sdwa s[8:9], v57, v66 src0_sel:WORD_0 src1_sel:DWORD
	s_nop 1
	v_and_b32_e32 v19, s8, v100
	v_and_b32_e32 v18, s9, v1
	v_bcnt_u32_b32 v19, v19, 0
	v_bcnt_u32_b32 v18, v18, v19
	v_cmp_gt_i32_e32 vcc, s14, v18
	s_and_b64 s[28:29], s[8:9], vcc
	s_and_saveexec_b64 s[26:27], s[28:29]
	s_lshl_b32 s15, s4, 1
	s_add_i32 s15, s52, s15
	v_lshl_add_u32 v18, v18, 1, s15
	ds_write_b16 v18, v197 offset:32768
	s_or_b64 exec, exec, s[26:27]
	s_bcnt1_i32_b64 s8, s[8:9]
	s_min_i32 s8, s8, s14
	s_add_i32 s4, s8, s4
	s_sub_i32 s14, s14, s8
	v_cmp_eq_u32_sdwa s[8:9], v57, v66 src0_sel:WORD_1 src1_sel:DWORD
	s_nop 1
	v_and_b32_e32 v19, s8, v100
	v_and_b32_e32 v18, s9, v1
	v_bcnt_u32_b32 v19, v19, 0
	v_bcnt_u32_b32 v18, v18, v19
	v_cmp_gt_i32_e32 vcc, s14, v18
	s_and_b64 s[28:29], s[8:9], vcc
	s_and_saveexec_b64 s[26:27], s[28:29]
	s_lshl_b32 s15, s4, 1
	s_add_i32 s15, s52, s15
	v_lshl_add_u32 v18, v18, 1, s15
	ds_write_b16 v18, v198 offset:32768
	s_or_b64 exec, exec, s[26:27]
	s_bcnt1_i32_b64 s8, s[8:9]
	s_min_i32 s8, s8, s14
	s_add_i32 s4, s8, s4
	s_sub_i32 s14, s14, s8
.LBB0_1737:
	s_cmp_gt_i32 s14, 0
	s_cselect_b64 s[8:9], -1, 0
	s_and_b64 s[8:9], s[40:41], s[8:9]
	s_andn2_b64 vcc, exec, s[8:9]
	s_cbranch_vccnz .LBB0_1756
	v_xor_b32_e32 v18, v67, v42
	v_bitop3_b32 v19, v67, s51, v42 bitop3:0x48
	v_cmp_eq_u32_e32 vcc, 0, v19
	v_cmp_gt_u32_e64 s[8:9], s49, v18
	v_xor_b32_e32 v18, v67, v43
	v_bitop3_b32 v19, v67, s51, v43 bitop3:0x48
	s_or_b64 s[26:27], s[8:9], vcc
	v_cmp_eq_u32_e32 vcc, 0, v19
	v_cmp_gt_u32_e64 s[8:9], s49, v18
	s_or_b64 s[8:9], s[8:9], vcc
	v_xor_b32_e32 v18, v67, v44
	v_bitop3_b32 v19, v67, s51, v44 bitop3:0x48
	s_or_b64 s[26:27], s[26:27], s[8:9]
	v_cmp_eq_u32_e32 vcc, 0, v19
	v_cmp_gt_u32_e64 s[8:9], s49, v18
	s_or_b64 s[8:9], s[8:9], vcc
	v_xor_b32_e32 v18, v67, v45
	v_bitop3_b32 v19, v67, s51, v45 bitop3:0x48
	s_or_b64 s[26:27], s[8:9], s[26:27]
	v_cmp_eq_u32_e32 vcc, 0, v19
	v_cmp_gt_u32_e64 s[8:9], s49, v18
	s_or_b64 s[8:9], s[8:9], vcc
	s_or_b64 vcc, s[8:9], s[26:27]
	s_cbranch_vccz .LBB0_1756
	v_cmp_eq_u32_sdwa s[8:9], v42, v66 src0_sel:WORD_0 src1_sel:DWORD
	s_nop 1
	v_and_b32_e32 v19, s8, v100
	v_and_b32_e32 v18, s9, v1
	v_bcnt_u32_b32 v19, v19, 0
	v_bcnt_u32_b32 v18, v18, v19
	v_cmp_gt_u32_e32 vcc, s14, v18
	s_and_b64 s[28:29], s[8:9], vcc
	s_and_saveexec_b64 s[26:27], s[28:29]
	s_lshl_b32 s15, s4, 1
	s_add_i32 s15, s52, s15
	v_lshl_add_u32 v18, v18, 1, s15
	ds_write_b16 v18, v199 offset:32768
	s_or_b64 exec, exec, s[26:27]
	s_bcnt1_i32_b64 s8, s[8:9]
	s_min_u32 s8, s8, s14
	s_add_i32 s4, s8, s4
	s_sub_i32 s14, s14, s8
	v_cmp_eq_u32_sdwa s[8:9], v42, v66 src0_sel:WORD_1 src1_sel:DWORD
	s_nop 1
	v_and_b32_e32 v19, s8, v100
	v_and_b32_e32 v18, s9, v1
	v_bcnt_u32_b32 v19, v19, 0
	v_bcnt_u32_b32 v18, v18, v19
	v_cmp_gt_i32_e32 vcc, s14, v18
	s_and_b64 s[28:29], s[8:9], vcc
	s_and_saveexec_b64 s[26:27], s[28:29]
	s_lshl_b32 s15, s4, 1
	s_add_i32 s15, s52, s15
	v_lshl_add_u32 v18, v18, 1, s15
	ds_write_b16 v18, v200 offset:32768
	s_or_b64 exec, exec, s[26:27]
	s_bcnt1_i32_b64 s8, s[8:9]
	s_min_i32 s8, s8, s14
	s_add_i32 s4, s8, s4
	s_sub_i32 s14, s14, s8
	v_cmp_eq_u32_sdwa s[8:9], v43, v66 src0_sel:WORD_0 src1_sel:DWORD
	s_nop 1
	v_and_b32_e32 v19, s8, v100
	v_and_b32_e32 v18, s9, v1
	v_bcnt_u32_b32 v19, v19, 0
	v_bcnt_u32_b32 v18, v18, v19
	v_cmp_gt_i32_e32 vcc, s14, v18
	s_and_b64 s[28:29], s[8:9], vcc
	s_and_saveexec_b64 s[26:27], s[28:29]
	s_lshl_b32 s15, s4, 1
	s_add_i32 s15, s52, s15
	v_lshl_add_u32 v18, v18, 1, s15
	ds_write_b16 v18, v201 offset:32768
	s_or_b64 exec, exec, s[26:27]
	s_bcnt1_i32_b64 s8, s[8:9]
	s_min_i32 s8, s8, s14
	s_add_i32 s4, s8, s4
	s_sub_i32 s14, s14, s8
	v_cmp_eq_u32_sdwa s[8:9], v43, v66 src0_sel:WORD_1 src1_sel:DWORD
	s_nop 1
	v_and_b32_e32 v19, s8, v100
	v_and_b32_e32 v18, s9, v1
	v_bcnt_u32_b32 v19, v19, 0
	v_bcnt_u32_b32 v18, v18, v19
	v_cmp_gt_i32_e32 vcc, s14, v18
	s_and_b64 s[28:29], s[8:9], vcc
	s_and_saveexec_b64 s[26:27], s[28:29]
	s_lshl_b32 s15, s4, 1
	s_add_i32 s15, s52, s15
	v_lshl_add_u32 v18, v18, 1, s15
	ds_write_b16 v18, v202 offset:32768
	s_or_b64 exec, exec, s[26:27]
	s_bcnt1_i32_b64 s8, s[8:9]
	s_min_i32 s8, s8, s14
	s_add_i32 s4, s8, s4
	s_sub_i32 s14, s14, s8
	v_cmp_eq_u32_sdwa s[8:9], v44, v66 src0_sel:WORD_0 src1_sel:DWORD
	s_nop 1
	v_and_b32_e32 v19, s8, v100
	v_and_b32_e32 v18, s9, v1
	v_bcnt_u32_b32 v19, v19, 0
	v_bcnt_u32_b32 v18, v18, v19
	v_cmp_gt_i32_e32 vcc, s14, v18
	s_and_b64 s[28:29], s[8:9], vcc
	s_and_saveexec_b64 s[26:27], s[28:29]
	s_lshl_b32 s15, s4, 1
	s_add_i32 s15, s52, s15
	v_lshl_add_u32 v18, v18, 1, s15
	ds_write_b16 v18, v203 offset:32768
	s_or_b64 exec, exec, s[26:27]
	s_bcnt1_i32_b64 s8, s[8:9]
	s_min_i32 s8, s8, s14
	s_add_i32 s4, s8, s4
	s_sub_i32 s14, s14, s8
	v_cmp_eq_u32_sdwa s[8:9], v44, v66 src0_sel:WORD_1 src1_sel:DWORD
	s_nop 1
	v_and_b32_e32 v19, s8, v100
	v_and_b32_e32 v18, s9, v1
	v_bcnt_u32_b32 v19, v19, 0
	v_bcnt_u32_b32 v18, v18, v19
	v_cmp_gt_i32_e32 vcc, s14, v18
	s_and_b64 s[28:29], s[8:9], vcc
	s_and_saveexec_b64 s[26:27], s[28:29]
	s_lshl_b32 s15, s4, 1
	s_add_i32 s15, s52, s15
	v_lshl_add_u32 v18, v18, 1, s15
	ds_write_b16 v18, v204 offset:32768
	s_or_b64 exec, exec, s[26:27]
	s_bcnt1_i32_b64 s8, s[8:9]
	s_min_i32 s8, s8, s14
	s_add_i32 s4, s8, s4
	s_sub_i32 s14, s14, s8
	v_cmp_eq_u32_sdwa s[8:9], v45, v66 src0_sel:WORD_0 src1_sel:DWORD
	s_nop 1
	v_and_b32_e32 v19, s8, v100
	v_and_b32_e32 v18, s9, v1
	v_bcnt_u32_b32 v19, v19, 0
	v_bcnt_u32_b32 v18, v18, v19
	v_cmp_gt_i32_e32 vcc, s14, v18
	s_and_b64 s[28:29], s[8:9], vcc
	s_and_saveexec_b64 s[26:27], s[28:29]
	s_lshl_b32 s15, s4, 1
	s_add_i32 s15, s52, s15
	v_lshl_add_u32 v18, v18, 1, s15
	ds_write_b16 v18, v205 offset:32768
	s_or_b64 exec, exec, s[26:27]
	s_bcnt1_i32_b64 s8, s[8:9]
	s_min_i32 s8, s8, s14
	s_add_i32 s4, s8, s4
	s_sub_i32 s14, s14, s8
	v_cmp_eq_u32_sdwa s[8:9], v45, v66 src0_sel:WORD_1 src1_sel:DWORD
	s_nop 1
	v_and_b32_e32 v19, s8, v100
	v_and_b32_e32 v18, s9, v1
	v_bcnt_u32_b32 v19, v19, 0
	v_bcnt_u32_b32 v18, v18, v19
	v_cmp_gt_i32_e32 vcc, s14, v18
	s_and_b64 s[28:29], s[8:9], vcc
	s_and_saveexec_b64 s[26:27], s[28:29]
	s_lshl_b32 s15, s4, 1
	s_add_i32 s15, s52, s15
	v_lshl_add_u32 v18, v18, 1, s15
	ds_write_b16 v18, v206 offset:32768
	s_or_b64 exec, exec, s[26:27]
	s_bcnt1_i32_b64 s8, s[8:9]
	s_min_i32 s8, s8, s14
	s_add_i32 s4, s8, s4
	s_sub_i32 s14, s14, s8
.LBB0_1756:
	s_cmp_gt_i32 s14, 0
	s_cselect_b64 s[8:9], -1, 0
	s_and_b64 s[8:9], s[38:39], s[8:9]
	s_andn2_b64 vcc, exec, s[8:9]
	s_cbranch_vccnz .LBB0_1775
	v_xor_b32_e32 v18, v67, v30
	v_bitop3_b32 v19, v67, s51, v30 bitop3:0x48
	v_cmp_eq_u32_e32 vcc, 0, v19
	v_cmp_gt_u32_e64 s[8:9], s49, v18
	v_xor_b32_e32 v18, v67, v31
	v_bitop3_b32 v19, v67, s51, v31 bitop3:0x48
	s_or_b64 s[26:27], s[8:9], vcc
	v_cmp_eq_u32_e32 vcc, 0, v19
	v_cmp_gt_u32_e64 s[8:9], s49, v18
	s_or_b64 s[8:9], s[8:9], vcc
	v_xor_b32_e32 v18, v67, v32
	v_bitop3_b32 v19, v67, s51, v32 bitop3:0x48
	s_or_b64 s[26:27], s[26:27], s[8:9]
	v_cmp_eq_u32_e32 vcc, 0, v19
	v_cmp_gt_u32_e64 s[8:9], s49, v18
	s_or_b64 s[8:9], s[8:9], vcc
	v_xor_b32_e32 v18, v67, v33
	v_bitop3_b32 v19, v67, s51, v33 bitop3:0x48
	s_or_b64 s[26:27], s[8:9], s[26:27]
	v_cmp_eq_u32_e32 vcc, 0, v19
	v_cmp_gt_u32_e64 s[8:9], s49, v18
	s_or_b64 s[8:9], s[8:9], vcc
	s_or_b64 vcc, s[8:9], s[26:27]
	s_cbranch_vccz .LBB0_1775
	v_cmp_eq_u32_sdwa s[8:9], v30, v66 src0_sel:WORD_0 src1_sel:DWORD
	s_nop 1
	v_and_b32_e32 v19, s8, v100
	v_and_b32_e32 v18, s9, v1
	v_bcnt_u32_b32 v19, v19, 0
	v_bcnt_u32_b32 v18, v18, v19
	v_cmp_gt_u32_e32 vcc, s14, v18
	s_and_b64 s[28:29], s[8:9], vcc
	s_and_saveexec_b64 s[26:27], s[28:29]
	s_lshl_b32 s15, s4, 1
	s_add_i32 s15, s52, s15
	v_lshl_add_u32 v18, v18, 1, s15
	ds_write_b16 v18, v207 offset:32768
	s_or_b64 exec, exec, s[26:27]
	s_bcnt1_i32_b64 s8, s[8:9]
	s_min_u32 s8, s8, s14
	s_add_i32 s4, s8, s4
	s_sub_i32 s14, s14, s8
	v_cmp_eq_u32_sdwa s[8:9], v30, v66 src0_sel:WORD_1 src1_sel:DWORD
	s_nop 1
	v_and_b32_e32 v19, s8, v100
	v_and_b32_e32 v18, s9, v1
	v_bcnt_u32_b32 v19, v19, 0
	v_bcnt_u32_b32 v18, v18, v19
	v_cmp_gt_i32_e32 vcc, s14, v18
	s_and_b64 s[28:29], s[8:9], vcc
	s_and_saveexec_b64 s[26:27], s[28:29]
	s_lshl_b32 s15, s4, 1
	s_add_i32 s15, s52, s15
	v_lshl_add_u32 v18, v18, 1, s15
	ds_write_b16 v18, v208 offset:32768
	s_or_b64 exec, exec, s[26:27]
	s_bcnt1_i32_b64 s8, s[8:9]
	s_min_i32 s8, s8, s14
	s_add_i32 s4, s8, s4
	s_sub_i32 s14, s14, s8
	v_cmp_eq_u32_sdwa s[8:9], v31, v66 src0_sel:WORD_0 src1_sel:DWORD
	s_nop 1
	v_and_b32_e32 v19, s8, v100
	v_and_b32_e32 v18, s9, v1
	v_bcnt_u32_b32 v19, v19, 0
	v_bcnt_u32_b32 v18, v18, v19
	v_cmp_gt_i32_e32 vcc, s14, v18
	s_and_b64 s[28:29], s[8:9], vcc
	s_and_saveexec_b64 s[26:27], s[28:29]
	s_lshl_b32 s15, s4, 1
	s_add_i32 s15, s52, s15
	v_lshl_add_u32 v18, v18, 1, s15
	ds_write_b16 v18, v209 offset:32768
	s_or_b64 exec, exec, s[26:27]
	s_bcnt1_i32_b64 s8, s[8:9]
	s_min_i32 s8, s8, s14
	s_add_i32 s4, s8, s4
	s_sub_i32 s14, s14, s8
	v_cmp_eq_u32_sdwa s[8:9], v31, v66 src0_sel:WORD_1 src1_sel:DWORD
	s_nop 1
	v_and_b32_e32 v19, s8, v100
	v_and_b32_e32 v18, s9, v1
	v_bcnt_u32_b32 v19, v19, 0
	v_bcnt_u32_b32 v18, v18, v19
	v_cmp_gt_i32_e32 vcc, s14, v18
	s_and_b64 s[28:29], s[8:9], vcc
	s_and_saveexec_b64 s[26:27], s[28:29]
	s_lshl_b32 s15, s4, 1
	s_add_i32 s15, s52, s15
	v_lshl_add_u32 v18, v18, 1, s15
	ds_write_b16 v18, v210 offset:32768
	s_or_b64 exec, exec, s[26:27]
	s_bcnt1_i32_b64 s8, s[8:9]
	s_min_i32 s8, s8, s14
	s_add_i32 s4, s8, s4
	s_sub_i32 s14, s14, s8
	v_cmp_eq_u32_sdwa s[8:9], v32, v66 src0_sel:WORD_0 src1_sel:DWORD
	s_nop 1
	v_and_b32_e32 v19, s8, v100
	v_and_b32_e32 v18, s9, v1
	v_bcnt_u32_b32 v19, v19, 0
	v_bcnt_u32_b32 v18, v18, v19
	v_cmp_gt_i32_e32 vcc, s14, v18
	s_and_b64 s[28:29], s[8:9], vcc
	s_and_saveexec_b64 s[26:27], s[28:29]
	s_lshl_b32 s15, s4, 1
	s_add_i32 s15, s52, s15
	v_lshl_add_u32 v18, v18, 1, s15
	ds_write_b16 v18, v211 offset:32768
	s_or_b64 exec, exec, s[26:27]
	s_bcnt1_i32_b64 s8, s[8:9]
	s_min_i32 s8, s8, s14
	s_add_i32 s4, s8, s4
	s_sub_i32 s14, s14, s8
	v_cmp_eq_u32_sdwa s[8:9], v32, v66 src0_sel:WORD_1 src1_sel:DWORD
	s_nop 1
	v_and_b32_e32 v19, s8, v100
	v_and_b32_e32 v18, s9, v1
	v_bcnt_u32_b32 v19, v19, 0
	v_bcnt_u32_b32 v18, v18, v19
	v_cmp_gt_i32_e32 vcc, s14, v18
	s_and_b64 s[28:29], s[8:9], vcc
	s_and_saveexec_b64 s[26:27], s[28:29]
	s_lshl_b32 s15, s4, 1
	s_add_i32 s15, s52, s15
	v_lshl_add_u32 v18, v18, 1, s15
	ds_write_b16 v18, v212 offset:32768
	s_or_b64 exec, exec, s[26:27]
	s_bcnt1_i32_b64 s8, s[8:9]
	s_min_i32 s8, s8, s14
	s_add_i32 s4, s8, s4
	s_sub_i32 s14, s14, s8
	v_cmp_eq_u32_sdwa s[8:9], v33, v66 src0_sel:WORD_0 src1_sel:DWORD
	s_nop 1
	v_and_b32_e32 v19, s8, v100
	v_and_b32_e32 v18, s9, v1
	v_bcnt_u32_b32 v19, v19, 0
	v_bcnt_u32_b32 v18, v18, v19
	v_cmp_gt_i32_e32 vcc, s14, v18
	s_and_b64 s[28:29], s[8:9], vcc
	s_and_saveexec_b64 s[26:27], s[28:29]
	s_lshl_b32 s15, s4, 1
	s_add_i32 s15, s52, s15
	v_lshl_add_u32 v18, v18, 1, s15
	ds_write_b16 v18, v213 offset:32768
	s_or_b64 exec, exec, s[26:27]
	s_bcnt1_i32_b64 s8, s[8:9]
	s_min_i32 s8, s8, s14
	s_add_i32 s4, s8, s4
	s_sub_i32 s14, s14, s8
	v_cmp_eq_u32_sdwa s[8:9], v33, v66 src0_sel:WORD_1 src1_sel:DWORD
	s_nop 1
	v_and_b32_e32 v19, s8, v100
	v_and_b32_e32 v18, s9, v1
	v_bcnt_u32_b32 v19, v19, 0
	v_bcnt_u32_b32 v18, v18, v19
	v_cmp_gt_i32_e32 vcc, s14, v18
	s_and_b64 s[28:29], s[8:9], vcc
	s_and_saveexec_b64 s[26:27], s[28:29]
	s_lshl_b32 s15, s4, 1
	s_add_i32 s15, s52, s15
	v_lshl_add_u32 v18, v18, 1, s15
	ds_write_b16 v18, v214 offset:32768
	s_or_b64 exec, exec, s[26:27]
	s_bcnt1_i32_b64 s8, s[8:9]
	s_min_i32 s8, s8, s14
	s_add_i32 s4, s8, s4
	s_sub_i32 s14, s14, s8
.LBB0_1775:
	s_cmp_gt_i32 s14, 0
	s_cselect_b64 s[8:9], -1, 0
	s_and_b64 s[2:3], s[2:3], s[8:9]
	s_andn2_b64 vcc, exec, s[2:3]
	s_cbranch_vccnz .LBB0_1794
	v_xor_b32_e32 v18, v67, v14
	v_bitop3_b32 v19, v67, s51, v14 bitop3:0x48
	v_cmp_eq_u32_e32 vcc, 0, v19
	v_cmp_gt_u32_e64 s[8:9], s49, v18
	v_xor_b32_e32 v18, v67, v15
	v_bitop3_b32 v19, v67, s51, v15 bitop3:0x48
	s_or_b64 s[2:3], s[8:9], vcc
	v_cmp_eq_u32_e32 vcc, 0, v19
	v_cmp_gt_u32_e64 s[8:9], s49, v18
	s_or_b64 s[8:9], s[8:9], vcc
	v_xor_b32_e32 v18, v67, v16
	v_bitop3_b32 v19, v67, s51, v16 bitop3:0x48
	s_or_b64 s[2:3], s[2:3], s[8:9]
	v_cmp_eq_u32_e32 vcc, 0, v19
	v_cmp_gt_u32_e64 s[8:9], s49, v18
	s_or_b64 s[8:9], s[8:9], vcc
	v_xor_b32_e32 v18, v67, v17
	v_bitop3_b32 v19, v67, s51, v17 bitop3:0x48
	s_or_b64 s[2:3], s[8:9], s[2:3]
	v_cmp_eq_u32_e32 vcc, 0, v19
	v_cmp_gt_u32_e64 s[8:9], s49, v18
	s_or_b64 s[8:9], s[8:9], vcc
	s_or_b64 vcc, s[8:9], s[2:3]
	s_cbranch_vccz .LBB0_1794
	v_cmp_eq_u32_sdwa s[2:3], v14, v66 src0_sel:WORD_0 src1_sel:DWORD
	s_nop 1
	v_and_b32_e32 v19, s2, v100
	v_and_b32_e32 v18, s3, v1
	v_bcnt_u32_b32 v19, v19, 0
	v_bcnt_u32_b32 v18, v18, v19
	v_cmp_gt_u32_e32 vcc, s14, v18
	s_and_b64 s[26:27], s[2:3], vcc
	s_and_saveexec_b64 s[8:9], s[26:27]
	s_lshl_b32 s15, s4, 1
	s_add_i32 s15, s52, s15
	v_lshl_add_u32 v18, v18, 1, s15
	ds_write_b16 v18, v215 offset:32768
	s_or_b64 exec, exec, s[8:9]
	s_bcnt1_i32_b64 s2, s[2:3]
	s_min_u32 s2, s2, s14
	s_add_i32 s4, s2, s4
	s_sub_i32 s14, s14, s2
	v_cmp_eq_u32_sdwa s[2:3], v14, v66 src0_sel:WORD_1 src1_sel:DWORD
	s_nop 1
	v_and_b32_e32 v18, s2, v100
	v_and_b32_e32 v14, s3, v1
	v_bcnt_u32_b32 v18, v18, 0
	v_bcnt_u32_b32 v14, v14, v18
	v_cmp_gt_i32_e32 vcc, s14, v14
	s_and_b64 s[26:27], s[2:3], vcc
	s_and_saveexec_b64 s[8:9], s[26:27]
	s_lshl_b32 s15, s4, 1
	s_add_i32 s15, s52, s15
	v_lshl_add_u32 v14, v14, 1, s15
	ds_write_b16 v14, v216 offset:32768
	s_or_b64 exec, exec, s[8:9]
	s_bcnt1_i32_b64 s2, s[2:3]
	s_min_i32 s2, s2, s14
	s_add_i32 s4, s2, s4
	s_sub_i32 s14, s14, s2
	v_cmp_eq_u32_sdwa s[2:3], v15, v66 src0_sel:WORD_0 src1_sel:DWORD
	s_nop 1
	v_and_b32_e32 v18, s2, v100
	v_and_b32_e32 v14, s3, v1
	v_bcnt_u32_b32 v18, v18, 0
	v_bcnt_u32_b32 v14, v14, v18
	v_cmp_gt_i32_e32 vcc, s14, v14
	s_and_b64 s[26:27], s[2:3], vcc
	s_and_saveexec_b64 s[8:9], s[26:27]
	s_lshl_b32 s15, s4, 1
	s_add_i32 s15, s52, s15
	v_lshl_add_u32 v14, v14, 1, s15
	ds_write_b16 v14, v217 offset:32768
	s_or_b64 exec, exec, s[8:9]
	s_bcnt1_i32_b64 s2, s[2:3]
	s_min_i32 s2, s2, s14
	s_add_i32 s4, s2, s4
	s_sub_i32 s14, s14, s2
	v_cmp_eq_u32_sdwa s[2:3], v15, v66 src0_sel:WORD_1 src1_sel:DWORD
	s_nop 1
	v_and_b32_e32 v15, s2, v100
	v_and_b32_e32 v14, s3, v1
	v_bcnt_u32_b32 v15, v15, 0
	v_bcnt_u32_b32 v14, v14, v15
	v_cmp_gt_i32_e32 vcc, s14, v14
	s_and_b64 s[26:27], s[2:3], vcc
	s_and_saveexec_b64 s[8:9], s[26:27]
	s_lshl_b32 s15, s4, 1
	s_add_i32 s15, s52, s15
	v_lshl_add_u32 v14, v14, 1, s15
	ds_write_b16 v14, v218 offset:32768
	s_or_b64 exec, exec, s[8:9]
	s_bcnt1_i32_b64 s2, s[2:3]
	s_min_i32 s2, s2, s14
	s_add_i32 s4, s2, s4
	s_sub_i32 s14, s14, s2
	v_cmp_eq_u32_sdwa s[2:3], v16, v66 src0_sel:WORD_0 src1_sel:DWORD
	s_nop 1
	v_and_b32_e32 v15, s2, v100
	v_and_b32_e32 v14, s3, v1
	v_bcnt_u32_b32 v15, v15, 0
	v_bcnt_u32_b32 v14, v14, v15
	v_cmp_gt_i32_e32 vcc, s14, v14
	s_and_b64 s[26:27], s[2:3], vcc
	s_and_saveexec_b64 s[8:9], s[26:27]
	s_lshl_b32 s15, s4, 1
	s_add_i32 s15, s52, s15
	v_lshl_add_u32 v14, v14, 1, s15
	ds_write_b16 v14, v219 offset:32768
	s_or_b64 exec, exec, s[8:9]
	s_bcnt1_i32_b64 s2, s[2:3]
	s_min_i32 s2, s2, s14
	s_add_i32 s4, s2, s4
	s_sub_i32 s14, s14, s2
	v_cmp_eq_u32_sdwa s[2:3], v16, v66 src0_sel:WORD_1 src1_sel:DWORD
	s_nop 1
	v_and_b32_e32 v15, s2, v100
	v_and_b32_e32 v14, s3, v1
	v_bcnt_u32_b32 v15, v15, 0
	v_bcnt_u32_b32 v14, v14, v15
	v_cmp_gt_i32_e32 vcc, s14, v14
	s_and_b64 s[26:27], s[2:3], vcc
	s_and_saveexec_b64 s[8:9], s[26:27]
	s_lshl_b32 s15, s4, 1
	s_add_i32 s15, s52, s15
	v_lshl_add_u32 v14, v14, 1, s15
	ds_write_b16 v14, v220 offset:32768
	s_or_b64 exec, exec, s[8:9]
	s_bcnt1_i32_b64 s2, s[2:3]
	s_min_i32 s2, s2, s14
	s_add_i32 s4, s2, s4
	s_sub_i32 s14, s14, s2
	v_cmp_eq_u32_sdwa s[2:3], v17, v66 src0_sel:WORD_0 src1_sel:DWORD
	s_nop 1
	v_and_b32_e32 v15, s2, v100
	v_and_b32_e32 v14, s3, v1
	v_bcnt_u32_b32 v15, v15, 0
	v_bcnt_u32_b32 v14, v14, v15
	v_cmp_gt_i32_e32 vcc, s14, v14
	s_and_b64 s[26:27], s[2:3], vcc
	s_and_saveexec_b64 s[8:9], s[26:27]
	s_lshl_b32 s15, s4, 1
	s_add_i32 s15, s52, s15
	v_lshl_add_u32 v14, v14, 1, s15
	ds_write_b16 v14, v221 offset:32768
	s_or_b64 exec, exec, s[8:9]
	s_bcnt1_i32_b64 s2, s[2:3]
	s_min_i32 s2, s2, s14
	s_add_i32 s4, s2, s4
	s_sub_i32 s14, s14, s2
	v_cmp_eq_u32_sdwa s[2:3], v17, v66 src0_sel:WORD_1 src1_sel:DWORD
	s_nop 1
	v_and_b32_e32 v15, s2, v100
	v_and_b32_e32 v14, s3, v1
	v_bcnt_u32_b32 v15, v15, 0
	v_bcnt_u32_b32 v14, v14, v15
	v_cmp_gt_i32_e32 vcc, s14, v14
	s_and_b64 s[26:27], s[2:3], vcc
	s_and_saveexec_b64 s[8:9], s[26:27]
	s_lshl_b32 s15, s4, 1
	s_add_i32 s15, s52, s15
	v_lshl_add_u32 v14, v14, 1, s15
	ds_write_b16 v14, v222 offset:32768
	s_or_b64 exec, exec, s[8:9]
	s_bcnt1_i32_b64 s2, s[2:3]
	s_min_i32 s2, s2, s14
	s_add_i32 s4, s2, s4
	s_sub_i32 s14, s14, s2
.LBB0_1794:
	s_cmp_gt_i32 s14, 0
	s_cselect_b64 s[2:3], -1, 0
	s_and_b64 s[2:3], s[36:37], s[2:3]
	s_andn2_b64 vcc, exec, s[2:3]
	s_cbranch_vccnz .LBB0_1813
	v_xor_b32_e32 v14, v67, v10
	v_bitop3_b32 v15, v67, s51, v10 bitop3:0x48
	v_cmp_eq_u32_e32 vcc, 0, v15
	v_cmp_gt_u32_e64 s[8:9], s49, v14
	v_xor_b32_e32 v14, v67, v11
	v_bitop3_b32 v15, v67, s51, v11 bitop3:0x48
	s_or_b64 s[2:3], s[8:9], vcc
	v_cmp_eq_u32_e32 vcc, 0, v15
	v_cmp_gt_u32_e64 s[8:9], s49, v14
	s_or_b64 s[8:9], s[8:9], vcc
	v_xor_b32_e32 v14, v67, v12
	v_bitop3_b32 v15, v67, s51, v12 bitop3:0x48
	s_or_b64 s[2:3], s[2:3], s[8:9]
	v_cmp_eq_u32_e32 vcc, 0, v15
	v_cmp_gt_u32_e64 s[8:9], s49, v14
	s_or_b64 s[8:9], s[8:9], vcc
	v_xor_b32_e32 v14, v67, v13
	v_bitop3_b32 v15, v67, s51, v13 bitop3:0x48
	s_or_b64 s[2:3], s[8:9], s[2:3]
	v_cmp_eq_u32_e32 vcc, 0, v15
	v_cmp_gt_u32_e64 s[8:9], s49, v14
	s_or_b64 s[8:9], s[8:9], vcc
	s_or_b64 vcc, s[8:9], s[2:3]
	s_cbranch_vccz .LBB0_1813
	v_cmp_eq_u32_sdwa s[2:3], v10, v66 src0_sel:WORD_0 src1_sel:DWORD
	s_nop 1
	v_and_b32_e32 v15, s2, v100
	v_and_b32_e32 v14, s3, v1
	v_bcnt_u32_b32 v15, v15, 0
	v_bcnt_u32_b32 v14, v14, v15
	v_cmp_gt_u32_e32 vcc, s14, v14
	s_and_b64 s[26:27], s[2:3], vcc
	s_and_saveexec_b64 s[8:9], s[26:27]
	s_lshl_b32 s15, s4, 1
	s_add_i32 s15, s52, s15
	v_lshl_add_u32 v14, v14, 1, s15
	ds_write_b16 v14, v223 offset:32768
	s_or_b64 exec, exec, s[8:9]
	s_bcnt1_i32_b64 s2, s[2:3]
	s_min_u32 s2, s2, s14
	s_add_i32 s4, s2, s4
	s_sub_i32 s14, s14, s2
	v_cmp_eq_u32_sdwa s[2:3], v10, v66 src0_sel:WORD_1 src1_sel:DWORD
	s_nop 1
	v_and_b32_e32 v14, s2, v100
	v_and_b32_e32 v10, s3, v1
	v_bcnt_u32_b32 v14, v14, 0
	v_bcnt_u32_b32 v10, v10, v14
	v_cmp_gt_i32_e32 vcc, s14, v10
	s_and_b64 s[26:27], s[2:3], vcc
	s_and_saveexec_b64 s[8:9], s[26:27]
	s_lshl_b32 s15, s4, 1
	s_add_i32 s15, s52, s15
	v_lshl_add_u32 v10, v10, 1, s15
	ds_write_b16 v10, v224 offset:32768
	s_or_b64 exec, exec, s[8:9]
	s_bcnt1_i32_b64 s2, s[2:3]
	s_min_i32 s2, s2, s14
	s_add_i32 s4, s2, s4
	s_sub_i32 s14, s14, s2
	v_cmp_eq_u32_sdwa s[2:3], v11, v66 src0_sel:WORD_0 src1_sel:DWORD
	s_nop 1
	v_and_b32_e32 v14, s2, v100
	v_and_b32_e32 v10, s3, v1
	v_bcnt_u32_b32 v14, v14, 0
	v_bcnt_u32_b32 v10, v10, v14
	v_cmp_gt_i32_e32 vcc, s14, v10
	s_and_b64 s[26:27], s[2:3], vcc
	s_and_saveexec_b64 s[8:9], s[26:27]
	s_lshl_b32 s15, s4, 1
	s_add_i32 s15, s52, s15
	v_lshl_add_u32 v10, v10, 1, s15
	ds_write_b16 v10, v225 offset:32768
	s_or_b64 exec, exec, s[8:9]
	s_bcnt1_i32_b64 s2, s[2:3]
	s_min_i32 s2, s2, s14
	s_add_i32 s4, s2, s4
	s_sub_i32 s14, s14, s2
	v_cmp_eq_u32_sdwa s[2:3], v11, v66 src0_sel:WORD_1 src1_sel:DWORD
	s_nop 1
	v_and_b32_e32 v11, s2, v100
	v_and_b32_e32 v10, s3, v1
	v_bcnt_u32_b32 v11, v11, 0
	v_bcnt_u32_b32 v10, v10, v11
	v_cmp_gt_i32_e32 vcc, s14, v10
	s_and_b64 s[26:27], s[2:3], vcc
	s_and_saveexec_b64 s[8:9], s[26:27]
	s_lshl_b32 s15, s4, 1
	s_add_i32 s15, s52, s15
	v_lshl_add_u32 v10, v10, 1, s15
	ds_write_b16 v10, v226 offset:32768
	s_or_b64 exec, exec, s[8:9]
	s_bcnt1_i32_b64 s2, s[2:3]
	s_min_i32 s2, s2, s14
	s_add_i32 s4, s2, s4
	s_sub_i32 s14, s14, s2
	v_cmp_eq_u32_sdwa s[2:3], v12, v66 src0_sel:WORD_0 src1_sel:DWORD
	s_nop 1
	v_and_b32_e32 v11, s2, v100
	v_and_b32_e32 v10, s3, v1
	v_bcnt_u32_b32 v11, v11, 0
	v_bcnt_u32_b32 v10, v10, v11
	v_cmp_gt_i32_e32 vcc, s14, v10
	s_and_b64 s[26:27], s[2:3], vcc
	s_and_saveexec_b64 s[8:9], s[26:27]
	s_lshl_b32 s15, s4, 1
	s_add_i32 s15, s52, s15
	v_lshl_add_u32 v10, v10, 1, s15
	ds_write_b16 v10, v227 offset:32768
	s_or_b64 exec, exec, s[8:9]
	s_bcnt1_i32_b64 s2, s[2:3]
	s_min_i32 s2, s2, s14
	s_add_i32 s4, s2, s4
	s_sub_i32 s14, s14, s2
	v_cmp_eq_u32_sdwa s[2:3], v12, v66 src0_sel:WORD_1 src1_sel:DWORD
	s_nop 1
	v_and_b32_e32 v11, s2, v100
	v_and_b32_e32 v10, s3, v1
	v_bcnt_u32_b32 v11, v11, 0
	v_bcnt_u32_b32 v10, v10, v11
	v_cmp_gt_i32_e32 vcc, s14, v10
	s_and_b64 s[26:27], s[2:3], vcc
	s_and_saveexec_b64 s[8:9], s[26:27]
	s_lshl_b32 s15, s4, 1
	s_add_i32 s15, s52, s15
	v_lshl_add_u32 v10, v10, 1, s15
	ds_write_b16 v10, v228 offset:32768
	s_or_b64 exec, exec, s[8:9]
	s_bcnt1_i32_b64 s2, s[2:3]
	s_min_i32 s2, s2, s14
	s_add_i32 s4, s2, s4
	s_sub_i32 s14, s14, s2
	v_cmp_eq_u32_sdwa s[2:3], v13, v66 src0_sel:WORD_0 src1_sel:DWORD
	s_nop 1
	v_and_b32_e32 v11, s2, v100
	v_and_b32_e32 v10, s3, v1
	v_bcnt_u32_b32 v11, v11, 0
	v_bcnt_u32_b32 v10, v10, v11
	v_cmp_gt_i32_e32 vcc, s14, v10
	s_and_b64 s[26:27], s[2:3], vcc
	s_and_saveexec_b64 s[8:9], s[26:27]
	s_lshl_b32 s15, s4, 1
	s_add_i32 s15, s52, s15
	v_lshl_add_u32 v10, v10, 1, s15
	ds_write_b16 v10, v229 offset:32768
	s_or_b64 exec, exec, s[8:9]
	s_bcnt1_i32_b64 s2, s[2:3]
	s_min_i32 s2, s2, s14
	s_add_i32 s4, s2, s4
	s_sub_i32 s14, s14, s2
	v_cmp_eq_u32_sdwa s[2:3], v13, v66 src0_sel:WORD_1 src1_sel:DWORD
	s_nop 1
	v_and_b32_e32 v11, s2, v100
	v_and_b32_e32 v10, s3, v1
	v_bcnt_u32_b32 v11, v11, 0
	v_bcnt_u32_b32 v10, v10, v11
	v_cmp_gt_i32_e32 vcc, s14, v10
	s_and_b64 s[26:27], s[2:3], vcc
	s_and_saveexec_b64 s[8:9], s[26:27]
	s_lshl_b32 s15, s4, 1
	s_add_i32 s15, s52, s15
	v_lshl_add_u32 v10, v10, 1, s15
	ds_write_b16 v10, v230 offset:32768
	s_or_b64 exec, exec, s[8:9]
	s_bcnt1_i32_b64 s2, s[2:3]
	s_min_i32 s2, s2, s14
	s_add_i32 s4, s2, s4
	s_sub_i32 s14, s14, s2
.LBB0_1813:
	s_cmp_gt_i32 s14, 0
	s_cselect_b64 s[2:3], -1, 0
	s_and_b64 s[2:3], s[34:35], s[2:3]
	s_andn2_b64 vcc, exec, s[2:3]
	s_cbranch_vccnz .LBB0_1832
	v_xor_b32_e32 v10, v67, v6
	v_bitop3_b32 v11, v67, s51, v6 bitop3:0x48
	v_cmp_eq_u32_e32 vcc, 0, v11
	v_cmp_gt_u32_e64 s[8:9], s49, v10
	v_xor_b32_e32 v10, v67, v7
	v_bitop3_b32 v11, v67, s51, v7 bitop3:0x48
	s_or_b64 s[2:3], s[8:9], vcc
	v_cmp_eq_u32_e32 vcc, 0, v11
	v_cmp_gt_u32_e64 s[8:9], s49, v10
	s_or_b64 s[8:9], s[8:9], vcc
	v_xor_b32_e32 v10, v67, v8
	v_bitop3_b32 v11, v67, s51, v8 bitop3:0x48
	s_or_b64 s[2:3], s[2:3], s[8:9]
	v_cmp_eq_u32_e32 vcc, 0, v11
	v_cmp_gt_u32_e64 s[8:9], s49, v10
	s_or_b64 s[8:9], s[8:9], vcc
	v_xor_b32_e32 v10, v67, v9
	v_bitop3_b32 v11, v67, s51, v9 bitop3:0x48
	s_or_b64 s[2:3], s[8:9], s[2:3]
	v_cmp_eq_u32_e32 vcc, 0, v11
	v_cmp_gt_u32_e64 s[8:9], s49, v10
	s_or_b64 s[8:9], s[8:9], vcc
	s_or_b64 vcc, s[8:9], s[2:3]
	s_cbranch_vccz .LBB0_1832
	v_cmp_eq_u32_sdwa s[2:3], v6, v66 src0_sel:WORD_0 src1_sel:DWORD
	s_nop 1
	v_and_b32_e32 v11, s2, v100
	v_and_b32_e32 v10, s3, v1
	v_bcnt_u32_b32 v11, v11, 0
	v_bcnt_u32_b32 v10, v10, v11
	v_cmp_gt_u32_e32 vcc, s14, v10
	s_and_b64 s[26:27], s[2:3], vcc
	s_and_saveexec_b64 s[8:9], s[26:27]
	s_lshl_b32 s15, s4, 1
	s_add_i32 s15, s52, s15
	v_lshl_add_u32 v10, v10, 1, s15
	ds_write_b16 v10, v231 offset:32768
	s_or_b64 exec, exec, s[8:9]
	s_bcnt1_i32_b64 s2, s[2:3]
	s_min_u32 s2, s2, s14
	s_add_i32 s4, s2, s4
	s_sub_i32 s14, s14, s2
	v_cmp_eq_u32_sdwa s[2:3], v6, v66 src0_sel:WORD_1 src1_sel:DWORD
	s_nop 1
	v_and_b32_e32 v10, s2, v100
	v_and_b32_e32 v6, s3, v1
	v_bcnt_u32_b32 v10, v10, 0
	v_bcnt_u32_b32 v6, v6, v10
	v_cmp_gt_i32_e32 vcc, s14, v6
	s_and_b64 s[26:27], s[2:3], vcc
	s_and_saveexec_b64 s[8:9], s[26:27]
	s_lshl_b32 s15, s4, 1
	s_add_i32 s15, s52, s15
	v_lshl_add_u32 v6, v6, 1, s15
	ds_write_b16 v6, v232 offset:32768
	s_or_b64 exec, exec, s[8:9]
	s_bcnt1_i32_b64 s2, s[2:3]
	s_min_i32 s2, s2, s14
	s_add_i32 s4, s2, s4
	s_sub_i32 s14, s14, s2
	v_cmp_eq_u32_sdwa s[2:3], v7, v66 src0_sel:WORD_0 src1_sel:DWORD
	s_nop 1
	v_and_b32_e32 v10, s2, v100
	v_and_b32_e32 v6, s3, v1
	v_bcnt_u32_b32 v10, v10, 0
	v_bcnt_u32_b32 v6, v6, v10
	v_cmp_gt_i32_e32 vcc, s14, v6
	s_and_b64 s[26:27], s[2:3], vcc
	s_and_saveexec_b64 s[8:9], s[26:27]
	s_lshl_b32 s15, s4, 1
	s_add_i32 s15, s52, s15
	v_lshl_add_u32 v6, v6, 1, s15
	ds_write_b16 v6, v233 offset:32768
	s_or_b64 exec, exec, s[8:9]
	s_bcnt1_i32_b64 s2, s[2:3]
	s_min_i32 s2, s2, s14
	s_add_i32 s4, s2, s4
	s_sub_i32 s14, s14, s2
	v_cmp_eq_u32_sdwa s[2:3], v7, v66 src0_sel:WORD_1 src1_sel:DWORD
	s_nop 1
	v_and_b32_e32 v7, s2, v100
	v_and_b32_e32 v6, s3, v1
	v_bcnt_u32_b32 v7, v7, 0
	v_bcnt_u32_b32 v6, v6, v7
	v_cmp_gt_i32_e32 vcc, s14, v6
	s_and_b64 s[26:27], s[2:3], vcc
	s_and_saveexec_b64 s[8:9], s[26:27]
	s_lshl_b32 s15, s4, 1
	s_add_i32 s15, s52, s15
	v_lshl_add_u32 v6, v6, 1, s15
	ds_write_b16 v6, v234 offset:32768
	s_or_b64 exec, exec, s[8:9]
	s_bcnt1_i32_b64 s2, s[2:3]
	s_min_i32 s2, s2, s14
	s_add_i32 s4, s2, s4
	s_sub_i32 s14, s14, s2
	v_cmp_eq_u32_sdwa s[2:3], v8, v66 src0_sel:WORD_0 src1_sel:DWORD
	s_nop 1
	v_and_b32_e32 v7, s2, v100
	v_and_b32_e32 v6, s3, v1
	v_bcnt_u32_b32 v7, v7, 0
	v_bcnt_u32_b32 v6, v6, v7
	v_cmp_gt_i32_e32 vcc, s14, v6
	s_and_b64 s[26:27], s[2:3], vcc
	s_and_saveexec_b64 s[8:9], s[26:27]
	s_lshl_b32 s15, s4, 1
	s_add_i32 s15, s52, s15
	v_lshl_add_u32 v6, v6, 1, s15
	ds_write_b16 v6, v235 offset:32768
	s_or_b64 exec, exec, s[8:9]
	s_bcnt1_i32_b64 s2, s[2:3]
	s_min_i32 s2, s2, s14
	s_add_i32 s4, s2, s4
	s_sub_i32 s14, s14, s2
	v_cmp_eq_u32_sdwa s[2:3], v8, v66 src0_sel:WORD_1 src1_sel:DWORD
	s_nop 1
	v_and_b32_e32 v7, s2, v100
	v_and_b32_e32 v6, s3, v1
	v_bcnt_u32_b32 v7, v7, 0
	v_bcnt_u32_b32 v6, v6, v7
	v_cmp_gt_i32_e32 vcc, s14, v6
	s_and_b64 s[26:27], s[2:3], vcc
	s_and_saveexec_b64 s[8:9], s[26:27]
	s_lshl_b32 s15, s4, 1
	s_add_i32 s15, s52, s15
	v_lshl_add_u32 v6, v6, 1, s15
	ds_write_b16 v6, v236 offset:32768
	s_or_b64 exec, exec, s[8:9]
	s_bcnt1_i32_b64 s2, s[2:3]
	s_min_i32 s2, s2, s14
	s_add_i32 s4, s2, s4
	s_sub_i32 s14, s14, s2
	v_cmp_eq_u32_sdwa s[2:3], v9, v66 src0_sel:WORD_0 src1_sel:DWORD
	s_nop 1
	v_and_b32_e32 v7, s2, v100
	v_and_b32_e32 v6, s3, v1
	v_bcnt_u32_b32 v7, v7, 0
	v_bcnt_u32_b32 v6, v6, v7
	v_cmp_gt_i32_e32 vcc, s14, v6
	s_and_b64 s[26:27], s[2:3], vcc
	s_and_saveexec_b64 s[8:9], s[26:27]
	s_lshl_b32 s15, s4, 1
	s_add_i32 s15, s52, s15
	v_lshl_add_u32 v6, v6, 1, s15
	ds_write_b16 v6, v237 offset:32768
	s_or_b64 exec, exec, s[8:9]
	s_bcnt1_i32_b64 s2, s[2:3]
	s_min_i32 s2, s2, s14
	s_add_i32 s4, s2, s4
	s_sub_i32 s14, s14, s2
	v_cmp_eq_u32_sdwa s[2:3], v9, v66 src0_sel:WORD_1 src1_sel:DWORD
	s_nop 1
	v_and_b32_e32 v7, s2, v100
	v_and_b32_e32 v6, s3, v1
	v_bcnt_u32_b32 v7, v7, 0
	v_bcnt_u32_b32 v6, v6, v7
	v_cmp_gt_i32_e32 vcc, s14, v6
	s_and_b64 s[26:27], s[2:3], vcc
	s_and_saveexec_b64 s[8:9], s[26:27]
	s_lshl_b32 s15, s4, 1
	s_add_i32 s15, s52, s15
	v_lshl_add_u32 v6, v6, 1, s15
	ds_write_b16 v6, v238 offset:32768
	s_or_b64 exec, exec, s[8:9]
	s_bcnt1_i32_b64 s2, s[2:3]
	s_min_i32 s2, s2, s14
	s_add_i32 s4, s2, s4
	s_sub_i32 s14, s14, s2
.LBB0_1832:
	s_cmp_gt_i32 s14, 0
	s_cselect_b64 s[2:3], -1, 0
	s_and_b64 s[2:3], s[30:31], s[2:3]
	s_andn2_b64 vcc, exec, s[2:3]
	s_cbranch_vccnz .LBB0_1851
	v_xor_b32_e32 v6, v67, v2
	v_bitop3_b32 v7, v67, s51, v2 bitop3:0x48
	v_cmp_eq_u32_e32 vcc, 0, v7
	v_cmp_gt_u32_e64 s[8:9], s49, v6
	v_xor_b32_e32 v6, v67, v3
	v_bitop3_b32 v7, v67, s51, v3 bitop3:0x48
	s_or_b64 s[2:3], s[8:9], vcc
	v_cmp_eq_u32_e32 vcc, 0, v7
	v_cmp_gt_u32_e64 s[8:9], s49, v6
	s_or_b64 s[8:9], s[8:9], vcc
	v_xor_b32_e32 v6, v67, v4
	v_bitop3_b32 v7, v67, s51, v4 bitop3:0x48
	s_or_b64 s[2:3], s[2:3], s[8:9]
	v_cmp_eq_u32_e32 vcc, 0, v7
	v_cmp_gt_u32_e64 s[8:9], s49, v6
	s_or_b64 s[8:9], s[8:9], vcc
	v_xor_b32_e32 v6, v67, v5
	v_bitop3_b32 v7, v67, s51, v5 bitop3:0x48
	s_or_b64 s[2:3], s[8:9], s[2:3]
	v_cmp_eq_u32_e32 vcc, 0, v7
	v_cmp_gt_u32_e64 s[8:9], s49, v6
	s_or_b64 s[8:9], s[8:9], vcc
	s_or_b64 vcc, s[8:9], s[2:3]
	s_cbranch_vccz .LBB0_1851
	v_cmp_eq_u32_sdwa s[2:3], v2, v66 src0_sel:WORD_0 src1_sel:DWORD
	s_nop 1
	v_and_b32_e32 v7, s2, v100
	v_and_b32_e32 v6, s3, v1
	v_bcnt_u32_b32 v7, v7, 0
	v_bcnt_u32_b32 v6, v6, v7
	v_cmp_gt_u32_e32 vcc, s14, v6
	s_and_b64 s[26:27], s[2:3], vcc
	s_and_saveexec_b64 s[8:9], s[26:27]
	s_lshl_b32 s15, s4, 1
	s_add_i32 s15, s52, s15
	v_lshl_add_u32 v6, v6, 1, s15
	ds_write_b16 v6, v239 offset:32768
	s_or_b64 exec, exec, s[8:9]
	s_bcnt1_i32_b64 s2, s[2:3]
	s_min_u32 s2, s2, s14
	s_add_i32 s4, s2, s4
	s_sub_i32 s14, s14, s2
	v_cmp_eq_u32_sdwa s[2:3], v2, v66 src0_sel:WORD_1 src1_sel:DWORD
	s_nop 1
	v_and_b32_e32 v6, s2, v100
	v_and_b32_e32 v2, s3, v1
	v_bcnt_u32_b32 v6, v6, 0
	v_bcnt_u32_b32 v2, v2, v6
	v_cmp_gt_i32_e32 vcc, s14, v2
	s_and_b64 s[26:27], s[2:3], vcc
	s_and_saveexec_b64 s[8:9], s[26:27]
	s_lshl_b32 s15, s4, 1
	s_add_i32 s15, s52, s15
	v_lshl_add_u32 v2, v2, 1, s15
	ds_write_b16 v2, v240 offset:32768
	s_or_b64 exec, exec, s[8:9]
	s_bcnt1_i32_b64 s2, s[2:3]
	s_min_i32 s2, s2, s14
	s_add_i32 s4, s2, s4
	s_sub_i32 s14, s14, s2
	v_cmp_eq_u32_sdwa s[2:3], v3, v66 src0_sel:WORD_0 src1_sel:DWORD
	s_nop 1
	v_and_b32_e32 v6, s2, v100
	v_and_b32_e32 v2, s3, v1
	v_bcnt_u32_b32 v6, v6, 0
	v_bcnt_u32_b32 v2, v2, v6
	v_cmp_gt_i32_e32 vcc, s14, v2
	s_and_b64 s[26:27], s[2:3], vcc
	s_and_saveexec_b64 s[8:9], s[26:27]
	s_lshl_b32 s15, s4, 1
	s_add_i32 s15, s52, s15
	v_lshl_add_u32 v2, v2, 1, s15
	ds_write_b16 v2, v241 offset:32768
	s_or_b64 exec, exec, s[8:9]
	s_bcnt1_i32_b64 s2, s[2:3]
	s_min_i32 s2, s2, s14
	s_add_i32 s4, s2, s4
	s_sub_i32 s14, s14, s2
	v_cmp_eq_u32_sdwa s[2:3], v3, v66 src0_sel:WORD_1 src1_sel:DWORD
	s_nop 1
	v_and_b32_e32 v3, s2, v100
	v_and_b32_e32 v2, s3, v1
	v_bcnt_u32_b32 v3, v3, 0
	v_bcnt_u32_b32 v2, v2, v3
	v_cmp_gt_i32_e32 vcc, s14, v2
	s_and_b64 s[26:27], s[2:3], vcc
	s_and_saveexec_b64 s[8:9], s[26:27]
	s_lshl_b32 s15, s4, 1
	s_add_i32 s15, s52, s15
	v_lshl_add_u32 v2, v2, 1, s15
	ds_write_b16 v2, v242 offset:32768
	s_or_b64 exec, exec, s[8:9]
	s_bcnt1_i32_b64 s2, s[2:3]
	s_min_i32 s2, s2, s14
	s_add_i32 s4, s2, s4
	s_sub_i32 s14, s14, s2
	v_cmp_eq_u32_sdwa s[2:3], v4, v66 src0_sel:WORD_0 src1_sel:DWORD
	s_nop 1
	v_and_b32_e32 v3, s2, v100
	v_and_b32_e32 v2, s3, v1
	v_bcnt_u32_b32 v3, v3, 0
	v_bcnt_u32_b32 v2, v2, v3
	v_cmp_gt_i32_e32 vcc, s14, v2
	s_and_b64 s[26:27], s[2:3], vcc
	s_and_saveexec_b64 s[8:9], s[26:27]
	s_lshl_b32 s15, s4, 1
	s_add_i32 s15, s52, s15
	v_lshl_add_u32 v2, v2, 1, s15
	ds_write_b16 v2, v243 offset:32768
	s_or_b64 exec, exec, s[8:9]
	s_bcnt1_i32_b64 s2, s[2:3]
	s_min_i32 s2, s2, s14
	s_add_i32 s4, s2, s4
	s_sub_i32 s14, s14, s2
	v_cmp_eq_u32_sdwa s[2:3], v4, v66 src0_sel:WORD_1 src1_sel:DWORD
	s_nop 1
	v_and_b32_e32 v3, s2, v100
	v_and_b32_e32 v2, s3, v1
	v_bcnt_u32_b32 v3, v3, 0
	v_bcnt_u32_b32 v2, v2, v3
	v_cmp_gt_i32_e32 vcc, s14, v2
	s_and_b64 s[26:27], s[2:3], vcc
	s_and_saveexec_b64 s[8:9], s[26:27]
	s_lshl_b32 s15, s4, 1
	s_add_i32 s15, s52, s15
	v_lshl_add_u32 v2, v2, 1, s15
	ds_write_b16 v2, v244 offset:32768
	s_or_b64 exec, exec, s[8:9]
	s_bcnt1_i32_b64 s2, s[2:3]
	s_min_i32 s2, s2, s14
	s_add_i32 s4, s2, s4
	s_sub_i32 s14, s14, s2
	v_cmp_eq_u32_sdwa s[2:3], v5, v66 src0_sel:WORD_0 src1_sel:DWORD
	s_nop 1
	v_and_b32_e32 v3, s2, v100
	v_and_b32_e32 v2, s3, v1
	v_bcnt_u32_b32 v3, v3, 0
	v_bcnt_u32_b32 v2, v2, v3
	v_cmp_gt_i32_e32 vcc, s14, v2
	s_and_b64 s[26:27], s[2:3], vcc
	s_and_saveexec_b64 s[8:9], s[26:27]
	s_lshl_b32 s15, s4, 1
	s_add_i32 s15, s52, s15
	v_lshl_add_u32 v2, v2, 1, s15
	ds_write_b16 v2, v245 offset:32768
	s_or_b64 exec, exec, s[8:9]
	s_bcnt1_i32_b64 s2, s[2:3]
	s_min_i32 s8, s2, s14
	v_cmp_eq_u32_sdwa s[2:3], v5, v66 src0_sel:WORD_1 src1_sel:DWORD
	s_sub_i32 s9, s14, s8
	s_nop 0
	v_and_b32_e32 v3, s2, v100
	v_and_b32_e32 v2, s3, v1
	v_bcnt_u32_b32 v3, v3, 0
	v_bcnt_u32_b32 v2, v2, v3
	v_cmp_gt_i32_e32 vcc, s9, v2
	s_and_b64 s[14:15], s[2:3], vcc
	s_and_saveexec_b64 s[2:3], s[14:15]
	s_cbranch_execz .LBB0_1850
	s_lshl_b32 s8, s8, 1
	s_add_i32 s8, s52, s8
	s_lshl_b32 s4, s4, 1
	s_add_i32 s8, s8, s4
	v_lshl_add_u32 v2, v2, 1, s8
	ds_write_b16 v2, v246 offset:32768
